# GEMM K-loops: mid-cluster s_setprio 0/1 flip pairs removed (outer raise/lower kept), on top of v143
# speedup vs baseline: 1.0053x; 1.0017x over previous
.LBB0_143:
	ds_read_b128 v[148:151], v142
	ds_read_b128 v[152:155], v142 offset:1024
	ds_read_b128 v[156:159], v142 offset:2048
	ds_read_b128 v[160:163], v142 offset:3072
	ds_read_b128 v[164:167], v143
	ds_read_b128 v[174:177], v143 offset:1024
	ds_read_b128 v[178:181], v143 offset:2048
	ds_read_b128 v[182:185], v143 offset:3072
	s_add_u32 s40, s22, 0x100
	s_addc_u32 s41, s23, 0
	s_cmp_eq_u32 s82, 12
	s_cselect_b32 s58, s33, s40
	s_cselect_b32 s59, s13, s41
	s_cselect_b32 s56, s79, s80
	s_cselect_b32 s57, s15, s81
	s_add_u32 s54, s58, 0x80
	s_addc_u32 s55, s59, 0
	ds_read_b128 v[186:189], v144
	ds_read_b128 v[190:193], v144 offset:1024
	ds_read_b128 v[194:197], v144 offset:2048
	ds_read_b128 v[198:201], v144 offset:3072
	ds_read_b128 v[202:205], v144 offset:4096
	ds_read_b128 v[206:209], v144 offset:5120
	ds_read_b128 v[210:213], v144 offset:6144
	ds_read_b128 v[214:217], v144 offset:7168
	s_add_u32 s22, s22, 0x40080
	s_addc_u32 s23, s23, 0
	s_mov_b32 s83, m0
	s_mov_b32 m0, s67
	s_nop 2
	global_load_lds_dwordx4 v136, s[22:23]
	s_mov_b32 m0, s83
	s_nop 0
	s_mov_b32 s83, m0
	s_mov_b32 m0, s76
	s_nop 2
	global_load_lds_dwordx4 v138, s[22:23]
	s_mov_b32 m0, s83
	s_waitcnt vmcnt(8)
	s_waitcnt lgkmcnt(0)
	s_barrier
	s_setprio 1
	v_mfma_f32_16x16x32_bf16 v[126:129], v[148:151], v[186:189], v[126:129]
	v_mfma_f32_16x16x32_bf16 v[122:125], v[156:159], v[186:189], v[122:125]
	v_mfma_f32_16x16x32_bf16 v[110:113], v[148:151], v[194:197], v[110:113]
	v_mfma_f32_16x16x32_bf16 v[106:109], v[156:159], v[194:197], v[106:109]
	v_mfma_f32_16x16x32_bf16 v[94:97], v[148:151], v[202:205], v[94:97]
	v_mfma_f32_16x16x32_bf16 v[90:93], v[156:159], v[202:205], v[90:93]
	v_mfma_f32_16x16x32_bf16 v[78:81], v[148:151], v[210:213], v[78:81]
	v_mfma_f32_16x16x32_bf16 v[74:77], v[156:159], v[210:213], v[74:77]
	v_mfma_f32_16x16x32_bf16 v[126:129], v[152:155], v[190:193], v[126:129]
	v_mfma_f32_16x16x32_bf16 v[122:125], v[160:163], v[190:193], v[122:125]
	v_mfma_f32_16x16x32_bf16 v[110:113], v[152:155], v[198:201], v[110:113]
	v_mfma_f32_16x16x32_bf16 v[106:109], v[160:163], v[198:201], v[106:109]
	v_mfma_f32_16x16x32_bf16 v[94:97], v[152:155], v[206:209], v[94:97]
	v_mfma_f32_16x16x32_bf16 v[90:93], v[160:163], v[206:209], v[90:93]
	v_mfma_f32_16x16x32_bf16 v[78:81], v[152:155], v[214:217], v[78:81]
	v_mfma_f32_16x16x32_bf16 v[74:77], v[160:163], v[214:217], v[74:77]
	v_mfma_f32_16x16x32_bf16 v[118:121], v[164:167], v[186:189], v[118:121]
	v_mfma_f32_16x16x32_bf16 v[114:117], v[178:181], v[186:189], v[114:117]
	v_mfma_f32_16x16x32_bf16 v[102:105], v[164:167], v[194:197], v[102:105]
	v_mfma_f32_16x16x32_bf16 v[98:101], v[178:181], v[194:197], v[98:101]
	v_mfma_f32_16x16x32_bf16 v[86:89], v[164:167], v[202:205], v[86:89]
	v_mfma_f32_16x16x32_bf16 v[82:85], v[178:181], v[202:205], v[82:85]
	v_mfma_f32_16x16x32_bf16 v[70:73], v[164:167], v[210:213], v[70:73]
	v_mfma_f32_16x16x32_bf16 v[66:69], v[178:181], v[210:213], v[66:69]
	v_mfma_f32_16x16x32_bf16 v[118:121], v[174:177], v[190:193], v[118:121]
	v_mfma_f32_16x16x32_bf16 v[114:117], v[182:185], v[190:193], v[114:117]
	v_mfma_f32_16x16x32_bf16 v[102:105], v[174:177], v[198:201], v[102:105]
	v_mfma_f32_16x16x32_bf16 v[98:101], v[182:185], v[198:201], v[98:101]
	v_mfma_f32_16x16x32_bf16 v[86:89], v[174:177], v[206:209], v[86:89]
	v_mfma_f32_16x16x32_bf16 v[82:85], v[182:185], v[206:209], v[82:85]
	v_mfma_f32_16x16x32_bf16 v[70:73], v[174:177], v[214:217], v[70:73]
	v_mfma_f32_16x16x32_bf16 v[66:69], v[182:185], v[214:217], v[66:69]
	s_setprio 0
	s_barrier
	ds_read_b128 v[186:189], v144 offset:16384
	ds_read_b128 v[190:193], v144 offset:17408
	ds_read_b128 v[194:197], v144 offset:18432
	ds_read_b128 v[198:201], v144 offset:19456
	ds_read_b128 v[202:205], v144 offset:20480
	ds_read_b128 v[206:209], v144 offset:21504
	ds_read_b128 v[210:213], v144 offset:22528
	ds_read_b128 v[214:217], v144 offset:23552
	s_mov_b32 s22, m0
	s_mov_b32 m0, s30
	s_nop 2
	global_load_lds_dwordx4 v137, s[56:57]
	s_mov_b32 m0, s22
	s_nop 0
	s_mov_b32 s22, m0
	s_mov_b32 m0, s31
	s_nop 2
	global_load_lds_dwordx4 v139, s[56:57]
	s_mov_b32 m0, s22
	s_add_u32 s22, s56, 0x40000
	s_addc_u32 s23, s57, 0
	s_mov_b32 s83, m0
	s_mov_b32 m0, s34
	s_nop 2
	global_load_lds_dwordx4 v137, s[22:23]
	s_mov_b32 m0, s83
	s_nop 0
	s_mov_b32 s83, m0
	s_mov_b32 m0, s35
	s_nop 2
	global_load_lds_dwordx4 v139, s[22:23]
	s_mov_b32 m0, s83
	s_mov_b32 s22, m0
	s_mov_b32 m0, s21
	s_nop 2
	global_load_lds_dwordx4 v136, s[58:59]
	s_mov_b32 m0, s22
	s_nop 0
	s_mov_b32 s22, m0
	s_mov_b32 m0, s36
	s_nop 2
	global_load_lds_dwordx4 v138, s[58:59]
	s_mov_b32 m0, s22
	s_waitcnt vmcnt(8)
	s_waitcnt lgkmcnt(0)
	s_barrier
	s_setprio 1
	v_mfma_f32_16x16x32_bf16 v[62:65], v[148:151], v[186:189], v[62:65]
	v_mfma_f32_16x16x32_bf16 v[58:61], v[156:159], v[186:189], v[58:61]
	v_mfma_f32_16x16x32_bf16 v[46:49], v[148:151], v[194:197], v[46:49]
	v_mfma_f32_16x16x32_bf16 v[42:45], v[156:159], v[194:197], v[42:45]
	v_mfma_f32_16x16x32_bf16 v[30:33], v[148:151], v[202:205], v[30:33]
	v_mfma_f32_16x16x32_bf16 v[26:29], v[156:159], v[202:205], v[26:29]
	v_mfma_f32_16x16x32_bf16 v[14:17], v[148:151], v[210:213], v[14:17]
	v_mfma_f32_16x16x32_bf16 v[10:13], v[156:159], v[210:213], v[10:13]
	v_mfma_f32_16x16x32_bf16 v[62:65], v[152:155], v[190:193], v[62:65]
	v_mfma_f32_16x16x32_bf16 v[58:61], v[160:163], v[190:193], v[58:61]
	v_mfma_f32_16x16x32_bf16 v[46:49], v[152:155], v[198:201], v[46:49]
	v_mfma_f32_16x16x32_bf16 v[42:45], v[160:163], v[198:201], v[42:45]
	v_mfma_f32_16x16x32_bf16 v[30:33], v[152:155], v[206:209], v[30:33]
	v_mfma_f32_16x16x32_bf16 v[26:29], v[160:163], v[206:209], v[26:29]
	v_mfma_f32_16x16x32_bf16 v[14:17], v[152:155], v[214:217], v[14:17]
	v_mfma_f32_16x16x32_bf16 v[10:13], v[160:163], v[214:217], v[10:13]
	v_mfma_f32_16x16x32_bf16 v[54:57], v[164:167], v[186:189], v[54:57]
	v_mfma_f32_16x16x32_bf16 v[50:53], v[178:181], v[186:189], v[50:53]
	v_mfma_f32_16x16x32_bf16 v[38:41], v[164:167], v[194:197], v[38:41]
	v_mfma_f32_16x16x32_bf16 v[34:37], v[178:181], v[194:197], v[34:37]
	v_mfma_f32_16x16x32_bf16 v[22:25], v[164:167], v[202:205], v[22:25]
	v_mfma_f32_16x16x32_bf16 v[18:21], v[178:181], v[202:205], v[18:21]
	v_mfma_f32_16x16x32_bf16 v[6:9], v[164:167], v[210:213], v[6:9]
	v_mfma_f32_16x16x32_bf16 v[2:5], v[178:181], v[210:213], v[2:5]
	v_mfma_f32_16x16x32_bf16 v[54:57], v[174:177], v[190:193], v[54:57]
	v_mfma_f32_16x16x32_bf16 v[50:53], v[182:185], v[190:193], v[50:53]
	v_mfma_f32_16x16x32_bf16 v[38:41], v[174:177], v[198:201], v[38:41]
	v_mfma_f32_16x16x32_bf16 v[34:37], v[182:185], v[198:201], v[34:37]
	v_mfma_f32_16x16x32_bf16 v[22:25], v[174:177], v[206:209], v[22:25]
	v_mfma_f32_16x16x32_bf16 v[18:21], v[182:185], v[206:209], v[18:21]
	v_mfma_f32_16x16x32_bf16 v[6:9], v[174:177], v[214:217], v[6:9]
	v_mfma_f32_16x16x32_bf16 v[2:5], v[182:185], v[214:217], v[2:5]
	s_setprio 0
	s_barrier
	ds_read_b128 v[148:151], v145
	ds_read_b128 v[152:155], v145 offset:1024
	ds_read_b128 v[156:159], v145 offset:2048
	ds_read_b128 v[160:163], v145 offset:3072
	ds_read_b128 v[164:167], v146
	ds_read_b128 v[174:177], v146 offset:1024
	ds_read_b128 v[178:181], v146 offset:2048
	ds_read_b128 v[182:185], v146 offset:3072
	ds_read_b128 v[186:189], v144 offset:32768
	ds_read_b128 v[190:193], v144 offset:33792
	ds_read_b128 v[194:197], v144 offset:34816
	ds_read_b128 v[198:201], v144 offset:35840
	ds_read_b128 v[202:205], v144 offset:36864
	ds_read_b128 v[206:209], v144 offset:37888
	ds_read_b128 v[210:213], v144 offset:38912
	ds_read_b128 v[214:217], v144 offset:39936
	s_add_u32 s22, s58, 0x40000
	s_addc_u32 s23, s59, 0
	s_mov_b32 s58, m0
	s_mov_b32 m0, s37
	s_nop 2
	global_load_lds_dwordx4 v136, s[22:23]
	s_mov_b32 m0, s58
	s_nop 0
	s_mov_b32 s58, m0
	s_mov_b32 m0, s52
	s_nop 2
	global_load_lds_dwordx4 v138, s[22:23]
	s_mov_b32 m0, s58
	s_waitcnt vmcnt(8)
	s_waitcnt lgkmcnt(0)
	s_barrier
	s_setprio 1
	v_mfma_f32_16x16x32_bf16 v[126:129], v[148:151], v[186:189], v[126:129]
	v_mfma_f32_16x16x32_bf16 v[122:125], v[156:159], v[186:189], v[122:125]
	v_mfma_f32_16x16x32_bf16 v[110:113], v[148:151], v[194:197], v[110:113]
	v_mfma_f32_16x16x32_bf16 v[106:109], v[156:159], v[194:197], v[106:109]
	v_mfma_f32_16x16x32_bf16 v[94:97], v[148:151], v[202:205], v[94:97]
	v_mfma_f32_16x16x32_bf16 v[90:93], v[156:159], v[202:205], v[90:93]
	v_mfma_f32_16x16x32_bf16 v[78:81], v[148:151], v[210:213], v[78:81]
	v_mfma_f32_16x16x32_bf16 v[74:77], v[156:159], v[210:213], v[74:77]
	v_mfma_f32_16x16x32_bf16 v[126:129], v[152:155], v[190:193], v[126:129]
	v_mfma_f32_16x16x32_bf16 v[122:125], v[160:163], v[190:193], v[122:125]
	v_mfma_f32_16x16x32_bf16 v[110:113], v[152:155], v[198:201], v[110:113]
	v_mfma_f32_16x16x32_bf16 v[106:109], v[160:163], v[198:201], v[106:109]
	v_mfma_f32_16x16x32_bf16 v[94:97], v[152:155], v[206:209], v[94:97]
	v_mfma_f32_16x16x32_bf16 v[90:93], v[160:163], v[206:209], v[90:93]
	v_mfma_f32_16x16x32_bf16 v[78:81], v[152:155], v[214:217], v[78:81]
	v_mfma_f32_16x16x32_bf16 v[74:77], v[160:163], v[214:217], v[74:77]
	v_mfma_f32_16x16x32_bf16 v[118:121], v[164:167], v[186:189], v[118:121]
	v_mfma_f32_16x16x32_bf16 v[114:117], v[178:181], v[186:189], v[114:117]
	v_mfma_f32_16x16x32_bf16 v[102:105], v[164:167], v[194:197], v[102:105]
	v_mfma_f32_16x16x32_bf16 v[98:101], v[178:181], v[194:197], v[98:101]
	v_mfma_f32_16x16x32_bf16 v[86:89], v[164:167], v[202:205], v[86:89]
	v_mfma_f32_16x16x32_bf16 v[82:85], v[178:181], v[202:205], v[82:85]
	v_mfma_f32_16x16x32_bf16 v[70:73], v[164:167], v[210:213], v[70:73]
	v_mfma_f32_16x16x32_bf16 v[66:69], v[178:181], v[210:213], v[66:69]
	v_mfma_f32_16x16x32_bf16 v[118:121], v[174:177], v[190:193], v[118:121]
	v_mfma_f32_16x16x32_bf16 v[114:117], v[182:185], v[190:193], v[114:117]
	v_mfma_f32_16x16x32_bf16 v[102:105], v[174:177], v[198:201], v[102:105]
	v_mfma_f32_16x16x32_bf16 v[98:101], v[182:185], v[198:201], v[98:101]
	v_mfma_f32_16x16x32_bf16 v[86:89], v[174:177], v[206:209], v[86:89]
	v_mfma_f32_16x16x32_bf16 v[82:85], v[182:185], v[206:209], v[82:85]
	v_mfma_f32_16x16x32_bf16 v[70:73], v[174:177], v[214:217], v[70:73]
	v_mfma_f32_16x16x32_bf16 v[66:69], v[182:185], v[214:217], v[66:69]
	s_setprio 0
	s_barrier
	ds_read_b128 v[186:189], v144 offset:49152
	ds_read_b128 v[190:193], v144 offset:50176
	ds_read_b128 v[194:197], v144 offset:51200
	ds_read_b128 v[198:201], v144 offset:52224
	ds_read_b128 v[202:205], v144 offset:53248
	ds_read_b128 v[206:209], v144 offset:54272
	ds_read_b128 v[210:213], v144 offset:55296
	ds_read_b128 v[214:217], v144 offset:56320
	s_add_u32 s22, s56, 0x80
	s_addc_u32 s23, s57, 0
	s_mov_b32 s58, m0
	s_mov_b32 m0, s61
	s_nop 2
	global_load_lds_dwordx4 v137, s[22:23]
	s_mov_b32 m0, s58
	s_nop 0
	s_mov_b32 s58, m0
	s_mov_b32 m0, s62
	s_nop 2
	global_load_lds_dwordx4 v139, s[22:23]
	s_mov_b32 m0, s58
	s_add_u32 s22, s56, 0x40080
	s_addc_u32 s23, s57, 0
	s_mov_b32 s56, m0
	s_mov_b32 m0, s65
	s_nop 2
	global_load_lds_dwordx4 v137, s[22:23]
	s_mov_b32 m0, s56
	s_nop 0
	s_mov_b32 s56, m0
	s_mov_b32 m0, s66
	s_nop 2
	global_load_lds_dwordx4 v139, s[22:23]
	s_mov_b32 m0, s56
	s_mov_b32 s22, m0
	s_mov_b32 m0, s63
	s_nop 2
	global_load_lds_dwordx4 v136, s[54:55]
	s_mov_b32 m0, s22
	s_nop 0
	s_mov_b32 s22, m0
	s_mov_b32 m0, s64
	s_nop 2
	global_load_lds_dwordx4 v138, s[54:55]
	s_mov_b32 m0, s22
	s_waitcnt vmcnt(8)
	s_waitcnt lgkmcnt(0)
	s_barrier
	s_setprio 1
	v_mfma_f32_16x16x32_bf16 v[62:65], v[148:151], v[186:189], v[62:65]
	v_mfma_f32_16x16x32_bf16 v[58:61], v[156:159], v[186:189], v[58:61]
	v_mfma_f32_16x16x32_bf16 v[46:49], v[148:151], v[194:197], v[46:49]
	v_mfma_f32_16x16x32_bf16 v[42:45], v[156:159], v[194:197], v[42:45]
	v_mfma_f32_16x16x32_bf16 v[30:33], v[148:151], v[202:205], v[30:33]
	v_mfma_f32_16x16x32_bf16 v[26:29], v[156:159], v[202:205], v[26:29]
	v_mfma_f32_16x16x32_bf16 v[14:17], v[148:151], v[210:213], v[14:17]
	v_mfma_f32_16x16x32_bf16 v[10:13], v[156:159], v[210:213], v[10:13]
	v_mfma_f32_16x16x32_bf16 v[62:65], v[152:155], v[190:193], v[62:65]
	v_mfma_f32_16x16x32_bf16 v[58:61], v[160:163], v[190:193], v[58:61]
	v_mfma_f32_16x16x32_bf16 v[46:49], v[152:155], v[198:201], v[46:49]
	v_mfma_f32_16x16x32_bf16 v[42:45], v[160:163], v[198:201], v[42:45]
	v_mfma_f32_16x16x32_bf16 v[30:33], v[152:155], v[206:209], v[30:33]
	v_mfma_f32_16x16x32_bf16 v[26:29], v[160:163], v[206:209], v[26:29]
	v_mfma_f32_16x16x32_bf16 v[14:17], v[152:155], v[214:217], v[14:17]
	v_mfma_f32_16x16x32_bf16 v[10:13], v[160:163], v[214:217], v[10:13]
	v_mfma_f32_16x16x32_bf16 v[54:57], v[164:167], v[186:189], v[54:57]
	v_mfma_f32_16x16x32_bf16 v[50:53], v[178:181], v[186:189], v[50:53]
	v_mfma_f32_16x16x32_bf16 v[38:41], v[164:167], v[194:197], v[38:41]
	v_mfma_f32_16x16x32_bf16 v[34:37], v[178:181], v[194:197], v[34:37]
	v_mfma_f32_16x16x32_bf16 v[22:25], v[164:167], v[202:205], v[22:25]
	v_mfma_f32_16x16x32_bf16 v[18:21], v[178:181], v[202:205], v[18:21]
	v_mfma_f32_16x16x32_bf16 v[6:9], v[164:167], v[210:213], v[6:9]
	v_mfma_f32_16x16x32_bf16 v[2:5], v[178:181], v[210:213], v[2:5]
	v_mfma_f32_16x16x32_bf16 v[54:57], v[174:177], v[190:193], v[54:57]
	v_mfma_f32_16x16x32_bf16 v[50:53], v[182:185], v[190:193], v[50:53]
	v_mfma_f32_16x16x32_bf16 v[38:41], v[174:177], v[198:201], v[38:41]
	v_mfma_f32_16x16x32_bf16 v[34:37], v[182:185], v[198:201], v[34:37]
	v_mfma_f32_16x16x32_bf16 v[22:25], v[174:177], v[206:209], v[22:25]
	v_mfma_f32_16x16x32_bf16 v[18:21], v[182:185], v[206:209], v[18:21]
	v_mfma_f32_16x16x32_bf16 v[6:9], v[174:177], v[214:217], v[6:9]
	v_mfma_f32_16x16x32_bf16 v[2:5], v[182:185], v[214:217], v[2:5]
	s_setprio 0
	s_barrier
	s_add_i32 s82, s82, 2
	s_add_u32 s80, s80, 0x100
	s_addc_u32 s81, s81, 0
	s_cmp_gt_u32 s82, 13
	s_mov_b64 s[22:23], s[40:41]
	s_cbranch_scc0 .LBB0_143
	s_and_b64 vcc, exec, s[10:11]
	s_cbranch_vccz .LBB0_146
	s_barrier

.Lpeel170:
	ds_read_b128 v[142:145], v136
	ds_read_b128 v[146:149], v136 offset:1024
	ds_read_b128 v[150:153], v136 offset:2048
	ds_read_b128 v[154:157], v136 offset:3072
	ds_read_b128 v[158:161], v137
	ds_read_b128 v[162:165], v137 offset:1024
	ds_read_b128 v[166:169], v137 offset:2048
	ds_read_b128 v[174:177], v137 offset:3072
	s_add_u32 s14, s12, 0x100
	s_addc_u32 s15, s13, 0
	s_cmp_eq_u32 s56, 12
	s_cselect_b32 s20, s10, s14
	s_cselect_b32 s21, s11, s15
	s_cselect_b32 s18, s8, s54
	s_cselect_b32 s19, s9, s55
	s_add_u32 s16, s20, 0x80
	s_addc_u32 s17, s21, 0
	ds_read_b128 v[178:181], v138
	ds_read_b128 v[182:185], v138 offset:1024
	ds_read_b128 v[186:189], v138 offset:2048
	ds_read_b128 v[190:193], v138 offset:3072
	ds_read_b128 v[194:197], v138 offset:4096
	ds_read_b128 v[198:201], v138 offset:5120
	ds_read_b128 v[202:205], v138 offset:6144
	ds_read_b128 v[206:209], v138 offset:7168
	s_add_u32 s12, s12, 0x40080
	s_addc_u32 s13, s13, 0
	s_mov_b32 s57, m0
	s_mov_b32 m0, s52
	s_nop 2
	global_load_lds_dwordx4 v132, s[12:13]
	s_mov_b32 m0, s57
	s_nop 0
	s_mov_b32 s57, m0
	s_mov_b32 m0, s53
	s_nop 2
	global_load_lds_dwordx4 v134, s[12:13]
	s_mov_b32 m0, s57
	s_waitcnt vmcnt(8)
	s_waitcnt lgkmcnt(0)
	s_barrier
	s_setprio 1
	v_mfma_f32_16x16x32_bf16 v[126:129], v[142:145], v[178:181], 0
	v_mfma_f32_16x16x32_bf16 v[122:125], v[150:153], v[178:181], 0
	v_mfma_f32_16x16x32_bf16 v[110:113], v[142:145], v[186:189], 0
	v_mfma_f32_16x16x32_bf16 v[106:109], v[150:153], v[186:189], 0
	v_mfma_f32_16x16x32_bf16 v[94:97], v[142:145], v[194:197], 0
	v_mfma_f32_16x16x32_bf16 v[90:93], v[150:153], v[194:197], 0
	v_mfma_f32_16x16x32_bf16 v[78:81], v[142:145], v[202:205], 0
	v_mfma_f32_16x16x32_bf16 v[74:77], v[150:153], v[202:205], 0
	v_mfma_f32_16x16x32_bf16 v[126:129], v[146:149], v[182:185], v[126:129]
	v_mfma_f32_16x16x32_bf16 v[122:125], v[154:157], v[182:185], v[122:125]
	v_mfma_f32_16x16x32_bf16 v[110:113], v[146:149], v[190:193], v[110:113]
	v_mfma_f32_16x16x32_bf16 v[106:109], v[154:157], v[190:193], v[106:109]
	v_mfma_f32_16x16x32_bf16 v[94:97], v[146:149], v[198:201], v[94:97]
	v_mfma_f32_16x16x32_bf16 v[90:93], v[154:157], v[198:201], v[90:93]
	v_mfma_f32_16x16x32_bf16 v[78:81], v[146:149], v[206:209], v[78:81]
	v_mfma_f32_16x16x32_bf16 v[74:77], v[154:157], v[206:209], v[74:77]
	v_mfma_f32_16x16x32_bf16 v[118:121], v[158:161], v[178:181], 0
	v_mfma_f32_16x16x32_bf16 v[114:117], v[166:169], v[178:181], 0
	v_mfma_f32_16x16x32_bf16 v[102:105], v[158:161], v[186:189], 0
	v_mfma_f32_16x16x32_bf16 v[98:101], v[166:169], v[186:189], 0
	v_mfma_f32_16x16x32_bf16 v[86:89], v[158:161], v[194:197], 0
	v_mfma_f32_16x16x32_bf16 v[82:85], v[166:169], v[194:197], 0
	v_mfma_f32_16x16x32_bf16 v[70:73], v[158:161], v[202:205], 0
	v_mfma_f32_16x16x32_bf16 v[66:69], v[166:169], v[202:205], 0
	v_mfma_f32_16x16x32_bf16 v[118:121], v[162:165], v[182:185], v[118:121]
	v_mfma_f32_16x16x32_bf16 v[114:117], v[174:177], v[182:185], v[114:117]
	v_mfma_f32_16x16x32_bf16 v[102:105], v[162:165], v[190:193], v[102:105]
	v_mfma_f32_16x16x32_bf16 v[98:101], v[174:177], v[190:193], v[98:101]
	v_mfma_f32_16x16x32_bf16 v[86:89], v[162:165], v[198:201], v[86:89]
	v_mfma_f32_16x16x32_bf16 v[82:85], v[174:177], v[198:201], v[82:85]
	v_mfma_f32_16x16x32_bf16 v[70:73], v[162:165], v[206:209], v[70:73]
	v_mfma_f32_16x16x32_bf16 v[66:69], v[174:177], v[206:209], v[66:69]
	s_setprio 0
	s_barrier
	ds_read_b128 v[178:181], v138 offset:16384
	ds_read_b128 v[182:185], v138 offset:17408
	ds_read_b128 v[186:189], v138 offset:18432
	ds_read_b128 v[190:193], v138 offset:19456
	ds_read_b128 v[194:197], v138 offset:20480
	ds_read_b128 v[198:201], v138 offset:21504
	ds_read_b128 v[202:205], v138 offset:22528
	ds_read_b128 v[206:209], v138 offset:23552
	s_mov_b32 s12, m0
	s_mov_b32 m0, s24
	s_nop 2
	global_load_lds_dwordx4 v133, s[18:19]
	s_mov_b32 m0, s12
	s_nop 0
	s_mov_b32 s12, m0
	s_mov_b32 m0, s25
	s_nop 2
	global_load_lds_dwordx4 v135, s[18:19]
	s_mov_b32 m0, s12
	s_add_u32 s12, s18, 0x40000
	s_addc_u32 s13, s19, 0
	s_mov_b32 s57, m0
	s_mov_b32 m0, s28
	s_nop 2
	global_load_lds_dwordx4 v133, s[12:13]
	s_mov_b32 m0, s57
	s_nop 0
	s_mov_b32 s57, m0
	s_mov_b32 m0, s29
	s_nop 2
	global_load_lds_dwordx4 v135, s[12:13]
	s_mov_b32 m0, s57
	s_mov_b32 s12, m0
	s_mov_b32 m0, s5
	s_nop 2
	global_load_lds_dwordx4 v132, s[20:21]
	s_mov_b32 m0, s12
	s_nop 0
	s_mov_b32 s12, m0
	s_mov_b32 m0, s30
	s_nop 2
	global_load_lds_dwordx4 v134, s[20:21]
	s_mov_b32 m0, s12
	s_waitcnt vmcnt(8)
	s_waitcnt lgkmcnt(0)
	s_barrier
	s_setprio 1
	v_mfma_f32_16x16x32_bf16 v[62:65], v[142:145], v[178:181], 0
	v_mfma_f32_16x16x32_bf16 v[58:61], v[150:153], v[178:181], 0
	v_mfma_f32_16x16x32_bf16 v[46:49], v[142:145], v[186:189], 0
	v_mfma_f32_16x16x32_bf16 v[42:45], v[150:153], v[186:189], 0
	v_mfma_f32_16x16x32_bf16 v[30:33], v[142:145], v[194:197], 0
	v_mfma_f32_16x16x32_bf16 v[26:29], v[150:153], v[194:197], 0
	v_mfma_f32_16x16x32_bf16 v[14:17], v[142:145], v[202:205], 0
	v_mfma_f32_16x16x32_bf16 v[10:13], v[150:153], v[202:205], 0
	v_mfma_f32_16x16x32_bf16 v[62:65], v[146:149], v[182:185], v[62:65]
	v_mfma_f32_16x16x32_bf16 v[58:61], v[154:157], v[182:185], v[58:61]
	v_mfma_f32_16x16x32_bf16 v[46:49], v[146:149], v[190:193], v[46:49]
	v_mfma_f32_16x16x32_bf16 v[42:45], v[154:157], v[190:193], v[42:45]
	v_mfma_f32_16x16x32_bf16 v[30:33], v[146:149], v[198:201], v[30:33]
	v_mfma_f32_16x16x32_bf16 v[26:29], v[154:157], v[198:201], v[26:29]
	v_mfma_f32_16x16x32_bf16 v[14:17], v[146:149], v[206:209], v[14:17]
	v_mfma_f32_16x16x32_bf16 v[10:13], v[154:157], v[206:209], v[10:13]
	v_mfma_f32_16x16x32_bf16 v[54:57], v[158:161], v[178:181], 0
	v_mfma_f32_16x16x32_bf16 v[50:53], v[166:169], v[178:181], 0
	v_mfma_f32_16x16x32_bf16 v[38:41], v[158:161], v[186:189], 0
	v_mfma_f32_16x16x32_bf16 v[34:37], v[166:169], v[186:189], 0
	v_mfma_f32_16x16x32_bf16 v[22:25], v[158:161], v[194:197], 0
	v_mfma_f32_16x16x32_bf16 v[18:21], v[166:169], v[194:197], 0
	v_mfma_f32_16x16x32_bf16 v[6:9], v[158:161], v[202:205], 0
	v_mfma_f32_16x16x32_bf16 v[2:5], v[166:169], v[202:205], 0
	v_mfma_f32_16x16x32_bf16 v[54:57], v[162:165], v[182:185], v[54:57]
	v_mfma_f32_16x16x32_bf16 v[50:53], v[174:177], v[182:185], v[50:53]
	v_mfma_f32_16x16x32_bf16 v[38:41], v[162:165], v[190:193], v[38:41]
	v_mfma_f32_16x16x32_bf16 v[34:37], v[174:177], v[190:193], v[34:37]
	v_mfma_f32_16x16x32_bf16 v[22:25], v[162:165], v[198:201], v[22:25]
	v_mfma_f32_16x16x32_bf16 v[18:21], v[174:177], v[198:201], v[18:21]
	v_mfma_f32_16x16x32_bf16 v[6:9], v[162:165], v[206:209], v[6:9]
	v_mfma_f32_16x16x32_bf16 v[2:5], v[174:177], v[206:209], v[2:5]
	s_setprio 0
	s_barrier
	s_branch .Lmid170
.LBB0_170:
	ds_read_b128 v[142:145], v136
	ds_read_b128 v[146:149], v136 offset:1024
	ds_read_b128 v[150:153], v136 offset:2048
	ds_read_b128 v[154:157], v136 offset:3072
	ds_read_b128 v[158:161], v137
	ds_read_b128 v[162:165], v137 offset:1024
	ds_read_b128 v[166:169], v137 offset:2048
	ds_read_b128 v[174:177], v137 offset:3072
	s_add_u32 s14, s12, 0x100
	s_addc_u32 s15, s13, 0
	s_cmp_eq_u32 s56, 12
	s_cselect_b32 s20, s10, s14
	s_cselect_b32 s21, s11, s15
	s_cselect_b32 s18, s8, s54
	s_cselect_b32 s19, s9, s55
	s_add_u32 s16, s20, 0x80
	s_addc_u32 s17, s21, 0
	ds_read_b128 v[178:181], v138
	ds_read_b128 v[182:185], v138 offset:1024
	ds_read_b128 v[186:189], v138 offset:2048
	ds_read_b128 v[190:193], v138 offset:3072
	ds_read_b128 v[194:197], v138 offset:4096
	ds_read_b128 v[198:201], v138 offset:5120
	ds_read_b128 v[202:205], v138 offset:6144
	ds_read_b128 v[206:209], v138 offset:7168
	s_add_u32 s12, s12, 0x40080
	s_addc_u32 s13, s13, 0
	s_mov_b32 s57, m0
	s_mov_b32 m0, s52
	s_nop 2
	global_load_lds_dwordx4 v132, s[12:13]
	s_mov_b32 m0, s57
	s_nop 0
	s_mov_b32 s57, m0
	s_mov_b32 m0, s53
	s_nop 2
	global_load_lds_dwordx4 v134, s[12:13]
	s_mov_b32 m0, s57
	s_waitcnt vmcnt(8)
	s_waitcnt lgkmcnt(0)
	s_barrier
	s_setprio 1
	v_mfma_f32_16x16x32_bf16 v[126:129], v[142:145], v[178:181], v[126:129]
	v_mfma_f32_16x16x32_bf16 v[122:125], v[150:153], v[178:181], v[122:125]
	v_mfma_f32_16x16x32_bf16 v[110:113], v[142:145], v[186:189], v[110:113]
	v_mfma_f32_16x16x32_bf16 v[106:109], v[150:153], v[186:189], v[106:109]
	v_mfma_f32_16x16x32_bf16 v[94:97], v[142:145], v[194:197], v[94:97]
	v_mfma_f32_16x16x32_bf16 v[90:93], v[150:153], v[194:197], v[90:93]
	v_mfma_f32_16x16x32_bf16 v[78:81], v[142:145], v[202:205], v[78:81]
	v_mfma_f32_16x16x32_bf16 v[74:77], v[150:153], v[202:205], v[74:77]
	v_mfma_f32_16x16x32_bf16 v[126:129], v[146:149], v[182:185], v[126:129]
	v_mfma_f32_16x16x32_bf16 v[122:125], v[154:157], v[182:185], v[122:125]
	v_mfma_f32_16x16x32_bf16 v[110:113], v[146:149], v[190:193], v[110:113]
	v_mfma_f32_16x16x32_bf16 v[106:109], v[154:157], v[190:193], v[106:109]
	v_mfma_f32_16x16x32_bf16 v[94:97], v[146:149], v[198:201], v[94:97]
	v_mfma_f32_16x16x32_bf16 v[90:93], v[154:157], v[198:201], v[90:93]
	v_mfma_f32_16x16x32_bf16 v[78:81], v[146:149], v[206:209], v[78:81]
	v_mfma_f32_16x16x32_bf16 v[74:77], v[154:157], v[206:209], v[74:77]
	v_mfma_f32_16x16x32_bf16 v[118:121], v[158:161], v[178:181], v[118:121]
	v_mfma_f32_16x16x32_bf16 v[114:117], v[166:169], v[178:181], v[114:117]
	v_mfma_f32_16x16x32_bf16 v[102:105], v[158:161], v[186:189], v[102:105]
	v_mfma_f32_16x16x32_bf16 v[98:101], v[166:169], v[186:189], v[98:101]
	v_mfma_f32_16x16x32_bf16 v[86:89], v[158:161], v[194:197], v[86:89]
	v_mfma_f32_16x16x32_bf16 v[82:85], v[166:169], v[194:197], v[82:85]
	v_mfma_f32_16x16x32_bf16 v[70:73], v[158:161], v[202:205], v[70:73]
	v_mfma_f32_16x16x32_bf16 v[66:69], v[166:169], v[202:205], v[66:69]
	v_mfma_f32_16x16x32_bf16 v[118:121], v[162:165], v[182:185], v[118:121]
	v_mfma_f32_16x16x32_bf16 v[114:117], v[174:177], v[182:185], v[114:117]
	v_mfma_f32_16x16x32_bf16 v[102:105], v[162:165], v[190:193], v[102:105]
	v_mfma_f32_16x16x32_bf16 v[98:101], v[174:177], v[190:193], v[98:101]
	v_mfma_f32_16x16x32_bf16 v[86:89], v[162:165], v[198:201], v[86:89]
	v_mfma_f32_16x16x32_bf16 v[82:85], v[174:177], v[198:201], v[82:85]
	v_mfma_f32_16x16x32_bf16 v[70:73], v[162:165], v[206:209], v[70:73]
	v_mfma_f32_16x16x32_bf16 v[66:69], v[174:177], v[206:209], v[66:69]
	s_setprio 0
	s_barrier
	ds_read_b128 v[178:181], v138 offset:16384
	ds_read_b128 v[182:185], v138 offset:17408
	ds_read_b128 v[186:189], v138 offset:18432
	ds_read_b128 v[190:193], v138 offset:19456
	ds_read_b128 v[194:197], v138 offset:20480
	ds_read_b128 v[198:201], v138 offset:21504
	ds_read_b128 v[202:205], v138 offset:22528
	ds_read_b128 v[206:209], v138 offset:23552
	s_mov_b32 s12, m0
	s_mov_b32 m0, s24
	s_nop 2
	global_load_lds_dwordx4 v133, s[18:19]
	s_mov_b32 m0, s12
	s_nop 0
	s_mov_b32 s12, m0
	s_mov_b32 m0, s25
	s_nop 2
	global_load_lds_dwordx4 v135, s[18:19]
	s_mov_b32 m0, s12
	s_add_u32 s12, s18, 0x40000
	s_addc_u32 s13, s19, 0
	s_mov_b32 s57, m0
	s_mov_b32 m0, s28
	s_nop 2
	global_load_lds_dwordx4 v133, s[12:13]
	s_mov_b32 m0, s57
	s_nop 0
	s_mov_b32 s57, m0
	s_mov_b32 m0, s29
	s_nop 2
	global_load_lds_dwordx4 v135, s[12:13]
	s_mov_b32 m0, s57
	s_mov_b32 s12, m0
	s_mov_b32 m0, s5
	s_nop 2
	global_load_lds_dwordx4 v132, s[20:21]
	s_mov_b32 m0, s12
	s_nop 0
	s_mov_b32 s12, m0
	s_mov_b32 m0, s30
	s_nop 2
	global_load_lds_dwordx4 v134, s[20:21]
	s_mov_b32 m0, s12
	s_waitcnt vmcnt(8)
	s_waitcnt lgkmcnt(0)
	s_barrier
	s_setprio 1
	v_mfma_f32_16x16x32_bf16 v[62:65], v[142:145], v[178:181], v[62:65]
	v_mfma_f32_16x16x32_bf16 v[58:61], v[150:153], v[178:181], v[58:61]
	v_mfma_f32_16x16x32_bf16 v[46:49], v[142:145], v[186:189], v[46:49]
	v_mfma_f32_16x16x32_bf16 v[42:45], v[150:153], v[186:189], v[42:45]
	v_mfma_f32_16x16x32_bf16 v[30:33], v[142:145], v[194:197], v[30:33]
	v_mfma_f32_16x16x32_bf16 v[26:29], v[150:153], v[194:197], v[26:29]
	v_mfma_f32_16x16x32_bf16 v[14:17], v[142:145], v[202:205], v[14:17]
	v_mfma_f32_16x16x32_bf16 v[10:13], v[150:153], v[202:205], v[10:13]
	v_mfma_f32_16x16x32_bf16 v[62:65], v[146:149], v[182:185], v[62:65]
	v_mfma_f32_16x16x32_bf16 v[58:61], v[154:157], v[182:185], v[58:61]
	v_mfma_f32_16x16x32_bf16 v[46:49], v[146:149], v[190:193], v[46:49]
	v_mfma_f32_16x16x32_bf16 v[42:45], v[154:157], v[190:193], v[42:45]
	v_mfma_f32_16x16x32_bf16 v[30:33], v[146:149], v[198:201], v[30:33]
	v_mfma_f32_16x16x32_bf16 v[26:29], v[154:157], v[198:201], v[26:29]
	v_mfma_f32_16x16x32_bf16 v[14:17], v[146:149], v[206:209], v[14:17]
	v_mfma_f32_16x16x32_bf16 v[10:13], v[154:157], v[206:209], v[10:13]
	v_mfma_f32_16x16x32_bf16 v[54:57], v[158:161], v[178:181], v[54:57]
	v_mfma_f32_16x16x32_bf16 v[50:53], v[166:169], v[178:181], v[50:53]
	v_mfma_f32_16x16x32_bf16 v[38:41], v[158:161], v[186:189], v[38:41]
	v_mfma_f32_16x16x32_bf16 v[34:37], v[166:169], v[186:189], v[34:37]
	v_mfma_f32_16x16x32_bf16 v[22:25], v[158:161], v[194:197], v[22:25]
	v_mfma_f32_16x16x32_bf16 v[18:21], v[166:169], v[194:197], v[18:21]
	v_mfma_f32_16x16x32_bf16 v[6:9], v[158:161], v[202:205], v[6:9]
	v_mfma_f32_16x16x32_bf16 v[2:5], v[166:169], v[202:205], v[2:5]
	v_mfma_f32_16x16x32_bf16 v[54:57], v[162:165], v[182:185], v[54:57]
	v_mfma_f32_16x16x32_bf16 v[50:53], v[174:177], v[182:185], v[50:53]
	v_mfma_f32_16x16x32_bf16 v[38:41], v[162:165], v[190:193], v[38:41]
	v_mfma_f32_16x16x32_bf16 v[34:37], v[174:177], v[190:193], v[34:37]
	v_mfma_f32_16x16x32_bf16 v[22:25], v[162:165], v[198:201], v[22:25]
	v_mfma_f32_16x16x32_bf16 v[18:21], v[174:177], v[198:201], v[18:21]
	v_mfma_f32_16x16x32_bf16 v[6:9], v[162:165], v[206:209], v[6:9]
	v_mfma_f32_16x16x32_bf16 v[2:5], v[174:177], v[206:209], v[2:5]
	s_setprio 0
	s_barrier
.Lmid170:
	ds_read_b128 v[142:145], v139
	ds_read_b128 v[146:149], v139 offset:1024
	ds_read_b128 v[150:153], v139 offset:2048
	ds_read_b128 v[154:157], v139 offset:3072
	ds_read_b128 v[158:161], v140
	ds_read_b128 v[162:165], v140 offset:1024
	ds_read_b128 v[166:169], v140 offset:2048
	ds_read_b128 v[174:177], v140 offset:3072
	ds_read_b128 v[178:181], v138 offset:32768
	ds_read_b128 v[182:185], v138 offset:33792
	ds_read_b128 v[186:189], v138 offset:34816
	ds_read_b128 v[190:193], v138 offset:35840
	ds_read_b128 v[194:197], v138 offset:36864
	ds_read_b128 v[198:201], v138 offset:37888
	ds_read_b128 v[202:205], v138 offset:38912
	ds_read_b128 v[206:209], v138 offset:39936
	s_add_u32 s12, s20, 0x40000
	s_addc_u32 s13, s21, 0
	s_mov_b32 s20, m0
	s_mov_b32 m0, s31
	s_nop 2
	global_load_lds_dwordx4 v132, s[12:13]
	s_mov_b32 m0, s20
	s_nop 0
	s_mov_b32 s20, m0
	s_mov_b32 m0, s33
	s_nop 2
	global_load_lds_dwordx4 v134, s[12:13]
	s_mov_b32 m0, s20
	s_waitcnt vmcnt(8)
	s_waitcnt lgkmcnt(0)
	s_barrier
	s_setprio 1
	v_mfma_f32_16x16x32_bf16 v[126:129], v[142:145], v[178:181], v[126:129]
	v_mfma_f32_16x16x32_bf16 v[122:125], v[150:153], v[178:181], v[122:125]
	v_mfma_f32_16x16x32_bf16 v[110:113], v[142:145], v[186:189], v[110:113]
	v_mfma_f32_16x16x32_bf16 v[106:109], v[150:153], v[186:189], v[106:109]
	v_mfma_f32_16x16x32_bf16 v[94:97], v[142:145], v[194:197], v[94:97]
	v_mfma_f32_16x16x32_bf16 v[90:93], v[150:153], v[194:197], v[90:93]
	v_mfma_f32_16x16x32_bf16 v[78:81], v[142:145], v[202:205], v[78:81]
	v_mfma_f32_16x16x32_bf16 v[74:77], v[150:153], v[202:205], v[74:77]
	v_mfma_f32_16x16x32_bf16 v[126:129], v[146:149], v[182:185], v[126:129]
	v_mfma_f32_16x16x32_bf16 v[122:125], v[154:157], v[182:185], v[122:125]
	v_mfma_f32_16x16x32_bf16 v[110:113], v[146:149], v[190:193], v[110:113]
	v_mfma_f32_16x16x32_bf16 v[106:109], v[154:157], v[190:193], v[106:109]
	v_mfma_f32_16x16x32_bf16 v[94:97], v[146:149], v[198:201], v[94:97]
	v_mfma_f32_16x16x32_bf16 v[90:93], v[154:157], v[198:201], v[90:93]
	v_mfma_f32_16x16x32_bf16 v[78:81], v[146:149], v[206:209], v[78:81]
	v_mfma_f32_16x16x32_bf16 v[74:77], v[154:157], v[206:209], v[74:77]
	v_mfma_f32_16x16x32_bf16 v[118:121], v[158:161], v[178:181], v[118:121]
	v_mfma_f32_16x16x32_bf16 v[114:117], v[166:169], v[178:181], v[114:117]
	v_mfma_f32_16x16x32_bf16 v[102:105], v[158:161], v[186:189], v[102:105]
	v_mfma_f32_16x16x32_bf16 v[98:101], v[166:169], v[186:189], v[98:101]
	v_mfma_f32_16x16x32_bf16 v[86:89], v[158:161], v[194:197], v[86:89]
	v_mfma_f32_16x16x32_bf16 v[82:85], v[166:169], v[194:197], v[82:85]
	v_mfma_f32_16x16x32_bf16 v[70:73], v[158:161], v[202:205], v[70:73]
	v_mfma_f32_16x16x32_bf16 v[66:69], v[166:169], v[202:205], v[66:69]
	v_mfma_f32_16x16x32_bf16 v[118:121], v[162:165], v[182:185], v[118:121]
	v_mfma_f32_16x16x32_bf16 v[114:117], v[174:177], v[182:185], v[114:117]
	v_mfma_f32_16x16x32_bf16 v[102:105], v[162:165], v[190:193], v[102:105]
	v_mfma_f32_16x16x32_bf16 v[98:101], v[174:177], v[190:193], v[98:101]
	v_mfma_f32_16x16x32_bf16 v[86:89], v[162:165], v[198:201], v[86:89]
	v_mfma_f32_16x16x32_bf16 v[82:85], v[174:177], v[198:201], v[82:85]
	v_mfma_f32_16x16x32_bf16 v[70:73], v[162:165], v[206:209], v[70:73]
	v_mfma_f32_16x16x32_bf16 v[66:69], v[174:177], v[206:209], v[66:69]
	s_setprio 0
	s_barrier
	ds_read_b128 v[178:181], v138 offset:49152
	ds_read_b128 v[182:185], v138 offset:50176
	ds_read_b128 v[186:189], v138 offset:51200
	ds_read_b128 v[190:193], v138 offset:52224
	ds_read_b128 v[194:197], v138 offset:53248
	ds_read_b128 v[198:201], v138 offset:54272
	ds_read_b128 v[202:205], v138 offset:55296
	ds_read_b128 v[206:209], v138 offset:56320
	s_add_u32 s12, s18, 0x80
	s_addc_u32 s13, s19, 0
	s_mov_b32 s20, m0
	s_mov_b32 m0, s34
	s_nop 2
	global_load_lds_dwordx4 v133, s[12:13]
	s_mov_b32 m0, s20
	s_nop 0
	s_mov_b32 s20, m0
	s_mov_b32 m0, s35
	s_nop 2
	global_load_lds_dwordx4 v135, s[12:13]
	s_mov_b32 m0, s20
	s_add_u32 s12, s18, 0x40080
	s_addc_u32 s13, s19, 0
	s_mov_b32 s18, m0
	s_mov_b32 m0, s40
	s_nop 2
	global_load_lds_dwordx4 v133, s[12:13]
	s_mov_b32 m0, s18
	s_nop 0
	s_mov_b32 s18, m0
	s_mov_b32 m0, s41
	s_nop 2
	global_load_lds_dwordx4 v135, s[12:13]
	s_mov_b32 m0, s18
	s_mov_b32 s12, m0
	s_mov_b32 m0, s36
	s_nop 2
	global_load_lds_dwordx4 v132, s[16:17]
	s_mov_b32 m0, s12
	s_nop 0
	s_mov_b32 s12, m0
	s_mov_b32 m0, s37
	s_nop 2
	global_load_lds_dwordx4 v134, s[16:17]
	s_mov_b32 m0, s12
	s_waitcnt vmcnt(8)
	s_waitcnt lgkmcnt(0)
	s_barrier
	s_setprio 1
	v_mfma_f32_16x16x32_bf16 v[62:65], v[142:145], v[178:181], v[62:65]
	v_mfma_f32_16x16x32_bf16 v[58:61], v[150:153], v[178:181], v[58:61]
	v_mfma_f32_16x16x32_bf16 v[46:49], v[142:145], v[186:189], v[46:49]
	v_mfma_f32_16x16x32_bf16 v[42:45], v[150:153], v[186:189], v[42:45]
	v_mfma_f32_16x16x32_bf16 v[30:33], v[142:145], v[194:197], v[30:33]
	v_mfma_f32_16x16x32_bf16 v[26:29], v[150:153], v[194:197], v[26:29]
	v_mfma_f32_16x16x32_bf16 v[14:17], v[142:145], v[202:205], v[14:17]
	v_mfma_f32_16x16x32_bf16 v[10:13], v[150:153], v[202:205], v[10:13]
	v_mfma_f32_16x16x32_bf16 v[62:65], v[146:149], v[182:185], v[62:65]
	v_mfma_f32_16x16x32_bf16 v[58:61], v[154:157], v[182:185], v[58:61]
	v_mfma_f32_16x16x32_bf16 v[46:49], v[146:149], v[190:193], v[46:49]
	v_mfma_f32_16x16x32_bf16 v[42:45], v[154:157], v[190:193], v[42:45]
	v_mfma_f32_16x16x32_bf16 v[30:33], v[146:149], v[198:201], v[30:33]
	v_mfma_f32_16x16x32_bf16 v[26:29], v[154:157], v[198:201], v[26:29]
	v_mfma_f32_16x16x32_bf16 v[14:17], v[146:149], v[206:209], v[14:17]
	v_mfma_f32_16x16x32_bf16 v[10:13], v[154:157], v[206:209], v[10:13]
	v_mfma_f32_16x16x32_bf16 v[54:57], v[158:161], v[178:181], v[54:57]
	v_mfma_f32_16x16x32_bf16 v[50:53], v[166:169], v[178:181], v[50:53]
	v_mfma_f32_16x16x32_bf16 v[38:41], v[158:161], v[186:189], v[38:41]
	v_mfma_f32_16x16x32_bf16 v[34:37], v[166:169], v[186:189], v[34:37]
	v_mfma_f32_16x16x32_bf16 v[22:25], v[158:161], v[194:197], v[22:25]
	v_mfma_f32_16x16x32_bf16 v[18:21], v[166:169], v[194:197], v[18:21]
	v_mfma_f32_16x16x32_bf16 v[6:9], v[158:161], v[202:205], v[6:9]
	v_mfma_f32_16x16x32_bf16 v[2:5], v[166:169], v[202:205], v[2:5]
	v_mfma_f32_16x16x32_bf16 v[54:57], v[162:165], v[182:185], v[54:57]
	v_mfma_f32_16x16x32_bf16 v[50:53], v[174:177], v[182:185], v[50:53]
	v_mfma_f32_16x16x32_bf16 v[38:41], v[162:165], v[190:193], v[38:41]
	v_mfma_f32_16x16x32_bf16 v[34:37], v[174:177], v[190:193], v[34:37]
	v_mfma_f32_16x16x32_bf16 v[22:25], v[162:165], v[198:201], v[22:25]
	v_mfma_f32_16x16x32_bf16 v[18:21], v[174:177], v[198:201], v[18:21]
	v_mfma_f32_16x16x32_bf16 v[6:9], v[162:165], v[206:209], v[6:9]
	v_mfma_f32_16x16x32_bf16 v[2:5], v[174:177], v[206:209], v[2:5]
	s_setprio 0
	s_barrier
	s_add_i32 s56, s56, 2
	s_add_u32 s54, s54, 0x100
	s_addc_u32 s55, s55, 0
	s_cmp_gt_u32 s56, 13
	s_mov_b64 s[12:13], s[14:15]
	s_cbranch_scc0 .LBB0_170
	s_cmpk_lt_u32 s23, 0x100
	s_cbranch_scc0 .LBB0_173
	s_barrier

.LBB0_190:
	ds_read_b128 v[18:21], v174
	ds_read_b128 v[22:25], v174 offset:1024
	ds_read_b128 v[26:29], v174 offset:2048
	ds_read_b128 v[30:33], v174 offset:3072
	ds_read_b128 v[2:5], v175
	ds_read_b128 v[6:9], v175 offset:1024
	ds_read_b128 v[10:13], v175 offset:2048
	ds_read_b128 v[14:17], v175 offset:3072
	s_add_u32 s76, s78, 0x100
	s_addc_u32 s77, s79, 0
	s_cmp_eq_u32 s33, 4
	s_cselect_b32 s84, s59, s76
	s_cselect_b32 s85, s7, s77
	s_cselect_b32 s82, s67, vcc_lo
	s_cselect_b32 s83, s57, vcc_hi
	s_add_u32 s80, s84, 0x80
	s_addc_u32 s81, s85, 0
	ds_read_b128 v[180:183], v176
	ds_read_b128 v[184:187], v176 offset:1024
	ds_read_b128 v[188:191], v176 offset:2048
	ds_read_b128 v[192:195], v176 offset:3072
	ds_read_b128 v[196:199], v176 offset:4096
	ds_read_b128 v[200:203], v176 offset:5120
	ds_read_b128 v[204:207], v176 offset:6144
	ds_read_b128 v[208:211], v176 offset:7168
	s_add_u32 s78, s78, 0x20080
	s_addc_u32 s79, s79, 0
	s_mov_b32 s88, m0
	s_mov_b32 m0, s96
	s_nop 2
	global_load_lds_dwordx4 v166, s[78:79]
	s_mov_b32 m0, s88
	s_nop 0
	s_mov_b32 s88, m0
	s_mov_b32 m0, s92
	s_nop 2
	global_load_lds_dwordx4 v168, s[78:79]
	s_mov_b32 m0, s88
	s_waitcnt vmcnt(8)
	s_waitcnt lgkmcnt(0)
	s_barrier
	s_setprio 1
	v_mfma_f32_16x16x128_f8f6f4 v[158:161], v[18:25], v[180:187], v[158:161]
	v_mfma_f32_16x16x128_f8f6f4 v[154:157], v[26:33], v[180:187], v[154:157]
	v_mfma_f32_16x16x128_f8f6f4 v[146:149], v[18:25], v[188:195], v[146:149]
	v_mfma_f32_16x16x128_f8f6f4 v[138:141], v[26:33], v[188:195], v[138:141]
	v_mfma_f32_16x16x128_f8f6f4 v[130:133], v[18:25], v[196:203], v[130:133]
	v_mfma_f32_16x16x128_f8f6f4 v[122:125], v[26:33], v[196:203], v[122:125]
	v_mfma_f32_16x16x128_f8f6f4 v[114:117], v[18:25], v[204:211], v[114:117]
	v_mfma_f32_16x16x128_f8f6f4 v[106:109], v[26:33], v[204:211], v[106:109]
	v_mfma_f32_16x16x128_f8f6f4 v[150:153], v[2:9], v[180:187], v[150:153]
	v_mfma_f32_16x16x128_f8f6f4 v[142:145], v[10:17], v[180:187], v[142:145]
	v_mfma_f32_16x16x128_f8f6f4 v[134:137], v[2:9], v[188:195], v[134:137]
	v_mfma_f32_16x16x128_f8f6f4 v[126:129], v[10:17], v[188:195], v[126:129]
	v_mfma_f32_16x16x128_f8f6f4 v[118:121], v[2:9], v[196:203], v[118:121]
	v_mfma_f32_16x16x128_f8f6f4 v[110:113], v[10:17], v[196:203], v[110:113]
	v_mfma_f32_16x16x128_f8f6f4 v[102:105], v[2:9], v[204:211], v[102:105]
	v_mfma_f32_16x16x128_f8f6f4 v[98:101], v[10:17], v[204:211], v[98:101]
	s_setprio 0
	s_barrier
	ds_read_b128 v[180:183], v176 offset:16384
	ds_read_b128 v[184:187], v176 offset:17408
	ds_read_b128 v[188:191], v176 offset:18432
	ds_read_b128 v[192:195], v176 offset:19456
	ds_read_b128 v[196:199], v176 offset:20480
	ds_read_b128 v[200:203], v176 offset:21504
	ds_read_b128 v[204:207], v176 offset:22528
	ds_read_b128 v[208:211], v176 offset:23552
	s_mov_b32 s78, m0
	s_mov_b32 m0, s36
	s_nop 2
	global_load_lds_dwordx4 v167, s[82:83]
	s_mov_b32 m0, s78
	s_nop 0
	s_mov_b32 s78, m0
	s_mov_b32 m0, s37
	s_nop 2
	global_load_lds_dwordx4 v169, s[82:83]
	s_mov_b32 m0, s78
	s_add_u32 s78, s82, 0x20000
	s_addc_u32 s79, s83, 0
	s_mov_b32 s88, m0
	s_mov_b32 m0, s55
	s_nop 2
	global_load_lds_dwordx4 v167, s[78:79]
	s_mov_b32 m0, s88
	s_nop 0
	s_mov_b32 s88, m0
	s_mov_b32 m0, s86
	s_nop 2
	global_load_lds_dwordx4 v169, s[78:79]
	s_mov_b32 m0, s88
	s_mov_b32 s78, m0
	s_mov_b32 m0, s35
	s_nop 2
	global_load_lds_dwordx4 v166, s[84:85]
	s_mov_b32 m0, s78
	s_nop 0
	s_mov_b32 s78, m0
	s_mov_b32 m0, s87
	s_nop 2
	global_load_lds_dwordx4 v168, s[84:85]
	s_mov_b32 m0, s78
	s_waitcnt vmcnt(8)
	s_waitcnt lgkmcnt(0)
	s_barrier
	s_setprio 1
	v_mfma_f32_16x16x128_f8f6f4 v[94:97], v[18:25], v[180:187], v[94:97]
	v_mfma_f32_16x16x128_f8f6f4 v[90:93], v[26:33], v[180:187], v[90:93]
	v_mfma_f32_16x16x128_f8f6f4 v[82:85], v[18:25], v[188:195], v[82:85]
	v_mfma_f32_16x16x128_f8f6f4 v[74:77], v[26:33], v[188:195], v[74:77]
	v_mfma_f32_16x16x128_f8f6f4 v[66:69], v[18:25], v[196:203], v[66:69]
	v_mfma_f32_16x16x128_f8f6f4 v[58:61], v[26:33], v[196:203], v[58:61]
	v_mfma_f32_16x16x128_f8f6f4 v[50:53], v[18:25], v[204:211], v[50:53]
	v_mfma_f32_16x16x128_f8f6f4 v[42:45], v[26:33], v[204:211], v[42:45]
	v_mfma_f32_16x16x128_f8f6f4 v[86:89], v[2:9], v[180:187], v[86:89]
	v_mfma_f32_16x16x128_f8f6f4 v[78:81], v[10:17], v[180:187], v[78:81]
	v_mfma_f32_16x16x128_f8f6f4 v[70:73], v[2:9], v[188:195], v[70:73]
	v_mfma_f32_16x16x128_f8f6f4 v[62:65], v[10:17], v[188:195], v[62:65]
	v_mfma_f32_16x16x128_f8f6f4 v[54:57], v[2:9], v[196:203], v[54:57]
	v_mfma_f32_16x16x128_f8f6f4 v[46:49], v[10:17], v[196:203], v[46:49]
	v_mfma_f32_16x16x128_f8f6f4 v[38:41], v[2:9], v[204:211], v[38:41]
	v_mfma_f32_16x16x128_f8f6f4 v[34:37], v[10:17], v[204:211], v[34:37]
	s_setprio 0
	s_barrier
	ds_read_b128 v[2:5], v177
	ds_read_b128 v[6:9], v177 offset:1024
	ds_read_b128 v[10:13], v177 offset:2048
	ds_read_b128 v[14:17], v177 offset:3072
	ds_read_b128 v[18:21], v178
	ds_read_b128 v[22:25], v178 offset:1024
	ds_read_b128 v[26:29], v178 offset:2048
	ds_read_b128 v[30:33], v178 offset:3072
	ds_read_b128 v[180:183], v176 offset:32768
	ds_read_b128 v[184:187], v176 offset:33792
	ds_read_b128 v[188:191], v176 offset:34816
	ds_read_b128 v[192:195], v176 offset:35840
	ds_read_b128 v[196:199], v176 offset:36864
	ds_read_b128 v[200:203], v176 offset:37888
	ds_read_b128 v[204:207], v176 offset:38912
	ds_read_b128 v[208:211], v176 offset:39936
	s_add_u32 s78, s84, 0x20000
	s_addc_u32 s79, s85, 0
	s_mov_b32 s84, m0
	s_mov_b32 m0, s89
	s_nop 2
	global_load_lds_dwordx4 v166, s[78:79]
	s_mov_b32 m0, s84
	s_nop 0
	s_mov_b32 s84, m0
	s_mov_b32 m0, s3
	s_nop 2
	global_load_lds_dwordx4 v168, s[78:79]
	s_mov_b32 m0, s84
	s_waitcnt vmcnt(8)
	s_waitcnt lgkmcnt(0)
	s_barrier
	s_setprio 1
	v_mfma_f32_16x16x128_f8f6f4 v[158:161], v[2:9], v[180:187], v[158:161]
	v_mfma_f32_16x16x128_f8f6f4 v[154:157], v[10:17], v[180:187], v[154:157]
	v_mfma_f32_16x16x128_f8f6f4 v[146:149], v[2:9], v[188:195], v[146:149]
	v_mfma_f32_16x16x128_f8f6f4 v[138:141], v[10:17], v[188:195], v[138:141]
	v_mfma_f32_16x16x128_f8f6f4 v[130:133], v[2:9], v[196:203], v[130:133]
	v_mfma_f32_16x16x128_f8f6f4 v[122:125], v[10:17], v[196:203], v[122:125]
	v_mfma_f32_16x16x128_f8f6f4 v[114:117], v[2:9], v[204:211], v[114:117]
	v_mfma_f32_16x16x128_f8f6f4 v[106:109], v[10:17], v[204:211], v[106:109]
	v_mfma_f32_16x16x128_f8f6f4 v[150:153], v[18:25], v[180:187], v[150:153]
	v_mfma_f32_16x16x128_f8f6f4 v[142:145], v[26:33], v[180:187], v[142:145]
	v_mfma_f32_16x16x128_f8f6f4 v[134:137], v[18:25], v[188:195], v[134:137]
	v_mfma_f32_16x16x128_f8f6f4 v[126:129], v[26:33], v[188:195], v[126:129]
	v_mfma_f32_16x16x128_f8f6f4 v[118:121], v[18:25], v[196:203], v[118:121]
	v_mfma_f32_16x16x128_f8f6f4 v[110:113], v[26:33], v[196:203], v[110:113]
	v_mfma_f32_16x16x128_f8f6f4 v[102:105], v[18:25], v[204:211], v[102:105]
	v_mfma_f32_16x16x128_f8f6f4 v[98:101], v[26:33], v[204:211], v[98:101]
	s_setprio 0
	s_barrier
	ds_read_b128 v[180:183], v176 offset:49152
	ds_read_b128 v[184:187], v176 offset:50176
	ds_read_b128 v[188:191], v176 offset:51200
	ds_read_b128 v[192:195], v176 offset:52224
	ds_read_b128 v[196:199], v176 offset:53248
	ds_read_b128 v[200:203], v176 offset:54272
	ds_read_b128 v[204:207], v176 offset:55296
	ds_read_b128 v[208:211], v176 offset:56320
	s_add_u32 s78, s82, 0x80
	s_addc_u32 s79, s83, 0
	s_mov_b32 s84, m0
	s_mov_b32 m0, s90
	s_nop 2
	global_load_lds_dwordx4 v167, s[78:79]
	s_mov_b32 m0, s84
	s_nop 0
	s_mov_b32 s84, m0
	s_mov_b32 m0, s28
	s_nop 2
	global_load_lds_dwordx4 v169, s[78:79]
	s_mov_b32 m0, s84
	s_add_u32 s78, s82, 0x20080
	s_addc_u32 s79, s83, 0
	s_mov_b32 s82, m0
	s_mov_b32 m0, s94
	s_nop 2
	global_load_lds_dwordx4 v167, s[78:79]
	s_mov_b32 m0, s82
	s_nop 0
	s_mov_b32 s82, m0
	s_mov_b32 m0, s95
	s_nop 2
	global_load_lds_dwordx4 v169, s[78:79]
	s_mov_b32 m0, s82
	s_mov_b32 s78, m0
	s_mov_b32 m0, s93
	s_nop 2
	global_load_lds_dwordx4 v166, s[80:81]
	s_mov_b32 m0, s78
	s_nop 0
	s_mov_b32 s78, m0
	s_mov_b32 m0, s2
	s_nop 2
	global_load_lds_dwordx4 v168, s[80:81]
	s_mov_b32 m0, s78
	s_waitcnt vmcnt(8)
	s_waitcnt lgkmcnt(0)
	s_barrier
	s_setprio 1
	v_mfma_f32_16x16x128_f8f6f4 v[94:97], v[2:9], v[180:187], v[94:97]
	v_mfma_f32_16x16x128_f8f6f4 v[90:93], v[10:17], v[180:187], v[90:93]
	v_mfma_f32_16x16x128_f8f6f4 v[82:85], v[2:9], v[188:195], v[82:85]
	v_mfma_f32_16x16x128_f8f6f4 v[74:77], v[10:17], v[188:195], v[74:77]
	v_mfma_f32_16x16x128_f8f6f4 v[66:69], v[2:9], v[196:203], v[66:69]
	v_mfma_f32_16x16x128_f8f6f4 v[58:61], v[10:17], v[196:203], v[58:61]
	v_mfma_f32_16x16x128_f8f6f4 v[50:53], v[2:9], v[204:211], v[50:53]
	v_mfma_f32_16x16x128_f8f6f4 v[42:45], v[10:17], v[204:211], v[42:45]
	v_mfma_f32_16x16x128_f8f6f4 v[86:89], v[18:25], v[180:187], v[86:89]
	v_mfma_f32_16x16x128_f8f6f4 v[78:81], v[26:33], v[180:187], v[78:81]
	v_mfma_f32_16x16x128_f8f6f4 v[70:73], v[18:25], v[188:195], v[70:73]
	v_mfma_f32_16x16x128_f8f6f4 v[62:65], v[26:33], v[188:195], v[62:65]
	v_mfma_f32_16x16x128_f8f6f4 v[54:57], v[18:25], v[196:203], v[54:57]
	v_mfma_f32_16x16x128_f8f6f4 v[46:49], v[26:33], v[196:203], v[46:49]
	v_mfma_f32_16x16x128_f8f6f4 v[38:41], v[18:25], v[204:211], v[38:41]
	v_mfma_f32_16x16x128_f8f6f4 v[34:37], v[26:33], v[204:211], v[34:37]
	s_setprio 0
	s_barrier
	s_add_i32 s33, s33, 2
	s_add_u32 vcc_lo, vcc_lo, 0x100
	s_addc_u32 vcc_hi, vcc_hi, 0
	s_cmp_gt_u32 s33, 5
	s_mov_b64 s[78:79], s[76:77]
	s_cbranch_scc0 .LBB0_190
	s_and_b64 vcc, exec, s[10:11]
	s_cbranch_vccz .LBB0_193
	s_barrier

.LBB0_217:
	s_cmp_lt_i32 s33, 0
	s_cbranch_scc1 .Lpeel1
	ds_read_b128 v[18:21], v168
	ds_read_b128 v[22:25], v168 offset:1024
	ds_read_b128 v[26:29], v168 offset:2048
	ds_read_b128 v[30:33], v168 offset:3072
	ds_read_b128 v[2:5], v169
	ds_read_b128 v[6:9], v169 offset:1024
	ds_read_b128 v[10:13], v169 offset:2048
	ds_read_b128 v[14:17], v169 offset:3072
	s_add_u32 s78, s80, 0x100
	s_addc_u32 s79, s81, 0
	s_cmp_eq_u32 s33, 4
	s_cselect_b32 s86, s57, s78
	s_cselect_b32 s87, s7, s79
	s_cselect_b32 s84, vcc_lo, vcc_hi
	s_cselect_b32 s85, s59, s89
	s_add_u32 s82, s86, 0x80
	s_addc_u32 s83, s87, 0
	ds_read_b128 v[176:179], v170
	ds_read_b128 v[180:183], v170 offset:1024
	ds_read_b128 v[184:187], v170 offset:2048
	ds_read_b128 v[188:191], v170 offset:3072
	ds_read_b128 v[192:195], v170 offset:4096
	ds_read_b128 v[196:199], v170 offset:5120
	ds_read_b128 v[200:203], v170 offset:6144
	ds_read_b128 v[204:207], v170 offset:7168
	s_add_u32 s80, s80, 0x20080
	s_addc_u32 s81, s81, 0
	s_mov_b32 s29, m0
	s_mov_b32 m0, s91
	s_nop 2
	global_load_lds_dwordx4 v162, s[80:81]
	s_mov_b32 m0, s29
	s_nop 0
	s_mov_b32 s29, m0
	s_mov_b32 m0, s92
	s_nop 2
	global_load_lds_dwordx4 v164, s[80:81]
	s_mov_b32 m0, s29
	s_waitcnt vmcnt(8)
	s_waitcnt lgkmcnt(0)
	s_barrier
	s_setprio 1
	v_mfma_f32_16x16x128_f8f6f4 v[158:161], v[18:25], v[176:183], v[158:161]
	v_mfma_f32_16x16x128_f8f6f4 v[154:157], v[26:33], v[176:183], v[154:157]
	v_mfma_f32_16x16x128_f8f6f4 v[146:149], v[18:25], v[184:191], v[146:149]
	v_mfma_f32_16x16x128_f8f6f4 v[138:141], v[26:33], v[184:191], v[138:141]
	v_mfma_f32_16x16x128_f8f6f4 v[130:133], v[18:25], v[192:199], v[130:133]
	v_mfma_f32_16x16x128_f8f6f4 v[122:125], v[26:33], v[192:199], v[122:125]
	v_mfma_f32_16x16x128_f8f6f4 v[114:117], v[18:25], v[200:207], v[114:117]
	v_mfma_f32_16x16x128_f8f6f4 v[106:109], v[26:33], v[200:207], v[106:109]
	v_mfma_f32_16x16x128_f8f6f4 v[150:153], v[2:9], v[176:183], v[150:153]
	v_mfma_f32_16x16x128_f8f6f4 v[142:145], v[10:17], v[176:183], v[142:145]
	v_mfma_f32_16x16x128_f8f6f4 v[134:137], v[2:9], v[184:191], v[134:137]
	v_mfma_f32_16x16x128_f8f6f4 v[126:129], v[10:17], v[184:191], v[126:129]
	v_mfma_f32_16x16x128_f8f6f4 v[118:121], v[2:9], v[192:199], v[118:121]
	v_mfma_f32_16x16x128_f8f6f4 v[110:113], v[10:17], v[192:199], v[110:113]
	v_mfma_f32_16x16x128_f8f6f4 v[102:105], v[2:9], v[200:207], v[102:105]
	v_mfma_f32_16x16x128_f8f6f4 v[98:101], v[10:17], v[200:207], v[98:101]
	s_setprio 0
	s_barrier
	ds_read_b128 v[176:179], v170 offset:16384
	ds_read_b128 v[180:183], v170 offset:17408
	ds_read_b128 v[184:187], v170 offset:18432
	ds_read_b128 v[188:191], v170 offset:19456
	ds_read_b128 v[192:195], v170 offset:20480
	ds_read_b128 v[196:199], v170 offset:21504
	ds_read_b128 v[200:203], v170 offset:22528
	ds_read_b128 v[204:207], v170 offset:23552
	s_mov_b32 s29, m0
	s_mov_b32 m0, s36
	s_nop 2
	global_load_lds_dwordx4 v163, s[84:85]
	s_mov_b32 m0, s29
	s_add_u32 s80, s84, 0x20000
	s_mov_b32 s29, m0
	s_mov_b32 m0, s37
	s_nop 2
	global_load_lds_dwordx4 v165, s[84:85]
	s_mov_b32 m0, s29
	s_addc_u32 s81, s85, 0
	s_mov_b32 s29, m0
	s_mov_b32 m0, s55
	s_nop 2
	global_load_lds_dwordx4 v163, s[80:81]
	s_mov_b32 m0, s29
	s_nop 0
	s_mov_b32 s29, m0
	s_mov_b32 m0, s77
	s_nop 2
	global_load_lds_dwordx4 v165, s[80:81]
	s_mov_b32 m0, s29
	s_nop 0
	s_mov_b32 s29, m0
	s_mov_b32 m0, s35
	s_nop 2
	global_load_lds_dwordx4 v162, s[86:87]
	s_mov_b32 m0, s29
	s_nop 0
	s_mov_b32 s29, m0
	s_mov_b32 m0, s88
	s_nop 2
	global_load_lds_dwordx4 v164, s[86:87]
	s_mov_b32 m0, s29
	s_waitcnt vmcnt(8)
	s_waitcnt lgkmcnt(0)
	s_barrier
	s_setprio 1
	v_mfma_f32_16x16x128_f8f6f4 v[94:97], v[18:25], v[176:183], v[94:97]
	v_mfma_f32_16x16x128_f8f6f4 v[90:93], v[26:33], v[176:183], v[90:93]
	v_mfma_f32_16x16x128_f8f6f4 v[82:85], v[18:25], v[184:191], v[82:85]
	v_mfma_f32_16x16x128_f8f6f4 v[74:77], v[26:33], v[184:191], v[74:77]
	v_mfma_f32_16x16x128_f8f6f4 v[66:69], v[18:25], v[192:199], v[66:69]
	v_mfma_f32_16x16x128_f8f6f4 v[58:61], v[26:33], v[192:199], v[58:61]
	v_mfma_f32_16x16x128_f8f6f4 v[50:53], v[18:25], v[200:207], v[50:53]
	v_mfma_f32_16x16x128_f8f6f4 v[42:45], v[26:33], v[200:207], v[42:45]
	v_mfma_f32_16x16x128_f8f6f4 v[86:89], v[2:9], v[176:183], v[86:89]
	v_mfma_f32_16x16x128_f8f6f4 v[78:81], v[10:17], v[176:183], v[78:81]
	v_mfma_f32_16x16x128_f8f6f4 v[70:73], v[2:9], v[184:191], v[70:73]
	v_mfma_f32_16x16x128_f8f6f4 v[62:65], v[10:17], v[184:191], v[62:65]
	v_mfma_f32_16x16x128_f8f6f4 v[54:57], v[2:9], v[192:199], v[54:57]
	v_mfma_f32_16x16x128_f8f6f4 v[46:49], v[10:17], v[192:199], v[46:49]
	v_mfma_f32_16x16x128_f8f6f4 v[38:41], v[2:9], v[200:207], v[38:41]
	v_mfma_f32_16x16x128_f8f6f4 v[34:37], v[10:17], v[200:207], v[34:37]
	s_setprio 0
	s_barrier
.Lmid1:
	ds_read_b128 v[2:5], v172
	ds_read_b128 v[6:9], v172 offset:1024
	ds_read_b128 v[10:13], v172 offset:2048
	ds_read_b128 v[14:17], v172 offset:3072
	ds_read_b128 v[18:21], v174
	ds_read_b128 v[22:25], v174 offset:1024
	ds_read_b128 v[26:29], v174 offset:2048
	ds_read_b128 v[30:33], v174 offset:3072
	ds_read_b128 v[176:179], v170 offset:32768
	ds_read_b128 v[180:183], v170 offset:33792
	ds_read_b128 v[184:187], v170 offset:34816
	ds_read_b128 v[188:191], v170 offset:35840
	ds_read_b128 v[192:195], v170 offset:36864
	ds_read_b128 v[196:199], v170 offset:37888
	ds_read_b128 v[200:203], v170 offset:38912
	ds_read_b128 v[204:207], v170 offset:39936
	s_add_u32 s80, s86, 0x20000
	s_addc_u32 s81, s87, 0
	s_mov_b32 s29, m0
	s_mov_b32 m0, s97
	s_nop 2
	global_load_lds_dwordx4 v162, s[80:81]
	s_mov_b32 m0, s29
	s_nop 0
	s_mov_b32 s29, m0
	s_mov_b32 m0, s3
	s_nop 2
	global_load_lds_dwordx4 v164, s[80:81]
	s_mov_b32 m0, s29
	s_waitcnt vmcnt(8)
	s_waitcnt lgkmcnt(0)
	s_barrier
	s_setprio 1
	v_mfma_f32_16x16x128_f8f6f4 v[158:161], v[2:9], v[176:183], v[158:161]
	v_mfma_f32_16x16x128_f8f6f4 v[154:157], v[10:17], v[176:183], v[154:157]
	v_mfma_f32_16x16x128_f8f6f4 v[146:149], v[2:9], v[184:191], v[146:149]
	v_mfma_f32_16x16x128_f8f6f4 v[138:141], v[10:17], v[184:191], v[138:141]
	v_mfma_f32_16x16x128_f8f6f4 v[130:133], v[2:9], v[192:199], v[130:133]
	v_mfma_f32_16x16x128_f8f6f4 v[122:125], v[10:17], v[192:199], v[122:125]
	v_mfma_f32_16x16x128_f8f6f4 v[114:117], v[2:9], v[200:207], v[114:117]
	v_mfma_f32_16x16x128_f8f6f4 v[106:109], v[10:17], v[200:207], v[106:109]
	v_mfma_f32_16x16x128_f8f6f4 v[150:153], v[18:25], v[176:183], v[150:153]
	v_mfma_f32_16x16x128_f8f6f4 v[142:145], v[26:33], v[176:183], v[142:145]
	v_mfma_f32_16x16x128_f8f6f4 v[134:137], v[18:25], v[184:191], v[134:137]
	v_mfma_f32_16x16x128_f8f6f4 v[126:129], v[26:33], v[184:191], v[126:129]
	v_mfma_f32_16x16x128_f8f6f4 v[118:121], v[18:25], v[192:199], v[118:121]
	v_mfma_f32_16x16x128_f8f6f4 v[110:113], v[26:33], v[192:199], v[110:113]
	v_mfma_f32_16x16x128_f8f6f4 v[102:105], v[18:25], v[200:207], v[102:105]
	v_mfma_f32_16x16x128_f8f6f4 v[98:101], v[26:33], v[200:207], v[98:101]
	s_setprio 0
	s_barrier
	ds_read_b128 v[176:179], v170 offset:49152
	ds_read_b128 v[180:183], v170 offset:50176
	ds_read_b128 v[184:187], v170 offset:51200
	ds_read_b128 v[188:191], v170 offset:52224
	ds_read_b128 v[192:195], v170 offset:53248
	ds_read_b128 v[196:199], v170 offset:54272
	ds_read_b128 v[200:203], v170 offset:55296
	ds_read_b128 v[204:207], v170 offset:56320
	s_add_u32 s80, s84, 0x80
	s_addc_u32 s81, s85, 0
	s_mov_b32 s29, m0
	s_mov_b32 m0, s90
	s_nop 2
	global_load_lds_dwordx4 v163, s[80:81]
	s_mov_b32 m0, s29
	s_nop 0
	s_mov_b32 s29, m0
	s_mov_b32 m0, s28
	s_nop 2
	global_load_lds_dwordx4 v165, s[80:81]
	s_mov_b32 m0, s29
	s_add_u32 s80, s84, 0x20080
	s_addc_u32 s81, s85, 0
	s_mov_b32 s29, m0
	s_mov_b32 m0, s94
	s_nop 2
	global_load_lds_dwordx4 v163, s[80:81]
	s_mov_b32 m0, s29
	s_nop 0
	s_mov_b32 s29, m0
	s_mov_b32 m0, s95
	s_nop 2
	global_load_lds_dwordx4 v165, s[80:81]
	s_mov_b32 m0, s29
	s_nop 0
	s_mov_b32 s29, m0
	s_mov_b32 m0, s93
	s_nop 2
	global_load_lds_dwordx4 v162, s[82:83]
	s_mov_b32 m0, s29
	s_nop 0
	s_mov_b32 s29, m0
	s_mov_b32 m0, s2
	s_nop 2
	global_load_lds_dwordx4 v164, s[82:83]
	s_mov_b32 m0, s29
	s_waitcnt vmcnt(8)
	s_waitcnt lgkmcnt(0)
	s_barrier
	s_setprio 1
	v_mfma_f32_16x16x128_f8f6f4 v[94:97], v[2:9], v[176:183], v[94:97]
	v_mfma_f32_16x16x128_f8f6f4 v[90:93], v[10:17], v[176:183], v[90:93]
	v_mfma_f32_16x16x128_f8f6f4 v[82:85], v[2:9], v[184:191], v[82:85]
	v_mfma_f32_16x16x128_f8f6f4 v[74:77], v[10:17], v[184:191], v[74:77]
	v_mfma_f32_16x16x128_f8f6f4 v[66:69], v[2:9], v[192:199], v[66:69]
	v_mfma_f32_16x16x128_f8f6f4 v[58:61], v[10:17], v[192:199], v[58:61]
	v_mfma_f32_16x16x128_f8f6f4 v[50:53], v[2:9], v[200:207], v[50:53]
	v_mfma_f32_16x16x128_f8f6f4 v[42:45], v[10:17], v[200:207], v[42:45]
	v_mfma_f32_16x16x128_f8f6f4 v[86:89], v[18:25], v[176:183], v[86:89]
	v_mfma_f32_16x16x128_f8f6f4 v[78:81], v[26:33], v[176:183], v[78:81]
	v_mfma_f32_16x16x128_f8f6f4 v[70:73], v[18:25], v[184:191], v[70:73]
	v_mfma_f32_16x16x128_f8f6f4 v[62:65], v[26:33], v[184:191], v[62:65]
	v_mfma_f32_16x16x128_f8f6f4 v[54:57], v[18:25], v[192:199], v[54:57]
	v_mfma_f32_16x16x128_f8f6f4 v[46:49], v[26:33], v[192:199], v[46:49]
	v_mfma_f32_16x16x128_f8f6f4 v[38:41], v[18:25], v[200:207], v[38:41]
	v_mfma_f32_16x16x128_f8f6f4 v[34:37], v[26:33], v[200:207], v[34:37]
	s_setprio 0
	s_cmp_lt_i32 s33, 4
	s_cbranch_scc1 .Lkb1_do
	s_cmp_lg_u64 s[10:11], 0
	s_cbranch_scc0 .Lkb1_skip

.Lpeel1:
	ds_read_b128 v[18:21], v168
	ds_read_b128 v[22:25], v168 offset:1024
	ds_read_b128 v[26:29], v168 offset:2048
	ds_read_b128 v[30:33], v168 offset:3072
	ds_read_b128 v[2:5], v169
	ds_read_b128 v[6:9], v169 offset:1024
	ds_read_b128 v[10:13], v169 offset:2048
	ds_read_b128 v[14:17], v169 offset:3072
	s_add_u32 s78, s80, 0x100
	s_addc_u32 s79, s81, 0
	s_cmp_eq_u32 s33, 4
	s_cselect_b32 s86, s57, s78
	s_cselect_b32 s87, s7, s79
	s_cselect_b32 s84, vcc_lo, vcc_hi
	s_cselect_b32 s85, s59, s89
	s_add_u32 s82, s86, 0x80
	s_addc_u32 s83, s87, 0
	ds_read_b128 v[176:179], v170
	ds_read_b128 v[180:183], v170 offset:1024
	ds_read_b128 v[184:187], v170 offset:2048
	ds_read_b128 v[188:191], v170 offset:3072
	ds_read_b128 v[192:195], v170 offset:4096
	ds_read_b128 v[196:199], v170 offset:5120
	ds_read_b128 v[200:203], v170 offset:6144
	ds_read_b128 v[204:207], v170 offset:7168
	s_add_u32 s80, s80, 0x20080
	s_addc_u32 s81, s81, 0
	s_mov_b32 s29, m0
	s_mov_b32 m0, s91
	s_nop 2
	global_load_lds_dwordx4 v162, s[80:81]
	s_mov_b32 m0, s29
	s_nop 0
	s_mov_b32 s29, m0
	s_mov_b32 m0, s92
	s_nop 2
	global_load_lds_dwordx4 v164, s[80:81]
	s_mov_b32 m0, s29
	s_waitcnt vmcnt(8)
	s_waitcnt lgkmcnt(0)
	s_barrier
	s_setprio 1
	v_mfma_f32_16x16x128_f8f6f4 v[158:161], v[18:25], v[176:183], 0
	v_mfma_f32_16x16x128_f8f6f4 v[154:157], v[26:33], v[176:183], 0
	v_mfma_f32_16x16x128_f8f6f4 v[146:149], v[18:25], v[184:191], 0
	v_mfma_f32_16x16x128_f8f6f4 v[138:141], v[26:33], v[184:191], 0
	v_mfma_f32_16x16x128_f8f6f4 v[130:133], v[18:25], v[192:199], 0
	v_mfma_f32_16x16x128_f8f6f4 v[122:125], v[26:33], v[192:199], 0
	v_mfma_f32_16x16x128_f8f6f4 v[114:117], v[18:25], v[200:207], 0
	v_mfma_f32_16x16x128_f8f6f4 v[106:109], v[26:33], v[200:207], 0
	v_mfma_f32_16x16x128_f8f6f4 v[150:153], v[2:9], v[176:183], 0
	v_mfma_f32_16x16x128_f8f6f4 v[142:145], v[10:17], v[176:183], 0
	v_mfma_f32_16x16x128_f8f6f4 v[134:137], v[2:9], v[184:191], 0
	v_mfma_f32_16x16x128_f8f6f4 v[126:129], v[10:17], v[184:191], 0
	v_mfma_f32_16x16x128_f8f6f4 v[118:121], v[2:9], v[192:199], 0
	v_mfma_f32_16x16x128_f8f6f4 v[110:113], v[10:17], v[192:199], 0
	v_mfma_f32_16x16x128_f8f6f4 v[102:105], v[2:9], v[200:207], 0
	v_mfma_f32_16x16x128_f8f6f4 v[98:101], v[10:17], v[200:207], 0
	s_setprio 0
	s_barrier
	ds_read_b128 v[176:179], v170 offset:16384
	ds_read_b128 v[180:183], v170 offset:17408
	ds_read_b128 v[184:187], v170 offset:18432
	ds_read_b128 v[188:191], v170 offset:19456
	ds_read_b128 v[192:195], v170 offset:20480
	ds_read_b128 v[196:199], v170 offset:21504
	ds_read_b128 v[200:203], v170 offset:22528
	ds_read_b128 v[204:207], v170 offset:23552
	s_mov_b32 s29, m0
	s_mov_b32 m0, s36
	s_nop 2
	global_load_lds_dwordx4 v163, s[84:85]
	s_mov_b32 m0, s29
	s_add_u32 s80, s84, 0x20000
	s_mov_b32 s29, m0
	s_mov_b32 m0, s37
	s_nop 2
	global_load_lds_dwordx4 v165, s[84:85]
	s_mov_b32 m0, s29
	s_addc_u32 s81, s85, 0
	s_mov_b32 s29, m0
	s_mov_b32 m0, s55
	s_nop 2
	global_load_lds_dwordx4 v163, s[80:81]
	s_mov_b32 m0, s29
	s_nop 0
	s_mov_b32 s29, m0
	s_mov_b32 m0, s77
	s_nop 2
	global_load_lds_dwordx4 v165, s[80:81]
	s_mov_b32 m0, s29
	s_nop 0
	s_mov_b32 s29, m0
	s_mov_b32 m0, s35
	s_nop 2
	global_load_lds_dwordx4 v162, s[86:87]
	s_mov_b32 m0, s29
	s_nop 0
	s_mov_b32 s29, m0
	s_mov_b32 m0, s88
	s_nop 2
	global_load_lds_dwordx4 v164, s[86:87]
	s_mov_b32 m0, s29
	s_waitcnt vmcnt(8)
	s_waitcnt lgkmcnt(0)
	s_barrier
	s_setprio 1
	v_mfma_f32_16x16x128_f8f6f4 v[94:97], v[18:25], v[176:183], 0
	v_mfma_f32_16x16x128_f8f6f4 v[90:93], v[26:33], v[176:183], 0
	v_mfma_f32_16x16x128_f8f6f4 v[82:85], v[18:25], v[184:191], 0
	v_mfma_f32_16x16x128_f8f6f4 v[74:77], v[26:33], v[184:191], 0
	v_mfma_f32_16x16x128_f8f6f4 v[66:69], v[18:25], v[192:199], 0
	v_mfma_f32_16x16x128_f8f6f4 v[58:61], v[26:33], v[192:199], 0
	v_mfma_f32_16x16x128_f8f6f4 v[50:53], v[18:25], v[200:207], 0
	v_mfma_f32_16x16x128_f8f6f4 v[42:45], v[26:33], v[200:207], 0
	v_mfma_f32_16x16x128_f8f6f4 v[86:89], v[2:9], v[176:183], 0
	v_mfma_f32_16x16x128_f8f6f4 v[78:81], v[10:17], v[176:183], 0
	v_mfma_f32_16x16x128_f8f6f4 v[70:73], v[2:9], v[184:191], 0
	v_mfma_f32_16x16x128_f8f6f4 v[62:65], v[10:17], v[184:191], 0
	v_mfma_f32_16x16x128_f8f6f4 v[54:57], v[2:9], v[192:199], 0
	v_mfma_f32_16x16x128_f8f6f4 v[46:49], v[10:17], v[192:199], 0
	v_mfma_f32_16x16x128_f8f6f4 v[38:41], v[2:9], v[200:207], 0
	v_mfma_f32_16x16x128_f8f6f4 v[34:37], v[10:17], v[200:207], 0
	s_setprio 0
	s_barrier
	s_branch .Lmid1

.Lpeel1046:
	ds_read_b128 v[136:139], v172
	ds_read_b128 v[140:143], v172 offset:1024
	ds_read_b128 v[144:147], v172 offset:2048
	ds_read_b128 v[148:151], v172 offset:3072
	ds_read_b128 v[152:155], v173
	ds_read_b128 v[156:159], v173 offset:1024
	ds_read_b128 v[160:163], v173 offset:2048
	ds_read_b128 v[178:181], v173 offset:3072
	s_add_u32 s25, s64, s56
	s_addc_u32 s33, s65, s57
	s_add_u32 s66, s25, 0x100
	s_addc_u32 s67, s33, 0
	s_add_u32 s23, s62, s56
	s_addc_u32 s24, s63, s57
	s_add_u32 s28, s23, 0x100
	s_addc_u32 s29, s24, 0
	s_add_u32 s58, s25, 0x180
	s_addc_u32 s59, s33, 0
	ds_read_b128 v[182:185], v174
	ds_read_b128 v[186:189], v174 offset:1024
	ds_read_b128 v[190:193], v174 offset:2048
	ds_read_b128 v[194:197], v174 offset:3072
	ds_read_b128 v[198:201], v174 offset:4096
	ds_read_b128 v[202:205], v174 offset:5120
	ds_read_b128 v[206:209], v174 offset:6144
	ds_read_b128 v[210:213], v174 offset:7168
	s_add_u32 s30, s25, 0x40080
	s_addc_u32 s31, s33, 0
	s_mov_b32 s36, m0
	s_mov_b32 m0, s26
	s_nop 2
	global_load_lds_dwordx4 v165, s[30:31]
	s_mov_b32 m0, s36
	s_nop 0
	s_mov_b32 s36, m0
	s_mov_b32 m0, s27
	s_nop 2
	global_load_lds_dwordx4 v167, s[30:31]
	s_mov_b32 m0, s36
	s_waitcnt vmcnt(8)
	s_waitcnt lgkmcnt(0)
	s_barrier
	s_setprio 1
	v_mfma_f32_16x16x32_bf16 v[26:29], v[136:139], v[182:185], 0
	v_mfma_f32_16x16x32_bf16 v[30:33], v[144:147], v[182:185], 0
	v_mfma_f32_16x16x32_bf16 v[50:53], v[136:139], v[190:193], 0
	v_mfma_f32_16x16x32_bf16 v[54:57], v[144:147], v[190:193], 0
	v_mfma_f32_16x16x32_bf16 v[74:77], v[136:139], v[198:201], 0
	v_mfma_f32_16x16x32_bf16 v[78:81], v[144:147], v[198:201], 0
	v_mfma_f32_16x16x32_bf16 v[94:97], v[136:139], v[206:209], 0
	v_mfma_f32_16x16x32_bf16 v[102:105], v[144:147], v[206:209], 0
	v_mfma_f32_16x16x32_bf16 v[26:29], v[140:143], v[186:189], v[26:29]
	v_mfma_f32_16x16x32_bf16 v[30:33], v[148:151], v[186:189], v[30:33]
	v_mfma_f32_16x16x32_bf16 v[50:53], v[140:143], v[194:197], v[50:53]
	v_mfma_f32_16x16x32_bf16 v[54:57], v[148:151], v[194:197], v[54:57]
	v_mfma_f32_16x16x32_bf16 v[74:77], v[140:143], v[202:205], v[74:77]
	v_mfma_f32_16x16x32_bf16 v[78:81], v[148:151], v[202:205], v[78:81]
	v_mfma_f32_16x16x32_bf16 v[94:97], v[140:143], v[210:213], v[94:97]
	v_mfma_f32_16x16x32_bf16 v[102:105], v[148:151], v[210:213], v[102:105]
	v_mfma_f32_16x16x32_bf16 v[38:41], v[152:155], v[182:185], 0
	v_mfma_f32_16x16x32_bf16 v[42:45], v[160:163], v[182:185], 0
	v_mfma_f32_16x16x32_bf16 v[62:65], v[152:155], v[190:193], 0
	v_mfma_f32_16x16x32_bf16 v[66:69], v[160:163], v[190:193], 0
	v_mfma_f32_16x16x32_bf16 v[82:85], v[152:155], v[198:201], 0
	v_mfma_f32_16x16x32_bf16 v[90:93], v[160:163], v[198:201], 0
	v_mfma_f32_16x16x32_bf16 v[106:109], v[152:155], v[206:209], 0
	v_mfma_f32_16x16x32_bf16 v[114:117], v[160:163], v[206:209], 0
	v_mfma_f32_16x16x32_bf16 v[38:41], v[156:159], v[186:189], v[38:41]
	v_mfma_f32_16x16x32_bf16 v[42:45], v[178:181], v[186:189], v[42:45]
	v_mfma_f32_16x16x32_bf16 v[62:65], v[156:159], v[194:197], v[62:65]
	v_mfma_f32_16x16x32_bf16 v[66:69], v[178:181], v[194:197], v[66:69]
	v_mfma_f32_16x16x32_bf16 v[82:85], v[156:159], v[202:205], v[82:85]
	v_mfma_f32_16x16x32_bf16 v[90:93], v[178:181], v[202:205], v[90:93]
	v_mfma_f32_16x16x32_bf16 v[106:109], v[156:159], v[210:213], v[106:109]
	v_mfma_f32_16x16x32_bf16 v[114:117], v[178:181], v[210:213], v[114:117]
	s_setprio 0
	s_barrier
	ds_read_b128 v[182:185], v174 offset:16384
	ds_read_b128 v[186:189], v174 offset:17408
	ds_read_b128 v[190:193], v174 offset:18432
	ds_read_b128 v[194:197], v174 offset:19456
	ds_read_b128 v[198:201], v174 offset:20480
	ds_read_b128 v[202:205], v174 offset:21504
	ds_read_b128 v[206:209], v174 offset:22528
	ds_read_b128 v[210:213], v174 offset:23552
	s_mov_b32 s30, m0
	s_mov_b32 m0, s80
	s_nop 2
	global_load_lds_dwordx4 v166, s[28:29]
	s_mov_b32 m0, s30
	s_nop 0
	s_mov_b32 s30, m0
	s_mov_b32 m0, s81
	s_nop 2
	global_load_lds_dwordx4 v168, s[28:29]
	s_mov_b32 m0, s30
	s_add_u32 s28, s23, 0x40100
	s_addc_u32 s29, s24, 0
	s_mov_b32 s30, m0
	s_mov_b32 m0, s82
	s_nop 2
	global_load_lds_dwordx4 v166, s[28:29]
	s_mov_b32 m0, s30
	s_nop 0
	s_mov_b32 s30, m0
	s_mov_b32 m0, s83
	s_nop 2
	global_load_lds_dwordx4 v168, s[28:29]
	s_mov_b32 m0, s30
	s_mov_b32 s28, m0
	s_mov_b32 m0, s79
	s_nop 2
	global_load_lds_dwordx4 v165, s[66:67]
	s_mov_b32 m0, s28
	s_nop 0
	s_mov_b32 s28, m0
	s_mov_b32 m0, s84
	s_nop 2
	global_load_lds_dwordx4 v167, s[66:67]
	s_mov_b32 m0, s28
	s_waitcnt vmcnt(8)
	s_waitcnt lgkmcnt(0)
	s_barrier
	s_setprio 1
	v_mfma_f32_16x16x32_bf16 v[118:121], v[136:139], v[182:185], 0
	v_mfma_f32_16x16x32_bf16 v[126:129], v[144:147], v[182:185], 0
	v_mfma_f32_16x16x32_bf16 v[98:101], v[136:139], v[190:193], 0
	v_mfma_f32_16x16x32_bf16 v[86:89], v[144:147], v[190:193], 0
	v_mfma_f32_16x16x32_bf16 v[46:49], v[136:139], v[198:201], 0
	v_mfma_f32_16x16x32_bf16 v[34:37], v[144:147], v[198:201], 0
	v_mfma_f32_16x16x32_bf16 v[14:17], v[136:139], v[206:209], 0
	v_mfma_f32_16x16x32_bf16 v[10:13], v[144:147], v[206:209], 0
	v_mfma_f32_16x16x32_bf16 v[118:121], v[140:143], v[186:189], v[118:121]
	v_mfma_f32_16x16x32_bf16 v[126:129], v[148:151], v[186:189], v[126:129]
	v_mfma_f32_16x16x32_bf16 v[98:101], v[140:143], v[194:197], v[98:101]
	v_mfma_f32_16x16x32_bf16 v[86:89], v[148:151], v[194:197], v[86:89]
	v_mfma_f32_16x16x32_bf16 v[46:49], v[140:143], v[202:205], v[46:49]
	v_mfma_f32_16x16x32_bf16 v[34:37], v[148:151], v[202:205], v[34:37]
	v_mfma_f32_16x16x32_bf16 v[14:17], v[140:143], v[210:213], v[14:17]
	v_mfma_f32_16x16x32_bf16 v[10:13], v[148:151], v[210:213], v[10:13]
	v_mfma_f32_16x16x32_bf16 v[122:125], v[152:155], v[182:185], 0
	v_mfma_f32_16x16x32_bf16 v[110:113], v[160:163], v[182:185], 0
	v_mfma_f32_16x16x32_bf16 v[70:73], v[152:155], v[190:193], 0
	v_mfma_f32_16x16x32_bf16 v[58:61], v[160:163], v[190:193], 0
	v_mfma_f32_16x16x32_bf16 v[22:25], v[152:155], v[198:201], 0
	v_mfma_f32_16x16x32_bf16 v[18:21], v[160:163], v[198:201], 0
	v_mfma_f32_16x16x32_bf16 v[6:9], v[152:155], v[206:209], 0
	v_mfma_f32_16x16x32_bf16 v[2:5], v[160:163], v[206:209], 0
	v_mfma_f32_16x16x32_bf16 v[122:125], v[156:159], v[186:189], v[122:125]
	v_mfma_f32_16x16x32_bf16 v[110:113], v[178:181], v[186:189], v[110:113]
	v_mfma_f32_16x16x32_bf16 v[70:73], v[156:159], v[194:197], v[70:73]
	v_mfma_f32_16x16x32_bf16 v[58:61], v[178:181], v[194:197], v[58:61]
	v_mfma_f32_16x16x32_bf16 v[22:25], v[156:159], v[202:205], v[22:25]
	v_mfma_f32_16x16x32_bf16 v[18:21], v[178:181], v[202:205], v[18:21]
	v_mfma_f32_16x16x32_bf16 v[6:9], v[156:159], v[210:213], v[6:9]
	v_mfma_f32_16x16x32_bf16 v[2:5], v[178:181], v[210:213], v[2:5]
	s_setprio 0
	s_barrier
	s_branch .Lmid1046
.LBB0_1046:
	ds_read_b128 v[136:139], v172
	ds_read_b128 v[140:143], v172 offset:1024
	ds_read_b128 v[144:147], v172 offset:2048
	ds_read_b128 v[148:151], v172 offset:3072
	ds_read_b128 v[152:155], v173
	ds_read_b128 v[156:159], v173 offset:1024
	ds_read_b128 v[160:163], v173 offset:2048
	ds_read_b128 v[178:181], v173 offset:3072
	s_add_u32 s25, s64, s56
	s_addc_u32 s33, s65, s57
	s_add_u32 s66, s25, 0x100
	s_addc_u32 s67, s33, 0
	s_add_u32 s23, s62, s56
	s_addc_u32 s24, s63, s57
	s_add_u32 s28, s23, 0x100
	s_addc_u32 s29, s24, 0
	s_add_u32 s58, s25, 0x180
	s_addc_u32 s59, s33, 0
	ds_read_b128 v[182:185], v174
	ds_read_b128 v[186:189], v174 offset:1024
	ds_read_b128 v[190:193], v174 offset:2048
	ds_read_b128 v[194:197], v174 offset:3072
	ds_read_b128 v[198:201], v174 offset:4096
	ds_read_b128 v[202:205], v174 offset:5120
	ds_read_b128 v[206:209], v174 offset:6144
	ds_read_b128 v[210:213], v174 offset:7168
	s_add_u32 s30, s25, 0x40080
	s_addc_u32 s31, s33, 0
	s_mov_b32 s36, m0
	s_mov_b32 m0, s26
	s_nop 2
	global_load_lds_dwordx4 v165, s[30:31]
	s_mov_b32 m0, s36
	s_nop 0
	s_mov_b32 s36, m0
	s_mov_b32 m0, s27
	s_nop 2
	global_load_lds_dwordx4 v167, s[30:31]
	s_mov_b32 m0, s36
	s_waitcnt vmcnt(8)
	s_waitcnt lgkmcnt(0)
	s_barrier
	s_setprio 1
	v_mfma_f32_16x16x32_bf16 v[26:29], v[136:139], v[182:185], v[26:29]
	v_mfma_f32_16x16x32_bf16 v[30:33], v[144:147], v[182:185], v[30:33]
	v_mfma_f32_16x16x32_bf16 v[50:53], v[136:139], v[190:193], v[50:53]
	v_mfma_f32_16x16x32_bf16 v[54:57], v[144:147], v[190:193], v[54:57]
	v_mfma_f32_16x16x32_bf16 v[74:77], v[136:139], v[198:201], v[74:77]
	v_mfma_f32_16x16x32_bf16 v[78:81], v[144:147], v[198:201], v[78:81]
	v_mfma_f32_16x16x32_bf16 v[94:97], v[136:139], v[206:209], v[94:97]
	v_mfma_f32_16x16x32_bf16 v[102:105], v[144:147], v[206:209], v[102:105]
	v_mfma_f32_16x16x32_bf16 v[26:29], v[140:143], v[186:189], v[26:29]
	v_mfma_f32_16x16x32_bf16 v[30:33], v[148:151], v[186:189], v[30:33]
	v_mfma_f32_16x16x32_bf16 v[50:53], v[140:143], v[194:197], v[50:53]
	v_mfma_f32_16x16x32_bf16 v[54:57], v[148:151], v[194:197], v[54:57]
	v_mfma_f32_16x16x32_bf16 v[74:77], v[140:143], v[202:205], v[74:77]
	v_mfma_f32_16x16x32_bf16 v[78:81], v[148:151], v[202:205], v[78:81]
	v_mfma_f32_16x16x32_bf16 v[94:97], v[140:143], v[210:213], v[94:97]
	v_mfma_f32_16x16x32_bf16 v[102:105], v[148:151], v[210:213], v[102:105]
	v_mfma_f32_16x16x32_bf16 v[38:41], v[152:155], v[182:185], v[38:41]
	v_mfma_f32_16x16x32_bf16 v[42:45], v[160:163], v[182:185], v[42:45]
	v_mfma_f32_16x16x32_bf16 v[62:65], v[152:155], v[190:193], v[62:65]
	v_mfma_f32_16x16x32_bf16 v[66:69], v[160:163], v[190:193], v[66:69]
	v_mfma_f32_16x16x32_bf16 v[82:85], v[152:155], v[198:201], v[82:85]
	v_mfma_f32_16x16x32_bf16 v[90:93], v[160:163], v[198:201], v[90:93]
	v_mfma_f32_16x16x32_bf16 v[106:109], v[152:155], v[206:209], v[106:109]
	v_mfma_f32_16x16x32_bf16 v[114:117], v[160:163], v[206:209], v[114:117]
	v_mfma_f32_16x16x32_bf16 v[38:41], v[156:159], v[186:189], v[38:41]
	v_mfma_f32_16x16x32_bf16 v[42:45], v[178:181], v[186:189], v[42:45]
	v_mfma_f32_16x16x32_bf16 v[62:65], v[156:159], v[194:197], v[62:65]
	v_mfma_f32_16x16x32_bf16 v[66:69], v[178:181], v[194:197], v[66:69]
	v_mfma_f32_16x16x32_bf16 v[82:85], v[156:159], v[202:205], v[82:85]
	v_mfma_f32_16x16x32_bf16 v[90:93], v[178:181], v[202:205], v[90:93]
	v_mfma_f32_16x16x32_bf16 v[106:109], v[156:159], v[210:213], v[106:109]
	v_mfma_f32_16x16x32_bf16 v[114:117], v[178:181], v[210:213], v[114:117]
	s_setprio 0
	s_barrier
	ds_read_b128 v[182:185], v174 offset:16384
	ds_read_b128 v[186:189], v174 offset:17408
	ds_read_b128 v[190:193], v174 offset:18432
	ds_read_b128 v[194:197], v174 offset:19456
	ds_read_b128 v[198:201], v174 offset:20480
	ds_read_b128 v[202:205], v174 offset:21504
	ds_read_b128 v[206:209], v174 offset:22528
	ds_read_b128 v[210:213], v174 offset:23552
	s_mov_b32 s30, m0
	s_mov_b32 m0, s80
	s_nop 2
	global_load_lds_dwordx4 v166, s[28:29]
	s_mov_b32 m0, s30
	s_nop 0
	s_mov_b32 s30, m0
	s_mov_b32 m0, s81
	s_nop 2
	global_load_lds_dwordx4 v168, s[28:29]
	s_mov_b32 m0, s30
	s_add_u32 s28, s23, 0x40100
	s_addc_u32 s29, s24, 0
	s_mov_b32 s30, m0
	s_mov_b32 m0, s82
	s_nop 2
	global_load_lds_dwordx4 v166, s[28:29]
	s_mov_b32 m0, s30
	s_nop 0
	s_mov_b32 s30, m0
	s_mov_b32 m0, s83
	s_nop 2
	global_load_lds_dwordx4 v168, s[28:29]
	s_mov_b32 m0, s30
	s_mov_b32 s28, m0
	s_mov_b32 m0, s79
	s_nop 2
	global_load_lds_dwordx4 v165, s[66:67]
	s_mov_b32 m0, s28
	s_nop 0
	s_mov_b32 s28, m0
	s_mov_b32 m0, s84
	s_nop 2
	global_load_lds_dwordx4 v167, s[66:67]
	s_mov_b32 m0, s28
	s_waitcnt vmcnt(8)
	s_waitcnt lgkmcnt(0)
	s_barrier
	s_setprio 1
	v_mfma_f32_16x16x32_bf16 v[118:121], v[136:139], v[182:185], v[118:121]
	v_mfma_f32_16x16x32_bf16 v[126:129], v[144:147], v[182:185], v[126:129]
	v_mfma_f32_16x16x32_bf16 v[98:101], v[136:139], v[190:193], v[98:101]
	v_mfma_f32_16x16x32_bf16 v[86:89], v[144:147], v[190:193], v[86:89]
	v_mfma_f32_16x16x32_bf16 v[46:49], v[136:139], v[198:201], v[46:49]
	v_mfma_f32_16x16x32_bf16 v[34:37], v[144:147], v[198:201], v[34:37]
	v_mfma_f32_16x16x32_bf16 v[14:17], v[136:139], v[206:209], v[14:17]
	v_mfma_f32_16x16x32_bf16 v[10:13], v[144:147], v[206:209], v[10:13]
	v_mfma_f32_16x16x32_bf16 v[118:121], v[140:143], v[186:189], v[118:121]
	v_mfma_f32_16x16x32_bf16 v[126:129], v[148:151], v[186:189], v[126:129]
	v_mfma_f32_16x16x32_bf16 v[98:101], v[140:143], v[194:197], v[98:101]
	v_mfma_f32_16x16x32_bf16 v[86:89], v[148:151], v[194:197], v[86:89]
	v_mfma_f32_16x16x32_bf16 v[46:49], v[140:143], v[202:205], v[46:49]
	v_mfma_f32_16x16x32_bf16 v[34:37], v[148:151], v[202:205], v[34:37]
	v_mfma_f32_16x16x32_bf16 v[14:17], v[140:143], v[210:213], v[14:17]
	v_mfma_f32_16x16x32_bf16 v[10:13], v[148:151], v[210:213], v[10:13]
	v_mfma_f32_16x16x32_bf16 v[122:125], v[152:155], v[182:185], v[122:125]
	v_mfma_f32_16x16x32_bf16 v[110:113], v[160:163], v[182:185], v[110:113]
	v_mfma_f32_16x16x32_bf16 v[70:73], v[152:155], v[190:193], v[70:73]
	v_mfma_f32_16x16x32_bf16 v[58:61], v[160:163], v[190:193], v[58:61]
	v_mfma_f32_16x16x32_bf16 v[22:25], v[152:155], v[198:201], v[22:25]
	v_mfma_f32_16x16x32_bf16 v[18:21], v[160:163], v[198:201], v[18:21]
	v_mfma_f32_16x16x32_bf16 v[6:9], v[152:155], v[206:209], v[6:9]
	v_mfma_f32_16x16x32_bf16 v[2:5], v[160:163], v[206:209], v[2:5]
	v_mfma_f32_16x16x32_bf16 v[122:125], v[156:159], v[186:189], v[122:125]
	v_mfma_f32_16x16x32_bf16 v[110:113], v[178:181], v[186:189], v[110:113]
	v_mfma_f32_16x16x32_bf16 v[70:73], v[156:159], v[194:197], v[70:73]
	v_mfma_f32_16x16x32_bf16 v[58:61], v[178:181], v[194:197], v[58:61]
	v_mfma_f32_16x16x32_bf16 v[22:25], v[156:159], v[202:205], v[22:25]
	v_mfma_f32_16x16x32_bf16 v[18:21], v[178:181], v[202:205], v[18:21]
	v_mfma_f32_16x16x32_bf16 v[6:9], v[156:159], v[210:213], v[6:9]
	v_mfma_f32_16x16x32_bf16 v[2:5], v[178:181], v[210:213], v[2:5]
	s_setprio 0
	s_barrier
.Lmid1046:
	ds_read_b128 v[136:139], v175
	ds_read_b128 v[140:143], v175 offset:1024
	ds_read_b128 v[144:147], v175 offset:2048
	ds_read_b128 v[148:151], v175 offset:3072
	ds_read_b128 v[152:155], v176
	ds_read_b128 v[156:159], v176 offset:1024
	ds_read_b128 v[160:163], v176 offset:2048
	ds_read_b128 v[178:181], v176 offset:3072
	ds_read_b128 v[182:185], v174 offset:32768
	ds_read_b128 v[186:189], v174 offset:33792
	ds_read_b128 v[190:193], v174 offset:34816
	ds_read_b128 v[194:197], v174 offset:35840
	ds_read_b128 v[198:201], v174 offset:36864
	ds_read_b128 v[202:205], v174 offset:37888
	ds_read_b128 v[206:209], v174 offset:38912
	ds_read_b128 v[210:213], v174 offset:39936
	s_add_u32 s28, s25, 0x40100
	s_addc_u32 s29, s33, 0
	s_mov_b32 s25, m0
	s_mov_b32 m0, s85
	s_nop 2
	global_load_lds_dwordx4 v165, s[28:29]
	s_mov_b32 m0, s25
	s_nop 0
	s_mov_b32 s25, m0
	s_mov_b32 m0, s86
	s_nop 2
	global_load_lds_dwordx4 v167, s[28:29]
	s_mov_b32 m0, s25
	s_waitcnt vmcnt(8)
	s_waitcnt lgkmcnt(0)
	s_barrier
	s_setprio 1
	v_mfma_f32_16x16x32_bf16 v[26:29], v[136:139], v[182:185], v[26:29]
	v_mfma_f32_16x16x32_bf16 v[30:33], v[144:147], v[182:185], v[30:33]
	v_mfma_f32_16x16x32_bf16 v[50:53], v[136:139], v[190:193], v[50:53]
	v_mfma_f32_16x16x32_bf16 v[54:57], v[144:147], v[190:193], v[54:57]
	v_mfma_f32_16x16x32_bf16 v[74:77], v[136:139], v[198:201], v[74:77]
	v_mfma_f32_16x16x32_bf16 v[78:81], v[144:147], v[198:201], v[78:81]
	v_mfma_f32_16x16x32_bf16 v[94:97], v[136:139], v[206:209], v[94:97]
	v_mfma_f32_16x16x32_bf16 v[102:105], v[144:147], v[206:209], v[102:105]
	v_mfma_f32_16x16x32_bf16 v[26:29], v[140:143], v[186:189], v[26:29]
	v_mfma_f32_16x16x32_bf16 v[30:33], v[148:151], v[186:189], v[30:33]
	v_mfma_f32_16x16x32_bf16 v[50:53], v[140:143], v[194:197], v[50:53]
	v_mfma_f32_16x16x32_bf16 v[54:57], v[148:151], v[194:197], v[54:57]
	v_mfma_f32_16x16x32_bf16 v[74:77], v[140:143], v[202:205], v[74:77]
	v_mfma_f32_16x16x32_bf16 v[78:81], v[148:151], v[202:205], v[78:81]
	v_mfma_f32_16x16x32_bf16 v[94:97], v[140:143], v[210:213], v[94:97]
	v_mfma_f32_16x16x32_bf16 v[102:105], v[148:151], v[210:213], v[102:105]
	v_mfma_f32_16x16x32_bf16 v[38:41], v[152:155], v[182:185], v[38:41]
	v_mfma_f32_16x16x32_bf16 v[42:45], v[160:163], v[182:185], v[42:45]
	v_mfma_f32_16x16x32_bf16 v[62:65], v[152:155], v[190:193], v[62:65]
	v_mfma_f32_16x16x32_bf16 v[66:69], v[160:163], v[190:193], v[66:69]
	v_mfma_f32_16x16x32_bf16 v[82:85], v[152:155], v[198:201], v[82:85]
	v_mfma_f32_16x16x32_bf16 v[90:93], v[160:163], v[198:201], v[90:93]
	v_mfma_f32_16x16x32_bf16 v[106:109], v[152:155], v[206:209], v[106:109]
	v_mfma_f32_16x16x32_bf16 v[114:117], v[160:163], v[206:209], v[114:117]
	v_mfma_f32_16x16x32_bf16 v[38:41], v[156:159], v[186:189], v[38:41]
	v_mfma_f32_16x16x32_bf16 v[42:45], v[178:181], v[186:189], v[42:45]
	v_mfma_f32_16x16x32_bf16 v[62:65], v[156:159], v[194:197], v[62:65]
	v_mfma_f32_16x16x32_bf16 v[66:69], v[178:181], v[194:197], v[66:69]
	v_mfma_f32_16x16x32_bf16 v[82:85], v[156:159], v[202:205], v[82:85]
	v_mfma_f32_16x16x32_bf16 v[90:93], v[178:181], v[202:205], v[90:93]
	v_mfma_f32_16x16x32_bf16 v[106:109], v[156:159], v[210:213], v[106:109]
	v_mfma_f32_16x16x32_bf16 v[114:117], v[178:181], v[210:213], v[114:117]
	s_setprio 0
	s_barrier
	ds_read_b128 v[182:185], v174 offset:49152
	ds_read_b128 v[186:189], v174 offset:50176
	ds_read_b128 v[190:193], v174 offset:51200
	ds_read_b128 v[194:197], v174 offset:52224
	ds_read_b128 v[198:201], v174 offset:53248
	ds_read_b128 v[202:205], v174 offset:54272
	ds_read_b128 v[206:209], v174 offset:55296
	ds_read_b128 v[210:213], v174 offset:56320
	s_add_u32 s28, s23, 0x180
	s_addc_u32 s29, s24, 0
	s_mov_b32 s25, m0
	s_mov_b32 m0, s92
	s_nop 2
	global_load_lds_dwordx4 v166, s[28:29]
	s_mov_b32 m0, s25
	s_nop 0
	s_mov_b32 s25, m0
	s_mov_b32 m0, s93
	s_nop 2
	global_load_lds_dwordx4 v168, s[28:29]
	s_mov_b32 m0, s25
	s_add_u32 s28, s23, 0x40180
	s_addc_u32 s29, s24, 0
	s_mov_b32 s23, m0
	s_mov_b32 m0, s96
	s_nop 2
	global_load_lds_dwordx4 v166, s[28:29]
	s_mov_b32 m0, s23
	s_nop 0
	s_mov_b32 s23, m0
	s_mov_b32 m0, s97
	s_nop 2
	global_load_lds_dwordx4 v168, s[28:29]
	s_mov_b32 m0, s23
	s_nop 0
	s_mov_b32 s23, m0
	s_mov_b32 m0, s94
	s_nop 2
	global_load_lds_dwordx4 v165, s[58:59]
	s_mov_b32 m0, s23
	s_nop 0
	s_mov_b32 s23, m0
	s_mov_b32 m0, s95
	s_nop 2
	global_load_lds_dwordx4 v167, s[58:59]
	s_mov_b32 m0, s23
	s_waitcnt vmcnt(8)
	s_waitcnt lgkmcnt(0)
	s_barrier
	s_setprio 1
	v_mfma_f32_16x16x32_bf16 v[118:121], v[136:139], v[182:185], v[118:121]
	v_mfma_f32_16x16x32_bf16 v[126:129], v[144:147], v[182:185], v[126:129]
	v_mfma_f32_16x16x32_bf16 v[98:101], v[136:139], v[190:193], v[98:101]
	v_mfma_f32_16x16x32_bf16 v[86:89], v[144:147], v[190:193], v[86:89]
	v_mfma_f32_16x16x32_bf16 v[46:49], v[136:139], v[198:201], v[46:49]
	v_mfma_f32_16x16x32_bf16 v[34:37], v[144:147], v[198:201], v[34:37]
	v_mfma_f32_16x16x32_bf16 v[14:17], v[136:139], v[206:209], v[14:17]
	v_mfma_f32_16x16x32_bf16 v[10:13], v[144:147], v[206:209], v[10:13]
	v_mfma_f32_16x16x32_bf16 v[118:121], v[140:143], v[186:189], v[118:121]
	v_mfma_f32_16x16x32_bf16 v[126:129], v[148:151], v[186:189], v[126:129]
	v_mfma_f32_16x16x32_bf16 v[98:101], v[140:143], v[194:197], v[98:101]
	v_mfma_f32_16x16x32_bf16 v[86:89], v[148:151], v[194:197], v[86:89]
	v_mfma_f32_16x16x32_bf16 v[46:49], v[140:143], v[202:205], v[46:49]
	v_mfma_f32_16x16x32_bf16 v[34:37], v[148:151], v[202:205], v[34:37]
	v_mfma_f32_16x16x32_bf16 v[14:17], v[140:143], v[210:213], v[14:17]
	v_mfma_f32_16x16x32_bf16 v[10:13], v[148:151], v[210:213], v[10:13]
	v_mfma_f32_16x16x32_bf16 v[122:125], v[152:155], v[182:185], v[122:125]
	v_mfma_f32_16x16x32_bf16 v[110:113], v[160:163], v[182:185], v[110:113]
	v_mfma_f32_16x16x32_bf16 v[70:73], v[152:155], v[190:193], v[70:73]
	v_mfma_f32_16x16x32_bf16 v[58:61], v[160:163], v[190:193], v[58:61]
	v_mfma_f32_16x16x32_bf16 v[22:25], v[152:155], v[198:201], v[22:25]
	v_mfma_f32_16x16x32_bf16 v[18:21], v[160:163], v[198:201], v[18:21]
	v_mfma_f32_16x16x32_bf16 v[6:9], v[152:155], v[206:209], v[6:9]
	v_mfma_f32_16x16x32_bf16 v[2:5], v[160:163], v[206:209], v[2:5]
	v_mfma_f32_16x16x32_bf16 v[122:125], v[156:159], v[186:189], v[122:125]
	v_mfma_f32_16x16x32_bf16 v[110:113], v[178:181], v[186:189], v[110:113]
	v_mfma_f32_16x16x32_bf16 v[70:73], v[156:159], v[194:197], v[70:73]
	v_mfma_f32_16x16x32_bf16 v[58:61], v[178:181], v[194:197], v[58:61]
	v_mfma_f32_16x16x32_bf16 v[22:25], v[156:159], v[202:205], v[22:25]
	v_mfma_f32_16x16x32_bf16 v[18:21], v[178:181], v[202:205], v[18:21]
	v_mfma_f32_16x16x32_bf16 v[6:9], v[156:159], v[210:213], v[6:9]
	v_mfma_f32_16x16x32_bf16 v[2:5], v[178:181], v[210:213], v[2:5]
	s_setprio 0
	s_barrier
	s_add_i32 s3, s3, 2
	s_add_u32 s56, s56, 0x100
	s_addc_u32 s57, s57, 0
	s_cmp_gt_u32 s3, 5
	s_cbranch_scc0 .LBB0_1046
	s_ashr_i32 s55, s54, 31
	s_lshl_b64 s[24:25], s[54:55], 19
	s_add_u32 s56, s69, s24
	s_addc_u32 s57, s76, s25
	s_ashr_i32 s23, s22, 31
	s_lshl_b64 s[24:25], s[22:23], 19
	s_add_u32 s58, s77, s24
	s_addc_u32 s59, s78, s25
	s_lshl_b32 s3, s60, 18
	s_lshl_b32 s23, s2, 8
	s_lshl_b32 s32, s2, 16
	s_add_i32 s2, s32, s3
	v_lshrrev_b32_e32 v214, 6, v0
	v_lshlrev_b32_e32 v214, 13, v214
	v_and_b32_e32 v215, 63, v0
	v_lshl_add_u32 v214, v215, 3, v214
	v_add_u32_e32 v134, s2, v214
	s_cmp_lg_u32 s37, 0
	s_cbranch_scc1 .Lmpf_have
	global_load_dwordx2 v[162:163], v134, s[14:15]
	global_load_dwordx2 v[178:179], v134, s[16:17]
	v_or_b32_e32 v136, 0x200, v134
	v_add_u32_e32 v137, 0x400, v134
	v_add_u32_e32 v138, 0x600, v134
	v_add_u32_e32 v139, 0x800, v134
	v_add_u32_e32 v140, 0xa00, v134
	v_add_u32_e32 v141, 0xc00, v134
	v_add_u32_e32 v161, 0xe00, v134
	global_load_dwordx2 v[180:181], v136, s[14:15]
	global_load_dwordx2 v[182:183], v136, s[16:17]
	global_load_dwordx2 v[158:159], v137, s[14:15]
	global_load_dwordx2 v[156:157], v137, s[16:17]
	global_load_dwordx2 v[154:155], v138, s[14:15]
	global_load_dwordx2 v[152:153], v138, s[16:17]
	global_load_dwordx2 v[150:151], v139, s[14:15]
	global_load_dwordx2 v[148:149], v139, s[16:17]
	global_load_dwordx2 v[146:147], v140, s[14:15]
	global_load_dwordx2 v[144:145], v140, s[16:17]
	global_load_dwordx2 v[142:143], v141, s[14:15]
	s_nop 0
	global_load_dwordx2 v[140:141], v141, s[16:17]
	s_nop 0
	global_load_dwordx2 v[138:139], v161, s[14:15]
	global_load_dwordx2 v[136:137], v161, s[16:17]
	s_branch .Lmpf_join

.LBB0_1048:
	ds_read_b128 v[136:139], v172
	ds_read_b128 v[140:143], v172 offset:1024
	ds_read_b128 v[144:147], v172 offset:2048
	ds_read_b128 v[148:151], v172 offset:3072
	ds_read_b128 v[152:155], v173
	ds_read_b128 v[156:159], v173 offset:1024
	ds_read_b128 v[160:163], v173 offset:2048
	ds_read_b128 v[178:181], v173 offset:3072
	s_cmp_eq_u32 s33, 12
	s_cselect_b32 s66, s3, s28
	s_cselect_b32 s67, s2, s29
	s_cselect_b32 s64, s25, s30
	s_cselect_b32 s65, s24, s31
	s_add_u32 s62, s66, 0x80
	s_addc_u32 s63, s67, 0
	ds_read_b128 v[182:185], v174
	ds_read_b128 v[186:189], v174 offset:1024
	ds_read_b128 v[190:193], v174 offset:2048
	ds_read_b128 v[194:197], v174 offset:3072
	ds_read_b128 v[198:201], v174 offset:4096
	ds_read_b128 v[202:205], v174 offset:5120
	ds_read_b128 v[206:209], v174 offset:6144
	ds_read_b128 v[210:213], v174 offset:7168
	s_add_u32 s36, s28, 0x3ff80
	s_addc_u32 s37, s29, 0
	s_mov_b32 s52, m0
	s_mov_b32 m0, s26
	s_nop 2
	global_load_lds_dwordx4 v165, s[36:37]
	s_mov_b32 m0, s52
	s_nop 0
	s_mov_b32 s52, m0
	s_mov_b32 m0, s27
	s_nop 2
	global_load_lds_dwordx4 v167, s[36:37]
	s_mov_b32 m0, s52
	s_waitcnt vmcnt(8)
	s_waitcnt lgkmcnt(0)
	s_barrier
	s_setprio 1
	v_mfma_f32_16x16x32_bf16 v[26:29], v[136:139], v[182:185], v[26:29]
	v_mfma_f32_16x16x32_bf16 v[30:33], v[144:147], v[182:185], v[30:33]
	v_mfma_f32_16x16x32_bf16 v[50:53], v[136:139], v[190:193], v[50:53]
	v_mfma_f32_16x16x32_bf16 v[54:57], v[144:147], v[190:193], v[54:57]
	v_mfma_f32_16x16x32_bf16 v[74:77], v[136:139], v[198:201], v[74:77]
	v_mfma_f32_16x16x32_bf16 v[78:81], v[144:147], v[198:201], v[78:81]
	v_mfma_f32_16x16x32_bf16 v[94:97], v[136:139], v[206:209], v[94:97]
	v_mfma_f32_16x16x32_bf16 v[102:105], v[144:147], v[206:209], v[102:105]
	v_mfma_f32_16x16x32_bf16 v[26:29], v[140:143], v[186:189], v[26:29]
	v_mfma_f32_16x16x32_bf16 v[30:33], v[148:151], v[186:189], v[30:33]
	v_mfma_f32_16x16x32_bf16 v[50:53], v[140:143], v[194:197], v[50:53]
	v_mfma_f32_16x16x32_bf16 v[54:57], v[148:151], v[194:197], v[54:57]
	v_mfma_f32_16x16x32_bf16 v[74:77], v[140:143], v[202:205], v[74:77]
	v_mfma_f32_16x16x32_bf16 v[78:81], v[148:151], v[202:205], v[78:81]
	v_mfma_f32_16x16x32_bf16 v[94:97], v[140:143], v[210:213], v[94:97]
	v_mfma_f32_16x16x32_bf16 v[102:105], v[148:151], v[210:213], v[102:105]
	v_mfma_f32_16x16x32_bf16 v[38:41], v[152:155], v[182:185], v[38:41]
	v_mfma_f32_16x16x32_bf16 v[42:45], v[160:163], v[182:185], v[42:45]
	v_mfma_f32_16x16x32_bf16 v[62:65], v[152:155], v[190:193], v[62:65]
	v_mfma_f32_16x16x32_bf16 v[66:69], v[160:163], v[190:193], v[66:69]
	v_mfma_f32_16x16x32_bf16 v[82:85], v[152:155], v[198:201], v[82:85]
	v_mfma_f32_16x16x32_bf16 v[90:93], v[160:163], v[198:201], v[90:93]
	v_mfma_f32_16x16x32_bf16 v[106:109], v[152:155], v[206:209], v[106:109]
	v_mfma_f32_16x16x32_bf16 v[114:117], v[160:163], v[206:209], v[114:117]
	v_mfma_f32_16x16x32_bf16 v[38:41], v[156:159], v[186:189], v[38:41]
	v_mfma_f32_16x16x32_bf16 v[42:45], v[178:181], v[186:189], v[42:45]
	v_mfma_f32_16x16x32_bf16 v[62:65], v[156:159], v[194:197], v[62:65]
	v_mfma_f32_16x16x32_bf16 v[66:69], v[178:181], v[194:197], v[66:69]
	v_mfma_f32_16x16x32_bf16 v[82:85], v[156:159], v[202:205], v[82:85]
	v_mfma_f32_16x16x32_bf16 v[90:93], v[178:181], v[202:205], v[90:93]
	v_mfma_f32_16x16x32_bf16 v[106:109], v[156:159], v[210:213], v[106:109]
	v_mfma_f32_16x16x32_bf16 v[114:117], v[178:181], v[210:213], v[114:117]
	s_setprio 0
	s_barrier
	ds_read_b128 v[182:185], v174 offset:16384
	ds_read_b128 v[186:189], v174 offset:17408
	ds_read_b128 v[190:193], v174 offset:18432
	ds_read_b128 v[194:197], v174 offset:19456
	ds_read_b128 v[198:201], v174 offset:20480
	ds_read_b128 v[202:205], v174 offset:21504
	ds_read_b128 v[206:209], v174 offset:22528
	ds_read_b128 v[210:213], v174 offset:23552
	s_mov_b32 s36, m0
	s_mov_b32 m0, s80
	s_nop 2
	global_load_lds_dwordx4 v166, s[64:65]
	s_mov_b32 m0, s36
	s_nop 0
	s_mov_b32 s36, m0
	s_mov_b32 m0, s81
	s_nop 2
	global_load_lds_dwordx4 v168, s[64:65]
	s_mov_b32 m0, s36
	s_add_u32 s36, s64, 0x40000
	s_addc_u32 s37, s65, 0
	s_mov_b32 s52, m0
	s_mov_b32 m0, s82
	s_nop 2
	global_load_lds_dwordx4 v166, s[36:37]
	s_mov_b32 m0, s52
	s_nop 0
	s_mov_b32 s52, m0
	s_mov_b32 m0, s83
	s_nop 2
	global_load_lds_dwordx4 v168, s[36:37]
	s_mov_b32 m0, s52
	s_mov_b32 s36, m0
	s_mov_b32 m0, s79
	s_nop 2
	global_load_lds_dwordx4 v165, s[66:67]
	s_mov_b32 m0, s36
	s_nop 0
	s_mov_b32 s36, m0
	s_mov_b32 m0, s84
	s_nop 2
	global_load_lds_dwordx4 v167, s[66:67]
	s_mov_b32 m0, s36
	s_waitcnt vmcnt(8)
	s_waitcnt lgkmcnt(0)
	s_barrier
	s_setprio 1
	v_mfma_f32_16x16x32_bf16 v[118:121], v[136:139], v[182:185], v[118:121]
	v_mfma_f32_16x16x32_bf16 v[126:129], v[144:147], v[182:185], v[126:129]
	v_mfma_f32_16x16x32_bf16 v[98:101], v[136:139], v[190:193], v[98:101]
	v_mfma_f32_16x16x32_bf16 v[86:89], v[144:147], v[190:193], v[86:89]
	v_mfma_f32_16x16x32_bf16 v[46:49], v[136:139], v[198:201], v[46:49]
	v_mfma_f32_16x16x32_bf16 v[34:37], v[144:147], v[198:201], v[34:37]
	v_mfma_f32_16x16x32_bf16 v[14:17], v[136:139], v[206:209], v[14:17]
	v_mfma_f32_16x16x32_bf16 v[10:13], v[144:147], v[206:209], v[10:13]
	v_mfma_f32_16x16x32_bf16 v[118:121], v[140:143], v[186:189], v[118:121]
	v_mfma_f32_16x16x32_bf16 v[126:129], v[148:151], v[186:189], v[126:129]
	v_mfma_f32_16x16x32_bf16 v[98:101], v[140:143], v[194:197], v[98:101]
	v_mfma_f32_16x16x32_bf16 v[86:89], v[148:151], v[194:197], v[86:89]
	v_mfma_f32_16x16x32_bf16 v[46:49], v[140:143], v[202:205], v[46:49]
	v_mfma_f32_16x16x32_bf16 v[34:37], v[148:151], v[202:205], v[34:37]
	v_mfma_f32_16x16x32_bf16 v[14:17], v[140:143], v[210:213], v[14:17]
	v_mfma_f32_16x16x32_bf16 v[10:13], v[148:151], v[210:213], v[10:13]
	v_mfma_f32_16x16x32_bf16 v[122:125], v[152:155], v[182:185], v[122:125]
	v_mfma_f32_16x16x32_bf16 v[110:113], v[160:163], v[182:185], v[110:113]
	v_mfma_f32_16x16x32_bf16 v[70:73], v[152:155], v[190:193], v[70:73]
	v_mfma_f32_16x16x32_bf16 v[58:61], v[160:163], v[190:193], v[58:61]
	v_mfma_f32_16x16x32_bf16 v[22:25], v[152:155], v[198:201], v[22:25]
	v_mfma_f32_16x16x32_bf16 v[18:21], v[160:163], v[198:201], v[18:21]
	v_mfma_f32_16x16x32_bf16 v[6:9], v[152:155], v[206:209], v[6:9]
	v_mfma_f32_16x16x32_bf16 v[2:5], v[160:163], v[206:209], v[2:5]
	v_mfma_f32_16x16x32_bf16 v[122:125], v[156:159], v[186:189], v[122:125]
	v_mfma_f32_16x16x32_bf16 v[110:113], v[178:181], v[186:189], v[110:113]
	v_mfma_f32_16x16x32_bf16 v[70:73], v[156:159], v[194:197], v[70:73]
	v_mfma_f32_16x16x32_bf16 v[58:61], v[178:181], v[194:197], v[58:61]
	v_mfma_f32_16x16x32_bf16 v[22:25], v[156:159], v[202:205], v[22:25]
	v_mfma_f32_16x16x32_bf16 v[18:21], v[178:181], v[202:205], v[18:21]
	v_mfma_f32_16x16x32_bf16 v[6:9], v[156:159], v[210:213], v[6:9]
	v_mfma_f32_16x16x32_bf16 v[2:5], v[178:181], v[210:213], v[2:5]
	s_setprio 0
	s_barrier
	ds_read_b128 v[136:139], v175
	ds_read_b128 v[140:143], v175 offset:1024
	ds_read_b128 v[144:147], v175 offset:2048
	ds_read_b128 v[148:151], v175 offset:3072
	ds_read_b128 v[152:155], v176
	ds_read_b128 v[156:159], v176 offset:1024
	ds_read_b128 v[160:163], v176 offset:2048
	ds_read_b128 v[178:181], v176 offset:3072
	ds_read_b128 v[182:185], v174 offset:32768
	ds_read_b128 v[186:189], v174 offset:33792
	ds_read_b128 v[190:193], v174 offset:34816
	ds_read_b128 v[194:197], v174 offset:35840
	ds_read_b128 v[198:201], v174 offset:36864
	ds_read_b128 v[202:205], v174 offset:37888
	ds_read_b128 v[206:209], v174 offset:38912
	ds_read_b128 v[210:213], v174 offset:39936
	s_add_u32 s36, s66, 0x40000
	s_addc_u32 s37, s67, 0
	s_mov_b32 s52, m0
	s_mov_b32 m0, s85
	s_nop 2
	global_load_lds_dwordx4 v165, s[36:37]
	s_mov_b32 m0, s52
	s_nop 0
	s_mov_b32 s52, m0
	s_mov_b32 m0, s86
	s_nop 2
	global_load_lds_dwordx4 v167, s[36:37]
	s_mov_b32 m0, s52
	s_waitcnt vmcnt(8)
	s_waitcnt lgkmcnt(0)
	s_barrier
	s_setprio 1
	v_mfma_f32_16x16x32_bf16 v[26:29], v[136:139], v[182:185], v[26:29]
	v_mfma_f32_16x16x32_bf16 v[30:33], v[144:147], v[182:185], v[30:33]
	v_mfma_f32_16x16x32_bf16 v[50:53], v[136:139], v[190:193], v[50:53]
	v_mfma_f32_16x16x32_bf16 v[54:57], v[144:147], v[190:193], v[54:57]
	v_mfma_f32_16x16x32_bf16 v[74:77], v[136:139], v[198:201], v[74:77]
	v_mfma_f32_16x16x32_bf16 v[78:81], v[144:147], v[198:201], v[78:81]
	v_mfma_f32_16x16x32_bf16 v[94:97], v[136:139], v[206:209], v[94:97]
	v_mfma_f32_16x16x32_bf16 v[102:105], v[144:147], v[206:209], v[102:105]
	v_mfma_f32_16x16x32_bf16 v[26:29], v[140:143], v[186:189], v[26:29]
	v_mfma_f32_16x16x32_bf16 v[30:33], v[148:151], v[186:189], v[30:33]
	v_mfma_f32_16x16x32_bf16 v[50:53], v[140:143], v[194:197], v[50:53]
	v_mfma_f32_16x16x32_bf16 v[54:57], v[148:151], v[194:197], v[54:57]
	v_mfma_f32_16x16x32_bf16 v[74:77], v[140:143], v[202:205], v[74:77]
	v_mfma_f32_16x16x32_bf16 v[78:81], v[148:151], v[202:205], v[78:81]
	v_mfma_f32_16x16x32_bf16 v[94:97], v[140:143], v[210:213], v[94:97]
	v_mfma_f32_16x16x32_bf16 v[102:105], v[148:151], v[210:213], v[102:105]
	v_mfma_f32_16x16x32_bf16 v[38:41], v[152:155], v[182:185], v[38:41]
	v_mfma_f32_16x16x32_bf16 v[42:45], v[160:163], v[182:185], v[42:45]
	v_mfma_f32_16x16x32_bf16 v[62:65], v[152:155], v[190:193], v[62:65]
	v_mfma_f32_16x16x32_bf16 v[66:69], v[160:163], v[190:193], v[66:69]
	v_mfma_f32_16x16x32_bf16 v[82:85], v[152:155], v[198:201], v[82:85]
	v_mfma_f32_16x16x32_bf16 v[90:93], v[160:163], v[198:201], v[90:93]
	v_mfma_f32_16x16x32_bf16 v[106:109], v[152:155], v[206:209], v[106:109]
	v_mfma_f32_16x16x32_bf16 v[114:117], v[160:163], v[206:209], v[114:117]
	v_mfma_f32_16x16x32_bf16 v[38:41], v[156:159], v[186:189], v[38:41]
	v_mfma_f32_16x16x32_bf16 v[42:45], v[178:181], v[186:189], v[42:45]
	v_mfma_f32_16x16x32_bf16 v[62:65], v[156:159], v[194:197], v[62:65]
	v_mfma_f32_16x16x32_bf16 v[66:69], v[178:181], v[194:197], v[66:69]
	v_mfma_f32_16x16x32_bf16 v[82:85], v[156:159], v[202:205], v[82:85]
	v_mfma_f32_16x16x32_bf16 v[90:93], v[178:181], v[202:205], v[90:93]
	v_mfma_f32_16x16x32_bf16 v[106:109], v[156:159], v[210:213], v[106:109]
	v_mfma_f32_16x16x32_bf16 v[114:117], v[178:181], v[210:213], v[114:117]
	s_setprio 0
	s_barrier
	ds_read_b128 v[182:185], v174 offset:49152
	ds_read_b128 v[186:189], v174 offset:50176
	ds_read_b128 v[190:193], v174 offset:51200
	ds_read_b128 v[194:197], v174 offset:52224
	ds_read_b128 v[198:201], v174 offset:53248
	ds_read_b128 v[202:205], v174 offset:54272
	ds_read_b128 v[206:209], v174 offset:55296
	ds_read_b128 v[210:213], v174 offset:56320
	s_add_u32 s36, s64, 0x80
	s_addc_u32 s37, s65, 0
	s_mov_b32 s52, m0
	s_mov_b32 m0, s92
	s_nop 2
	global_load_lds_dwordx4 v166, s[36:37]
	s_mov_b32 m0, s52
	s_nop 0
	s_mov_b32 s52, m0
	s_mov_b32 m0, s93
	s_nop 2
	global_load_lds_dwordx4 v168, s[36:37]
	s_mov_b32 m0, s52
	s_add_u32 s36, s64, 0x40080
	s_addc_u32 s37, s65, 0
	s_mov_b32 s52, m0
	s_mov_b32 m0, s96
	s_nop 2
	global_load_lds_dwordx4 v166, s[36:37]
	s_mov_b32 m0, s52
	s_nop 0
	s_mov_b32 s52, m0
	s_mov_b32 m0, s97
	s_nop 2
	global_load_lds_dwordx4 v168, s[36:37]
	s_mov_b32 m0, s52
	s_mov_b32 s36, m0
	s_mov_b32 m0, s94
	s_nop 2
	global_load_lds_dwordx4 v165, s[62:63]
	s_mov_b32 m0, s36
	s_nop 0
	s_mov_b32 s36, m0
	s_mov_b32 m0, s95
	s_nop 2
	global_load_lds_dwordx4 v167, s[62:63]
	s_mov_b32 m0, s36
	s_waitcnt vmcnt(8)
	s_waitcnt lgkmcnt(0)
	s_barrier
	s_setprio 1
	v_mfma_f32_16x16x32_bf16 v[118:121], v[136:139], v[182:185], v[118:121]
	v_mfma_f32_16x16x32_bf16 v[126:129], v[144:147], v[182:185], v[126:129]
	v_mfma_f32_16x16x32_bf16 v[98:101], v[136:139], v[190:193], v[98:101]
	v_mfma_f32_16x16x32_bf16 v[86:89], v[144:147], v[190:193], v[86:89]
	v_mfma_f32_16x16x32_bf16 v[46:49], v[136:139], v[198:201], v[46:49]
	v_mfma_f32_16x16x32_bf16 v[34:37], v[144:147], v[198:201], v[34:37]
	v_mfma_f32_16x16x32_bf16 v[14:17], v[136:139], v[206:209], v[14:17]
	v_mfma_f32_16x16x32_bf16 v[10:13], v[144:147], v[206:209], v[10:13]
	v_mfma_f32_16x16x32_bf16 v[118:121], v[140:143], v[186:189], v[118:121]
	v_mfma_f32_16x16x32_bf16 v[126:129], v[148:151], v[186:189], v[126:129]
	v_mfma_f32_16x16x32_bf16 v[98:101], v[140:143], v[194:197], v[98:101]
	v_mfma_f32_16x16x32_bf16 v[86:89], v[148:151], v[194:197], v[86:89]
	v_mfma_f32_16x16x32_bf16 v[46:49], v[140:143], v[202:205], v[46:49]
	v_mfma_f32_16x16x32_bf16 v[34:37], v[148:151], v[202:205], v[34:37]
	v_mfma_f32_16x16x32_bf16 v[14:17], v[140:143], v[210:213], v[14:17]
	v_mfma_f32_16x16x32_bf16 v[10:13], v[148:151], v[210:213], v[10:13]
	v_mfma_f32_16x16x32_bf16 v[122:125], v[152:155], v[182:185], v[122:125]
	v_mfma_f32_16x16x32_bf16 v[110:113], v[160:163], v[182:185], v[110:113]
	v_mfma_f32_16x16x32_bf16 v[70:73], v[152:155], v[190:193], v[70:73]
	v_mfma_f32_16x16x32_bf16 v[58:61], v[160:163], v[190:193], v[58:61]
	v_mfma_f32_16x16x32_bf16 v[22:25], v[152:155], v[198:201], v[22:25]
	v_mfma_f32_16x16x32_bf16 v[18:21], v[160:163], v[198:201], v[18:21]
	v_mfma_f32_16x16x32_bf16 v[6:9], v[152:155], v[206:209], v[6:9]
	v_mfma_f32_16x16x32_bf16 v[2:5], v[160:163], v[206:209], v[2:5]
	v_mfma_f32_16x16x32_bf16 v[122:125], v[156:159], v[186:189], v[122:125]
	v_mfma_f32_16x16x32_bf16 v[110:113], v[178:181], v[186:189], v[110:113]
	v_mfma_f32_16x16x32_bf16 v[70:73], v[156:159], v[194:197], v[70:73]
	v_mfma_f32_16x16x32_bf16 v[58:61], v[178:181], v[194:197], v[58:61]
	v_mfma_f32_16x16x32_bf16 v[22:25], v[156:159], v[202:205], v[22:25]
	v_mfma_f32_16x16x32_bf16 v[18:21], v[178:181], v[202:205], v[18:21]
	v_mfma_f32_16x16x32_bf16 v[6:9], v[156:159], v[210:213], v[6:9]
	v_mfma_f32_16x16x32_bf16 v[2:5], v[178:181], v[210:213], v[2:5]
	s_setprio 0
	s_barrier
	s_add_i32 s33, s33, 2
	s_add_u32 s28, s28, 0x100
	s_addc_u32 s29, s29, 0
	s_add_u32 s30, s30, 0x100
	s_addc_u32 s31, s31, 0
	s_cmp_lt_u32 s33, 14
	s_cbranch_scc1 .LBB0_1048
	s_and_b64 vcc, exec, s[20:21]
	s_cbranch_vccz .LBB0_1051
	s_barrier

.Lpeel1440:
	ds_read_b128 v[130:133], v234
	ds_read_b128 v[134:137], v234 offset:1024
	ds_read_b128 v[138:141], v234 offset:2048
	ds_read_b128 v[142:145], v234 offset:3072
	ds_read_b128 v[146:149], v235
	ds_read_b128 v[150:153], v235 offset:1024
	ds_read_b128 v[154:157], v235 offset:2048
	ds_read_b128 v[158:161], v235 offset:3072
	s_add_u32 s60, s58, 0x100
	s_addc_u32 s61, s59, 0
	s_cmp_eq_u32 s87, 12
	s_cselect_b32 s66, s33, s60
	s_cselect_b32 s67, s21, s61
	s_cselect_b32 s64, s84, s85
	s_cselect_b32 s65, s19, s86
	s_add_u32 s62, s66, 0x80
	s_addc_u32 s63, s67, 0
	ds_read_b128 v[162:165], v236
	ds_read_b128 v[166:169], v236 offset:1024
	ds_read_b128 v[170:173], v236 offset:2048
	ds_read_b128 v[174:177], v236 offset:3072
	ds_read_b128 v[178:181], v236 offset:4096
	ds_read_b128 v[182:185], v236 offset:5120
	ds_read_b128 v[186:189], v236 offset:6144
	ds_read_b128 v[190:193], v236 offset:7168
	s_add_u32 s58, s58, 0x40080
	s_addc_u32 s59, s59, 0
	s_mov_b32 s88, m0
	s_mov_b32 m0, s80
	s_nop 2
	global_load_lds_dwordx4 v228, s[58:59]
	s_mov_b32 m0, s88
	s_nop 0
	s_mov_b32 s88, m0
	s_mov_b32 m0, s81
	s_nop 2
	global_load_lds_dwordx4 v230, s[58:59]
	s_mov_b32 m0, s88
	s_waitcnt vmcnt(8)
	s_waitcnt lgkmcnt(0)
	s_barrier
	s_setprio 1
	v_mfma_f32_16x16x32_bf16 v[126:129], v[130:133], v[162:165], 0
	v_mfma_f32_16x16x32_bf16 v[122:125], v[138:141], v[162:165], 0
	v_mfma_f32_16x16x32_bf16 v[114:117], v[130:133], v[170:173], 0
	v_mfma_f32_16x16x32_bf16 v[106:109], v[138:141], v[170:173], 0
	v_mfma_f32_16x16x32_bf16 v[94:97], v[130:133], v[178:181], 0
	v_mfma_f32_16x16x32_bf16 v[90:93], v[138:141], v[178:181], 0
	v_mfma_f32_16x16x32_bf16 v[86:89], v[130:133], v[186:189], 0
	v_mfma_f32_16x16x32_bf16 v[78:81], v[138:141], v[186:189], 0
	v_mfma_f32_16x16x32_bf16 v[126:129], v[134:137], v[166:169], v[126:129]
	v_mfma_f32_16x16x32_bf16 v[122:125], v[142:145], v[166:169], v[122:125]
	v_mfma_f32_16x16x32_bf16 v[114:117], v[134:137], v[174:177], v[114:117]
	v_mfma_f32_16x16x32_bf16 v[106:109], v[142:145], v[174:177], v[106:109]
	v_mfma_f32_16x16x32_bf16 v[94:97], v[134:137], v[182:185], v[94:97]
	v_mfma_f32_16x16x32_bf16 v[90:93], v[142:145], v[182:185], v[90:93]
	v_mfma_f32_16x16x32_bf16 v[86:89], v[134:137], v[190:193], v[86:89]
	v_mfma_f32_16x16x32_bf16 v[78:81], v[142:145], v[190:193], v[78:81]
	v_mfma_f32_16x16x32_bf16 v[118:121], v[146:149], v[162:165], 0
	v_mfma_f32_16x16x32_bf16 v[110:113], v[154:157], v[162:165], 0
	v_mfma_f32_16x16x32_bf16 v[102:105], v[146:149], v[170:173], 0
	v_mfma_f32_16x16x32_bf16 v[98:101], v[154:157], v[170:173], 0
	v_mfma_f32_16x16x32_bf16 v[82:85], v[146:149], v[178:181], 0
	v_mfma_f32_16x16x32_bf16 v[74:77], v[154:157], v[178:181], 0
	v_mfma_f32_16x16x32_bf16 v[70:73], v[146:149], v[186:189], 0
	v_mfma_f32_16x16x32_bf16 v[66:69], v[154:157], v[186:189], 0
	v_mfma_f32_16x16x32_bf16 v[118:121], v[150:153], v[166:169], v[118:121]
	v_mfma_f32_16x16x32_bf16 v[110:113], v[158:161], v[166:169], v[110:113]
	v_mfma_f32_16x16x32_bf16 v[102:105], v[150:153], v[174:177], v[102:105]
	v_mfma_f32_16x16x32_bf16 v[98:101], v[158:161], v[174:177], v[98:101]
	v_mfma_f32_16x16x32_bf16 v[82:85], v[150:153], v[182:185], v[82:85]
	v_mfma_f32_16x16x32_bf16 v[74:77], v[158:161], v[182:185], v[74:77]
	v_mfma_f32_16x16x32_bf16 v[70:73], v[150:153], v[190:193], v[70:73]
	v_mfma_f32_16x16x32_bf16 v[66:69], v[158:161], v[190:193], v[66:69]
	s_setprio 0
	s_barrier
	ds_read_b128 v[162:165], v236 offset:16384
	ds_read_b128 v[166:169], v236 offset:17408
	ds_read_b128 v[170:173], v236 offset:18432
	ds_read_b128 v[174:177], v236 offset:19456
	ds_read_b128 v[178:181], v236 offset:20480
	ds_read_b128 v[182:185], v236 offset:21504
	ds_read_b128 v[186:189], v236 offset:22528
	ds_read_b128 v[190:193], v236 offset:23552
	s_mov_b32 s58, m0
	s_mov_b32 m0, s30
	s_nop 2
	global_load_lds_dwordx4 v229, s[64:65]
	s_mov_b32 m0, s58
	s_nop 0
	s_mov_b32 s58, m0
	s_mov_b32 m0, s31
	s_nop 2
	global_load_lds_dwordx4 v231, s[64:65]
	s_mov_b32 m0, s58
	s_add_u32 s58, s64, 0x40000
	s_addc_u32 s59, s65, 0
	s_mov_b32 s88, m0
	s_mov_b32 m0, s34
	s_nop 2
	global_load_lds_dwordx4 v229, s[58:59]
	s_mov_b32 m0, s88
	s_nop 0
	s_mov_b32 s88, m0
	s_mov_b32 m0, s35
	s_nop 2
	global_load_lds_dwordx4 v231, s[58:59]
	s_mov_b32 m0, s88
	s_mov_b32 s58, m0
	s_mov_b32 m0, s28
	s_nop 2
	global_load_lds_dwordx4 v228, s[66:67]
	s_mov_b32 m0, s58
	s_nop 0
	s_mov_b32 s58, m0
	s_mov_b32 m0, s36
	s_nop 2
	global_load_lds_dwordx4 v230, s[66:67]
	s_mov_b32 m0, s58
	s_waitcnt vmcnt(8)
	s_waitcnt lgkmcnt(0)
	s_barrier
	s_setprio 1
	v_mfma_f32_16x16x32_bf16 v[62:65], v[130:133], v[162:165], 0
	v_mfma_f32_16x16x32_bf16 v[58:61], v[138:141], v[162:165], 0
	v_mfma_f32_16x16x32_bf16 v[54:57], v[130:133], v[170:173], 0
	v_mfma_f32_16x16x32_bf16 v[46:49], v[138:141], v[170:173], 0
	v_mfma_f32_16x16x32_bf16 v[38:41], v[130:133], v[178:181], 0
	v_mfma_f32_16x16x32_bf16 v[30:33], v[138:141], v[178:181], 0
	v_mfma_f32_16x16x32_bf16 v[22:25], v[130:133], v[186:189], 0
	v_mfma_f32_16x16x32_bf16 v[14:17], v[138:141], v[186:189], 0
	v_mfma_f32_16x16x32_bf16 v[62:65], v[134:137], v[166:169], v[62:65]
	v_mfma_f32_16x16x32_bf16 v[58:61], v[142:145], v[166:169], v[58:61]
	v_mfma_f32_16x16x32_bf16 v[54:57], v[134:137], v[174:177], v[54:57]
	v_mfma_f32_16x16x32_bf16 v[46:49], v[142:145], v[174:177], v[46:49]
	v_mfma_f32_16x16x32_bf16 v[38:41], v[134:137], v[182:185], v[38:41]
	v_mfma_f32_16x16x32_bf16 v[30:33], v[142:145], v[182:185], v[30:33]
	v_mfma_f32_16x16x32_bf16 v[22:25], v[134:137], v[190:193], v[22:25]
	v_mfma_f32_16x16x32_bf16 v[14:17], v[142:145], v[190:193], v[14:17]
	v_mfma_f32_16x16x32_bf16 v[50:53], v[146:149], v[162:165], 0
	v_mfma_f32_16x16x32_bf16 v[42:45], v[154:157], v[162:165], 0
	v_mfma_f32_16x16x32_bf16 v[34:37], v[146:149], v[170:173], 0
	v_mfma_f32_16x16x32_bf16 v[26:29], v[154:157], v[170:173], 0
	v_mfma_f32_16x16x32_bf16 v[18:21], v[146:149], v[178:181], 0
	v_mfma_f32_16x16x32_bf16 v[10:13], v[154:157], v[178:181], 0
	v_mfma_f32_16x16x32_bf16 v[6:9], v[146:149], v[186:189], 0
	v_mfma_f32_16x16x32_bf16 v[2:5], v[154:157], v[186:189], 0
	v_mfma_f32_16x16x32_bf16 v[50:53], v[150:153], v[166:169], v[50:53]
	v_mfma_f32_16x16x32_bf16 v[42:45], v[158:161], v[166:169], v[42:45]
	v_mfma_f32_16x16x32_bf16 v[34:37], v[150:153], v[174:177], v[34:37]
	v_mfma_f32_16x16x32_bf16 v[26:29], v[158:161], v[174:177], v[26:29]
	v_mfma_f32_16x16x32_bf16 v[18:21], v[150:153], v[182:185], v[18:21]
	v_mfma_f32_16x16x32_bf16 v[10:13], v[158:161], v[182:185], v[10:13]
	v_mfma_f32_16x16x32_bf16 v[6:9], v[150:153], v[190:193], v[6:9]
	v_mfma_f32_16x16x32_bf16 v[2:5], v[158:161], v[190:193], v[2:5]
	s_setprio 0
	s_barrier
	s_branch .Lmid1440
.LBB0_1440:
	ds_read_b128 v[130:133], v234
	ds_read_b128 v[134:137], v234 offset:1024
	ds_read_b128 v[138:141], v234 offset:2048
	ds_read_b128 v[142:145], v234 offset:3072
	ds_read_b128 v[146:149], v235
	ds_read_b128 v[150:153], v235 offset:1024
	ds_read_b128 v[154:157], v235 offset:2048
	ds_read_b128 v[158:161], v235 offset:3072
	s_add_u32 s60, s58, 0x100
	s_addc_u32 s61, s59, 0
	s_cmp_eq_u32 s87, 12
	s_cselect_b32 s66, s33, s60
	s_cselect_b32 s67, s21, s61
	s_cselect_b32 s64, s84, s85
	s_cselect_b32 s65, s19, s86
	s_add_u32 s62, s66, 0x80
	s_addc_u32 s63, s67, 0
	ds_read_b128 v[162:165], v236
	ds_read_b128 v[166:169], v236 offset:1024
	ds_read_b128 v[170:173], v236 offset:2048
	ds_read_b128 v[174:177], v236 offset:3072
	ds_read_b128 v[178:181], v236 offset:4096
	ds_read_b128 v[182:185], v236 offset:5120
	ds_read_b128 v[186:189], v236 offset:6144
	ds_read_b128 v[190:193], v236 offset:7168
	s_add_u32 s58, s58, 0x40080
	s_addc_u32 s59, s59, 0
	s_mov_b32 s88, m0
	s_mov_b32 m0, s80
	s_nop 2
	global_load_lds_dwordx4 v228, s[58:59]
	s_mov_b32 m0, s88
	s_nop 0
	s_mov_b32 s88, m0
	s_mov_b32 m0, s81
	s_nop 2
	global_load_lds_dwordx4 v230, s[58:59]
	s_mov_b32 m0, s88
	s_waitcnt vmcnt(8)
	s_waitcnt lgkmcnt(0)
	s_barrier
	s_setprio 1
	v_mfma_f32_16x16x32_bf16 v[126:129], v[130:133], v[162:165], v[126:129]
	v_mfma_f32_16x16x32_bf16 v[122:125], v[138:141], v[162:165], v[122:125]
	v_mfma_f32_16x16x32_bf16 v[114:117], v[130:133], v[170:173], v[114:117]
	v_mfma_f32_16x16x32_bf16 v[106:109], v[138:141], v[170:173], v[106:109]
	v_mfma_f32_16x16x32_bf16 v[94:97], v[130:133], v[178:181], v[94:97]
	v_mfma_f32_16x16x32_bf16 v[90:93], v[138:141], v[178:181], v[90:93]
	v_mfma_f32_16x16x32_bf16 v[86:89], v[130:133], v[186:189], v[86:89]
	v_mfma_f32_16x16x32_bf16 v[78:81], v[138:141], v[186:189], v[78:81]
	v_mfma_f32_16x16x32_bf16 v[126:129], v[134:137], v[166:169], v[126:129]
	v_mfma_f32_16x16x32_bf16 v[122:125], v[142:145], v[166:169], v[122:125]
	v_mfma_f32_16x16x32_bf16 v[114:117], v[134:137], v[174:177], v[114:117]
	v_mfma_f32_16x16x32_bf16 v[106:109], v[142:145], v[174:177], v[106:109]
	v_mfma_f32_16x16x32_bf16 v[94:97], v[134:137], v[182:185], v[94:97]
	v_mfma_f32_16x16x32_bf16 v[90:93], v[142:145], v[182:185], v[90:93]
	v_mfma_f32_16x16x32_bf16 v[86:89], v[134:137], v[190:193], v[86:89]
	v_mfma_f32_16x16x32_bf16 v[78:81], v[142:145], v[190:193], v[78:81]
	v_mfma_f32_16x16x32_bf16 v[118:121], v[146:149], v[162:165], v[118:121]
	v_mfma_f32_16x16x32_bf16 v[110:113], v[154:157], v[162:165], v[110:113]
	v_mfma_f32_16x16x32_bf16 v[102:105], v[146:149], v[170:173], v[102:105]
	v_mfma_f32_16x16x32_bf16 v[98:101], v[154:157], v[170:173], v[98:101]
	v_mfma_f32_16x16x32_bf16 v[82:85], v[146:149], v[178:181], v[82:85]
	v_mfma_f32_16x16x32_bf16 v[74:77], v[154:157], v[178:181], v[74:77]
	v_mfma_f32_16x16x32_bf16 v[70:73], v[146:149], v[186:189], v[70:73]
	v_mfma_f32_16x16x32_bf16 v[66:69], v[154:157], v[186:189], v[66:69]
	v_mfma_f32_16x16x32_bf16 v[118:121], v[150:153], v[166:169], v[118:121]
	v_mfma_f32_16x16x32_bf16 v[110:113], v[158:161], v[166:169], v[110:113]
	v_mfma_f32_16x16x32_bf16 v[102:105], v[150:153], v[174:177], v[102:105]
	v_mfma_f32_16x16x32_bf16 v[98:101], v[158:161], v[174:177], v[98:101]
	v_mfma_f32_16x16x32_bf16 v[82:85], v[150:153], v[182:185], v[82:85]
	v_mfma_f32_16x16x32_bf16 v[74:77], v[158:161], v[182:185], v[74:77]
	v_mfma_f32_16x16x32_bf16 v[70:73], v[150:153], v[190:193], v[70:73]
	v_mfma_f32_16x16x32_bf16 v[66:69], v[158:161], v[190:193], v[66:69]
	s_setprio 0
	s_barrier
	ds_read_b128 v[162:165], v236 offset:16384
	ds_read_b128 v[166:169], v236 offset:17408
	ds_read_b128 v[170:173], v236 offset:18432
	ds_read_b128 v[174:177], v236 offset:19456
	ds_read_b128 v[178:181], v236 offset:20480
	ds_read_b128 v[182:185], v236 offset:21504
	ds_read_b128 v[186:189], v236 offset:22528
	ds_read_b128 v[190:193], v236 offset:23552
	s_mov_b32 s58, m0
	s_mov_b32 m0, s30
	s_nop 2
	global_load_lds_dwordx4 v229, s[64:65]
	s_mov_b32 m0, s58
	s_nop 0
	s_mov_b32 s58, m0
	s_mov_b32 m0, s31
	s_nop 2
	global_load_lds_dwordx4 v231, s[64:65]
	s_mov_b32 m0, s58
	s_add_u32 s58, s64, 0x40000
	s_addc_u32 s59, s65, 0
	s_mov_b32 s88, m0
	s_mov_b32 m0, s34
	s_nop 2
	global_load_lds_dwordx4 v229, s[58:59]
	s_mov_b32 m0, s88
	s_nop 0
	s_mov_b32 s88, m0
	s_mov_b32 m0, s35
	s_nop 2
	global_load_lds_dwordx4 v231, s[58:59]
	s_mov_b32 m0, s88
	s_mov_b32 s58, m0
	s_mov_b32 m0, s28
	s_nop 2
	global_load_lds_dwordx4 v228, s[66:67]
	s_mov_b32 m0, s58
	s_nop 0
	s_mov_b32 s58, m0
	s_mov_b32 m0, s36
	s_nop 2
	global_load_lds_dwordx4 v230, s[66:67]
	s_mov_b32 m0, s58
	s_waitcnt vmcnt(8)
	s_waitcnt lgkmcnt(0)
	s_barrier
	s_setprio 1
	v_mfma_f32_16x16x32_bf16 v[62:65], v[130:133], v[162:165], v[62:65]
	v_mfma_f32_16x16x32_bf16 v[58:61], v[138:141], v[162:165], v[58:61]
	v_mfma_f32_16x16x32_bf16 v[54:57], v[130:133], v[170:173], v[54:57]
	v_mfma_f32_16x16x32_bf16 v[46:49], v[138:141], v[170:173], v[46:49]
	v_mfma_f32_16x16x32_bf16 v[38:41], v[130:133], v[178:181], v[38:41]
	v_mfma_f32_16x16x32_bf16 v[30:33], v[138:141], v[178:181], v[30:33]
	v_mfma_f32_16x16x32_bf16 v[22:25], v[130:133], v[186:189], v[22:25]
	v_mfma_f32_16x16x32_bf16 v[14:17], v[138:141], v[186:189], v[14:17]
	v_mfma_f32_16x16x32_bf16 v[62:65], v[134:137], v[166:169], v[62:65]
	v_mfma_f32_16x16x32_bf16 v[58:61], v[142:145], v[166:169], v[58:61]
	v_mfma_f32_16x16x32_bf16 v[54:57], v[134:137], v[174:177], v[54:57]
	v_mfma_f32_16x16x32_bf16 v[46:49], v[142:145], v[174:177], v[46:49]
	v_mfma_f32_16x16x32_bf16 v[38:41], v[134:137], v[182:185], v[38:41]
	v_mfma_f32_16x16x32_bf16 v[30:33], v[142:145], v[182:185], v[30:33]
	v_mfma_f32_16x16x32_bf16 v[22:25], v[134:137], v[190:193], v[22:25]
	v_mfma_f32_16x16x32_bf16 v[14:17], v[142:145], v[190:193], v[14:17]
	v_mfma_f32_16x16x32_bf16 v[50:53], v[146:149], v[162:165], v[50:53]
	v_mfma_f32_16x16x32_bf16 v[42:45], v[154:157], v[162:165], v[42:45]
	v_mfma_f32_16x16x32_bf16 v[34:37], v[146:149], v[170:173], v[34:37]
	v_mfma_f32_16x16x32_bf16 v[26:29], v[154:157], v[170:173], v[26:29]
	v_mfma_f32_16x16x32_bf16 v[18:21], v[146:149], v[178:181], v[18:21]
	v_mfma_f32_16x16x32_bf16 v[10:13], v[154:157], v[178:181], v[10:13]
	v_mfma_f32_16x16x32_bf16 v[6:9], v[146:149], v[186:189], v[6:9]
	v_mfma_f32_16x16x32_bf16 v[2:5], v[154:157], v[186:189], v[2:5]
	v_mfma_f32_16x16x32_bf16 v[50:53], v[150:153], v[166:169], v[50:53]
	v_mfma_f32_16x16x32_bf16 v[42:45], v[158:161], v[166:169], v[42:45]
	v_mfma_f32_16x16x32_bf16 v[34:37], v[150:153], v[174:177], v[34:37]
	v_mfma_f32_16x16x32_bf16 v[26:29], v[158:161], v[174:177], v[26:29]
	v_mfma_f32_16x16x32_bf16 v[18:21], v[150:153], v[182:185], v[18:21]
	v_mfma_f32_16x16x32_bf16 v[10:13], v[158:161], v[182:185], v[10:13]
	v_mfma_f32_16x16x32_bf16 v[6:9], v[150:153], v[190:193], v[6:9]
	v_mfma_f32_16x16x32_bf16 v[2:5], v[158:161], v[190:193], v[2:5]
	s_setprio 0
	s_barrier
.Lmid1440:
	ds_read_b128 v[130:133], v237
	ds_read_b128 v[134:137], v237 offset:1024
	ds_read_b128 v[138:141], v237 offset:2048
	ds_read_b128 v[142:145], v237 offset:3072
	ds_read_b128 v[146:149], v238
	ds_read_b128 v[150:153], v238 offset:1024
	ds_read_b128 v[154:157], v238 offset:2048
	ds_read_b128 v[158:161], v238 offset:3072
	ds_read_b128 v[162:165], v236 offset:32768
	ds_read_b128 v[166:169], v236 offset:33792
	ds_read_b128 v[170:173], v236 offset:34816
	ds_read_b128 v[174:177], v236 offset:35840
	ds_read_b128 v[178:181], v236 offset:36864
	ds_read_b128 v[182:185], v236 offset:37888
	ds_read_b128 v[186:189], v236 offset:38912
	ds_read_b128 v[190:193], v236 offset:39936
	s_add_u32 s58, s66, 0x40000
	s_addc_u32 s59, s67, 0
	s_mov_b32 s66, m0
	s_mov_b32 m0, s37
	s_nop 2
	global_load_lds_dwordx4 v228, s[58:59]
	s_mov_b32 m0, s66
	s_nop 0
	s_mov_b32 s66, m0
	s_mov_b32 m0, s52
	s_nop 2
	global_load_lds_dwordx4 v230, s[58:59]
	s_mov_b32 m0, s66
	s_waitcnt vmcnt(8)
	s_waitcnt lgkmcnt(0)
	s_barrier
	s_setprio 1
	v_mfma_f32_16x16x32_bf16 v[126:129], v[130:133], v[162:165], v[126:129]
	v_mfma_f32_16x16x32_bf16 v[122:125], v[138:141], v[162:165], v[122:125]
	v_mfma_f32_16x16x32_bf16 v[114:117], v[130:133], v[170:173], v[114:117]
	v_mfma_f32_16x16x32_bf16 v[106:109], v[138:141], v[170:173], v[106:109]
	v_mfma_f32_16x16x32_bf16 v[94:97], v[130:133], v[178:181], v[94:97]
	v_mfma_f32_16x16x32_bf16 v[90:93], v[138:141], v[178:181], v[90:93]
	v_mfma_f32_16x16x32_bf16 v[86:89], v[130:133], v[186:189], v[86:89]
	v_mfma_f32_16x16x32_bf16 v[78:81], v[138:141], v[186:189], v[78:81]
	v_mfma_f32_16x16x32_bf16 v[126:129], v[134:137], v[166:169], v[126:129]
	v_mfma_f32_16x16x32_bf16 v[122:125], v[142:145], v[166:169], v[122:125]
	v_mfma_f32_16x16x32_bf16 v[114:117], v[134:137], v[174:177], v[114:117]
	v_mfma_f32_16x16x32_bf16 v[106:109], v[142:145], v[174:177], v[106:109]
	v_mfma_f32_16x16x32_bf16 v[94:97], v[134:137], v[182:185], v[94:97]
	v_mfma_f32_16x16x32_bf16 v[90:93], v[142:145], v[182:185], v[90:93]
	v_mfma_f32_16x16x32_bf16 v[86:89], v[134:137], v[190:193], v[86:89]
	v_mfma_f32_16x16x32_bf16 v[78:81], v[142:145], v[190:193], v[78:81]
	v_mfma_f32_16x16x32_bf16 v[118:121], v[146:149], v[162:165], v[118:121]
	v_mfma_f32_16x16x32_bf16 v[110:113], v[154:157], v[162:165], v[110:113]
	v_mfma_f32_16x16x32_bf16 v[102:105], v[146:149], v[170:173], v[102:105]
	v_mfma_f32_16x16x32_bf16 v[98:101], v[154:157], v[170:173], v[98:101]
	v_mfma_f32_16x16x32_bf16 v[82:85], v[146:149], v[178:181], v[82:85]
	v_mfma_f32_16x16x32_bf16 v[74:77], v[154:157], v[178:181], v[74:77]
	v_mfma_f32_16x16x32_bf16 v[70:73], v[146:149], v[186:189], v[70:73]
	v_mfma_f32_16x16x32_bf16 v[66:69], v[154:157], v[186:189], v[66:69]
	v_mfma_f32_16x16x32_bf16 v[118:121], v[150:153], v[166:169], v[118:121]
	v_mfma_f32_16x16x32_bf16 v[110:113], v[158:161], v[166:169], v[110:113]
	v_mfma_f32_16x16x32_bf16 v[102:105], v[150:153], v[174:177], v[102:105]
	v_mfma_f32_16x16x32_bf16 v[98:101], v[158:161], v[174:177], v[98:101]
	v_mfma_f32_16x16x32_bf16 v[82:85], v[150:153], v[182:185], v[82:85]
	v_mfma_f32_16x16x32_bf16 v[74:77], v[158:161], v[182:185], v[74:77]
	v_mfma_f32_16x16x32_bf16 v[70:73], v[150:153], v[190:193], v[70:73]
	v_mfma_f32_16x16x32_bf16 v[66:69], v[158:161], v[190:193], v[66:69]
	s_setprio 0
	s_barrier
	ds_read_b128 v[162:165], v236 offset:49152
	ds_read_b128 v[166:169], v236 offset:50176
	ds_read_b128 v[170:173], v236 offset:51200
	ds_read_b128 v[174:177], v236 offset:52224
	ds_read_b128 v[178:181], v236 offset:53248
	ds_read_b128 v[182:185], v236 offset:54272
	ds_read_b128 v[186:189], v236 offset:55296
	ds_read_b128 v[190:193], v236 offset:56320
	s_add_u32 s58, s64, 0x80
	s_addc_u32 s59, s65, 0
	s_mov_b32 s66, m0
	s_mov_b32 m0, s68
	s_nop 2
	global_load_lds_dwordx4 v229, s[58:59]
	s_mov_b32 m0, s66
	s_nop 0
	s_mov_b32 s66, m0
	s_mov_b32 m0, s69
	s_nop 2
	global_load_lds_dwordx4 v231, s[58:59]
	s_mov_b32 m0, s66
	s_add_u32 s58, s64, 0x40080
	s_addc_u32 s59, s65, 0
	s_mov_b32 s64, m0
	s_mov_b32 m0, s78
	s_nop 2
	global_load_lds_dwordx4 v229, s[58:59]
	s_mov_b32 m0, s64
	s_nop 0
	s_mov_b32 s64, m0
	s_mov_b32 m0, s79
	s_nop 2
	global_load_lds_dwordx4 v231, s[58:59]
	s_mov_b32 m0, s64
	s_mov_b32 s58, m0
	s_mov_b32 m0, s76
	s_nop 2
	global_load_lds_dwordx4 v228, s[62:63]
	s_mov_b32 m0, s58
	s_nop 0
	s_mov_b32 s58, m0
	s_mov_b32 m0, s77
	s_nop 2
	global_load_lds_dwordx4 v230, s[62:63]
	s_mov_b32 m0, s58
	s_waitcnt vmcnt(8)
	s_waitcnt lgkmcnt(0)
	s_barrier
	s_setprio 1
	v_mfma_f32_16x16x32_bf16 v[62:65], v[130:133], v[162:165], v[62:65]
	v_mfma_f32_16x16x32_bf16 v[58:61], v[138:141], v[162:165], v[58:61]
	v_mfma_f32_16x16x32_bf16 v[54:57], v[130:133], v[170:173], v[54:57]
	v_mfma_f32_16x16x32_bf16 v[46:49], v[138:141], v[170:173], v[46:49]
	v_mfma_f32_16x16x32_bf16 v[38:41], v[130:133], v[178:181], v[38:41]
	v_mfma_f32_16x16x32_bf16 v[30:33], v[138:141], v[178:181], v[30:33]
	v_mfma_f32_16x16x32_bf16 v[22:25], v[130:133], v[186:189], v[22:25]
	v_mfma_f32_16x16x32_bf16 v[14:17], v[138:141], v[186:189], v[14:17]
	v_mfma_f32_16x16x32_bf16 v[62:65], v[134:137], v[166:169], v[62:65]
	v_mfma_f32_16x16x32_bf16 v[58:61], v[142:145], v[166:169], v[58:61]
	v_mfma_f32_16x16x32_bf16 v[54:57], v[134:137], v[174:177], v[54:57]
	v_mfma_f32_16x16x32_bf16 v[46:49], v[142:145], v[174:177], v[46:49]
	v_mfma_f32_16x16x32_bf16 v[38:41], v[134:137], v[182:185], v[38:41]
	v_mfma_f32_16x16x32_bf16 v[30:33], v[142:145], v[182:185], v[30:33]
	v_mfma_f32_16x16x32_bf16 v[22:25], v[134:137], v[190:193], v[22:25]
	v_mfma_f32_16x16x32_bf16 v[14:17], v[142:145], v[190:193], v[14:17]
	v_mfma_f32_16x16x32_bf16 v[50:53], v[146:149], v[162:165], v[50:53]
	v_mfma_f32_16x16x32_bf16 v[42:45], v[154:157], v[162:165], v[42:45]
	v_mfma_f32_16x16x32_bf16 v[34:37], v[146:149], v[170:173], v[34:37]
	v_mfma_f32_16x16x32_bf16 v[26:29], v[154:157], v[170:173], v[26:29]
	v_mfma_f32_16x16x32_bf16 v[18:21], v[146:149], v[178:181], v[18:21]
	v_mfma_f32_16x16x32_bf16 v[10:13], v[154:157], v[178:181], v[10:13]
	v_mfma_f32_16x16x32_bf16 v[6:9], v[146:149], v[186:189], v[6:9]
	v_mfma_f32_16x16x32_bf16 v[2:5], v[154:157], v[186:189], v[2:5]
	v_mfma_f32_16x16x32_bf16 v[50:53], v[150:153], v[166:169], v[50:53]
	v_mfma_f32_16x16x32_bf16 v[42:45], v[158:161], v[166:169], v[42:45]
	v_mfma_f32_16x16x32_bf16 v[34:37], v[150:153], v[174:177], v[34:37]
	v_mfma_f32_16x16x32_bf16 v[26:29], v[158:161], v[174:177], v[26:29]
	v_mfma_f32_16x16x32_bf16 v[18:21], v[150:153], v[182:185], v[18:21]
	v_mfma_f32_16x16x32_bf16 v[10:13], v[158:161], v[182:185], v[10:13]
	v_mfma_f32_16x16x32_bf16 v[6:9], v[150:153], v[190:193], v[6:9]
	v_mfma_f32_16x16x32_bf16 v[2:5], v[158:161], v[190:193], v[2:5]
	s_setprio 0
	s_barrier
	s_add_i32 s87, s87, 2
	s_add_u32 s85, s85, 0x100
	s_addc_u32 s86, s86, 0
	s_cmp_gt_u32 s87, 13
	s_mov_b64 s[58:59], s[60:61]
	s_cbranch_scc0 .LBB0_1440
	s_and_b64 vcc, exec, s[16:17]
	s_cbranch_vccz .LBB0_1443
	s_barrier

.LBB0_1896:
	s_cmp_eq_u32 s40, 0
	s_cbranch_scc1 .Lpeel6
	s_add_u32 s33, s74, s40
	s_addc_u32 s44, s75, s41
	s_add_u32 s56, s33, 0x1d800080
	s_addc_u32 s57, s44, 0
	s_add_u32 s33, s33, 0x1d800100
	s_addc_u32 s52, s44, 0
	v_add_u32_e32 v2, 0x10000, v173
	v_add_u32_e32 v14, 0x14000, v173
	s_and_b64 s[44:45], s[42:43], exec
	ds_read_b128 v[18:21], v2
	ds_read_b128 v[22:25], v2 offset:1024
	ds_read_b128 v[26:29], v2 offset:2048
	ds_read_b128 v[30:33], v2 offset:3072
	ds_read_b128 v[2:5], v14
	ds_read_b128 v[6:9], v14 offset:1024
	ds_read_b128 v[10:13], v14 offset:2048
	ds_read_b128 v[14:17], v14 offset:3072
	s_cselect_b32 s55, s11, s52
	s_cselect_b32 s54, s10, s33
	s_add_u32 s33, s2, s40
	s_addc_u32 s44, s23, s41
	s_and_b64 s[42:43], s[42:43], exec
	s_cselect_b32 s43, s39, s44
	s_cselect_b32 s42, s38, s33
	s_add_u32 s44, s54, 0x80
	s_addc_u32 s45, s55, 0
	s_add_u32 s52, s42, 0x80
	s_addc_u32 s53, s43, 0
	ds_read_b128 v[180:183], v174
	ds_read_b128 v[184:187], v174 offset:1024
	ds_read_b128 v[188:191], v174 offset:2048
	ds_read_b128 v[192:195], v174 offset:3072
	ds_read_b128 v[196:199], v174 offset:4096
	ds_read_b128 v[200:203], v174 offset:5120
	ds_read_b128 v[204:207], v174 offset:6144
	ds_read_b128 v[208:211], v174 offset:7168
	s_mov_b32 s33, m0
	s_mov_b32 m0, s93
	s_nop 2
	global_load_lds_dwordx4 v178, s[56:57]
	s_mov_b32 m0, s33
	s_nop 0
	s_mov_b32 s33, m0
	s_mov_b32 m0, s94
	s_nop 2
	global_load_lds_dwordx4 v177, s[56:57]
	s_mov_b32 m0, s33
	s_waitcnt vmcnt(8)
	s_waitcnt lgkmcnt(0)
	s_barrier
	s_setprio 1
	v_mfma_f32_16x16x128_f8f6f4 v[158:161], v[18:25], v[180:187], v[158:161]
	v_mfma_f32_16x16x128_f8f6f4 v[154:157], v[26:33], v[180:187], v[154:157]
	v_mfma_f32_16x16x128_f8f6f4 v[150:153], v[18:25], v[188:195], v[150:153]
	v_mfma_f32_16x16x128_f8f6f4 v[146:149], v[26:33], v[188:195], v[146:149]
	v_mfma_f32_16x16x128_f8f6f4 v[142:145], v[18:25], v[196:203], v[142:145]
	v_mfma_f32_16x16x128_f8f6f4 v[138:141], v[26:33], v[196:203], v[138:141]
	v_mfma_f32_16x16x128_f8f6f4 v[134:137], v[18:25], v[204:211], v[134:137]
	v_mfma_f32_16x16x128_f8f6f4 v[130:133], v[26:33], v[204:211], v[130:133]
	v_mfma_f32_16x16x128_f8f6f4 v[126:129], v[2:9], v[180:187], v[126:129]
	v_mfma_f32_16x16x128_f8f6f4 v[122:125], v[10:17], v[180:187], v[122:125]
	v_mfma_f32_16x16x128_f8f6f4 v[118:121], v[2:9], v[188:195], v[118:121]
	v_mfma_f32_16x16x128_f8f6f4 v[114:117], v[10:17], v[188:195], v[114:117]
	v_mfma_f32_16x16x128_f8f6f4 v[110:113], v[2:9], v[196:203], v[110:113]
	v_mfma_f32_16x16x128_f8f6f4 v[106:109], v[10:17], v[196:203], v[106:109]
	v_mfma_f32_16x16x128_f8f6f4 v[102:105], v[2:9], v[204:211], v[102:105]
	v_mfma_f32_16x16x128_f8f6f4 v[98:101], v[10:17], v[204:211], v[98:101]
	s_setprio 0
	s_barrier
	ds_read_b128 v[180:183], v174 offset:16384
	ds_read_b128 v[184:187], v174 offset:17408
	ds_read_b128 v[188:191], v174 offset:18432
	ds_read_b128 v[192:195], v174 offset:19456
	ds_read_b128 v[196:199], v174 offset:20480
	ds_read_b128 v[200:203], v174 offset:21504
	ds_read_b128 v[204:207], v174 offset:22528
	ds_read_b128 v[208:211], v174 offset:23552
	s_mov_b32 s33, m0
	s_mov_b32 m0, s67
	s_nop 2
	global_load_lds_dwordx4 v1, s[42:43]
	s_mov_b32 m0, s33
	s_add_u32 s56, s42, 0x20000
	s_mov_b32 s33, m0
	s_mov_b32 m0, s68
	s_nop 2
	global_load_lds_dwordx4 v163, s[42:43]
	s_mov_b32 m0, s33
	s_addc_u32 s57, s43, 0
	s_mov_b32 s33, m0
	s_mov_b32 m0, s69
	s_nop 2
	global_load_lds_dwordx4 v1, s[56:57]
	s_mov_b32 m0, s33
	s_nop 0
	s_mov_b32 s33, m0
	s_mov_b32 m0, s76
	s_nop 2
	global_load_lds_dwordx4 v163, s[56:57]
	s_mov_b32 m0, s33
	s_nop 0
	s_mov_b32 s33, m0
	s_mov_b32 m0, s15
	s_nop 2
	global_load_lds_dwordx4 v168, s[54:55]
	s_mov_b32 m0, s33
	s_nop 0
	s_mov_b32 s33, m0
	s_mov_b32 m0, s79
	s_nop 2
	global_load_lds_dwordx4 v172, s[54:55]
	s_mov_b32 m0, s33
	s_waitcnt vmcnt(8)
	s_waitcnt lgkmcnt(0)
	s_barrier
	s_setprio 1
	v_mfma_f32_16x16x128_f8f6f4 v[94:97], v[18:25], v[180:187], v[94:97]
	v_mfma_f32_16x16x128_f8f6f4 v[90:93], v[26:33], v[180:187], v[90:93]
	v_mfma_f32_16x16x128_f8f6f4 v[86:89], v[18:25], v[188:195], v[86:89]
	v_mfma_f32_16x16x128_f8f6f4 v[82:85], v[26:33], v[188:195], v[82:85]
	v_mfma_f32_16x16x128_f8f6f4 v[78:81], v[18:25], v[196:203], v[78:81]
	v_mfma_f32_16x16x128_f8f6f4 v[74:77], v[26:33], v[196:203], v[74:77]
	v_mfma_f32_16x16x128_f8f6f4 v[70:73], v[18:25], v[204:211], v[70:73]
	v_mfma_f32_16x16x128_f8f6f4 v[66:69], v[26:33], v[204:211], v[66:69]
	v_mfma_f32_16x16x128_f8f6f4 v[62:65], v[2:9], v[180:187], v[62:65]
	v_mfma_f32_16x16x128_f8f6f4 v[58:61], v[10:17], v[180:187], v[58:61]
	v_mfma_f32_16x16x128_f8f6f4 v[54:57], v[2:9], v[188:195], v[54:57]
	v_mfma_f32_16x16x128_f8f6f4 v[50:53], v[10:17], v[188:195], v[50:53]
	v_mfma_f32_16x16x128_f8f6f4 v[46:49], v[2:9], v[196:203], v[46:49]
	v_mfma_f32_16x16x128_f8f6f4 v[42:45], v[10:17], v[196:203], v[42:45]
	v_mfma_f32_16x16x128_f8f6f4 v[38:41], v[2:9], v[204:211], v[38:41]
	v_mfma_f32_16x16x128_f8f6f4 v[34:37], v[10:17], v[204:211], v[34:37]
	s_setprio 0
	s_barrier
.Lmid6:
	v_add_u32_e32 v14, 0x18000, v173
	v_add_u32_e32 v30, 0x1c000, v173
	ds_read_b128 v[2:5], v14
	ds_read_b128 v[6:9], v14 offset:1024
	ds_read_b128 v[10:13], v14 offset:2048
	ds_read_b128 v[14:17], v14 offset:3072
	ds_read_b128 v[18:21], v30
	ds_read_b128 v[22:25], v30 offset:1024
	ds_read_b128 v[26:29], v30 offset:2048
	ds_read_b128 v[30:33], v30 offset:3072
	ds_read_b128 v[180:183], v174 offset:32768
	ds_read_b128 v[184:187], v174 offset:33792
	ds_read_b128 v[188:191], v174 offset:34816
	ds_read_b128 v[192:195], v174 offset:35840
	ds_read_b128 v[196:199], v174 offset:36864
	ds_read_b128 v[200:203], v174 offset:37888
	ds_read_b128 v[204:207], v174 offset:38912
	ds_read_b128 v[208:211], v174 offset:39936
	s_mov_b32 s33, m0
	s_mov_b32 m0, s80
	s_nop 2
	global_load_lds_dwordx4 v169, s[54:55]
	s_mov_b32 m0, s33
	s_nop 0
	s_mov_b32 s33, m0
	s_mov_b32 m0, s81
	s_nop 2
	global_load_lds_dwordx4 v175, s[54:55]
	s_mov_b32 m0, s33
	s_waitcnt vmcnt(8)
	s_waitcnt lgkmcnt(0)
	s_barrier
	s_setprio 1
	v_mfma_f32_16x16x128_f8f6f4 v[158:161], v[2:9], v[180:187], v[158:161]
	v_mfma_f32_16x16x128_f8f6f4 v[154:157], v[10:17], v[180:187], v[154:157]
	v_mfma_f32_16x16x128_f8f6f4 v[150:153], v[2:9], v[188:195], v[150:153]
	v_mfma_f32_16x16x128_f8f6f4 v[146:149], v[10:17], v[188:195], v[146:149]
	v_mfma_f32_16x16x128_f8f6f4 v[142:145], v[2:9], v[196:203], v[142:145]
	v_mfma_f32_16x16x128_f8f6f4 v[138:141], v[10:17], v[196:203], v[138:141]
	v_mfma_f32_16x16x128_f8f6f4 v[134:137], v[2:9], v[204:211], v[134:137]
	v_mfma_f32_16x16x128_f8f6f4 v[130:133], v[10:17], v[204:211], v[130:133]
	v_mfma_f32_16x16x128_f8f6f4 v[126:129], v[18:25], v[180:187], v[126:129]
	v_mfma_f32_16x16x128_f8f6f4 v[122:125], v[26:33], v[180:187], v[122:125]
	v_mfma_f32_16x16x128_f8f6f4 v[118:121], v[18:25], v[188:195], v[118:121]
	v_mfma_f32_16x16x128_f8f6f4 v[114:117], v[26:33], v[188:195], v[114:117]
	v_mfma_f32_16x16x128_f8f6f4 v[110:113], v[18:25], v[196:203], v[110:113]
	v_mfma_f32_16x16x128_f8f6f4 v[106:109], v[26:33], v[196:203], v[106:109]
	v_mfma_f32_16x16x128_f8f6f4 v[102:105], v[18:25], v[204:211], v[102:105]
	v_mfma_f32_16x16x128_f8f6f4 v[98:101], v[26:33], v[204:211], v[98:101]
	s_setprio 0
	s_barrier
	ds_read_b128 v[180:183], v174 offset:49152
	ds_read_b128 v[184:187], v174 offset:50176
	ds_read_b128 v[188:191], v174 offset:51200
	ds_read_b128 v[192:195], v174 offset:52224
	ds_read_b128 v[196:199], v174 offset:53248
	ds_read_b128 v[200:203], v174 offset:54272
	ds_read_b128 v[204:207], v174 offset:55296
	ds_read_b128 v[208:211], v174 offset:56320
	s_mov_b32 s33, m0
	s_mov_b32 m0, s84
	s_nop 2
	global_load_lds_dwordx4 v1, s[52:53]
	s_mov_b32 m0, s33
	s_add_u32 s42, s42, 0x20080
	s_mov_b32 s33, m0
	s_mov_b32 m0, s85
	s_nop 2
	global_load_lds_dwordx4 v163, s[52:53]
	s_mov_b32 m0, s33
	s_addc_u32 s43, s43, 0
	s_mov_b32 s33, m0
	s_mov_b32 m0, s91
	s_nop 2
	global_load_lds_dwordx4 v1, s[42:43]
	s_mov_b32 m0, s33
	s_nop 0
	s_mov_b32 s33, m0
	s_mov_b32 m0, s92
	s_nop 2
	global_load_lds_dwordx4 v163, s[42:43]
	s_mov_b32 m0, s33
	s_nop 0
	s_mov_b32 s33, m0
	s_mov_b32 m0, s86
	s_nop 2
	global_load_lds_dwordx4 v168, s[44:45]
	s_mov_b32 m0, s33
	s_nop 0
	s_mov_b32 s33, m0
	s_mov_b32 m0, s87
	s_nop 2
	global_load_lds_dwordx4 v172, s[44:45]
	s_mov_b32 m0, s33
	s_waitcnt vmcnt(8)
	s_waitcnt lgkmcnt(0)
	s_barrier
	s_setprio 1
	v_mfma_f32_16x16x128_f8f6f4 v[94:97], v[2:9], v[180:187], v[94:97]
	v_mfma_f32_16x16x128_f8f6f4 v[90:93], v[10:17], v[180:187], v[90:93]
	v_mfma_f32_16x16x128_f8f6f4 v[86:89], v[2:9], v[188:195], v[86:89]
	v_mfma_f32_16x16x128_f8f6f4 v[82:85], v[10:17], v[188:195], v[82:85]
	v_mfma_f32_16x16x128_f8f6f4 v[78:81], v[2:9], v[196:203], v[78:81]
	v_mfma_f32_16x16x128_f8f6f4 v[74:77], v[10:17], v[196:203], v[74:77]
	v_mfma_f32_16x16x128_f8f6f4 v[70:73], v[2:9], v[204:211], v[70:73]
	v_mfma_f32_16x16x128_f8f6f4 v[66:69], v[10:17], v[204:211], v[66:69]
	v_mfma_f32_16x16x128_f8f6f4 v[62:65], v[18:25], v[180:187], v[62:65]
	v_mfma_f32_16x16x128_f8f6f4 v[58:61], v[26:33], v[180:187], v[58:61]
	v_mfma_f32_16x16x128_f8f6f4 v[54:57], v[18:25], v[188:195], v[54:57]
	v_mfma_f32_16x16x128_f8f6f4 v[50:53], v[26:33], v[188:195], v[50:53]
	v_mfma_f32_16x16x128_f8f6f4 v[46:49], v[18:25], v[196:203], v[46:49]
	v_mfma_f32_16x16x128_f8f6f4 v[42:45], v[26:33], v[196:203], v[42:45]
	v_mfma_f32_16x16x128_f8f6f4 v[38:41], v[18:25], v[204:211], v[38:41]
	v_mfma_f32_16x16x128_f8f6f4 v[34:37], v[26:33], v[204:211], v[34:37]
	s_setprio 0
	s_cmp_lt_i32 s9, 4
	s_cbranch_scc1 .Lkb6_do
	s_cmp_lg_u64 s[16:17], 0
	s_cbranch_scc0 .Lkb6_skip

.Lpeel6:
	s_add_u32 s33, s74, s40
	s_addc_u32 s44, s75, s41
	s_add_u32 s56, s33, 0x1d800080
	s_addc_u32 s57, s44, 0
	s_add_u32 s33, s33, 0x1d800100
	s_addc_u32 s52, s44, 0
	v_add_u32_e32 v2, 0x10000, v173
	v_add_u32_e32 v14, 0x14000, v173
	s_and_b64 s[44:45], s[42:43], exec
	ds_read_b128 v[18:21], v2
	ds_read_b128 v[22:25], v2 offset:1024
	ds_read_b128 v[26:29], v2 offset:2048
	ds_read_b128 v[30:33], v2 offset:3072
	ds_read_b128 v[2:5], v14
	ds_read_b128 v[6:9], v14 offset:1024
	ds_read_b128 v[10:13], v14 offset:2048
	ds_read_b128 v[14:17], v14 offset:3072
	s_cselect_b32 s55, s11, s52
	s_cselect_b32 s54, s10, s33
	s_add_u32 s33, s2, s40
	s_addc_u32 s44, s23, s41
	s_and_b64 s[42:43], s[42:43], exec
	s_cselect_b32 s43, s39, s44
	s_cselect_b32 s42, s38, s33
	s_add_u32 s44, s54, 0x80
	s_addc_u32 s45, s55, 0
	s_add_u32 s52, s42, 0x80
	s_addc_u32 s53, s43, 0
	ds_read_b128 v[180:183], v174
	ds_read_b128 v[184:187], v174 offset:1024
	ds_read_b128 v[188:191], v174 offset:2048
	ds_read_b128 v[192:195], v174 offset:3072
	ds_read_b128 v[196:199], v174 offset:4096
	ds_read_b128 v[200:203], v174 offset:5120
	ds_read_b128 v[204:207], v174 offset:6144
	ds_read_b128 v[208:211], v174 offset:7168
	s_mov_b32 s33, m0
	s_mov_b32 m0, s93
	s_nop 2
	global_load_lds_dwordx4 v178, s[56:57]
	s_mov_b32 m0, s33
	s_nop 0
	s_mov_b32 s33, m0
	s_mov_b32 m0, s94
	s_nop 2
	global_load_lds_dwordx4 v177, s[56:57]
	s_mov_b32 m0, s33
	s_waitcnt vmcnt(8)
	s_waitcnt lgkmcnt(0)
	s_barrier
	s_setprio 1
	v_mfma_f32_16x16x128_f8f6f4 v[158:161], v[18:25], v[180:187], 0
	v_mfma_f32_16x16x128_f8f6f4 v[154:157], v[26:33], v[180:187], 0
	v_mfma_f32_16x16x128_f8f6f4 v[150:153], v[18:25], v[188:195], 0
	v_mfma_f32_16x16x128_f8f6f4 v[146:149], v[26:33], v[188:195], 0
	v_mfma_f32_16x16x128_f8f6f4 v[142:145], v[18:25], v[196:203], 0
	v_mfma_f32_16x16x128_f8f6f4 v[138:141], v[26:33], v[196:203], 0
	v_mfma_f32_16x16x128_f8f6f4 v[134:137], v[18:25], v[204:211], 0
	v_mfma_f32_16x16x128_f8f6f4 v[130:133], v[26:33], v[204:211], 0
	v_mfma_f32_16x16x128_f8f6f4 v[126:129], v[2:9], v[180:187], 0
	v_mfma_f32_16x16x128_f8f6f4 v[122:125], v[10:17], v[180:187], 0
	v_mfma_f32_16x16x128_f8f6f4 v[118:121], v[2:9], v[188:195], 0
	v_mfma_f32_16x16x128_f8f6f4 v[114:117], v[10:17], v[188:195], 0
	v_mfma_f32_16x16x128_f8f6f4 v[110:113], v[2:9], v[196:203], 0
	v_mfma_f32_16x16x128_f8f6f4 v[106:109], v[10:17], v[196:203], 0
	v_mfma_f32_16x16x128_f8f6f4 v[102:105], v[2:9], v[204:211], 0
	v_mfma_f32_16x16x128_f8f6f4 v[98:101], v[10:17], v[204:211], 0
	s_setprio 0
	s_barrier
	ds_read_b128 v[180:183], v174 offset:16384
	ds_read_b128 v[184:187], v174 offset:17408
	ds_read_b128 v[188:191], v174 offset:18432
	ds_read_b128 v[192:195], v174 offset:19456
	ds_read_b128 v[196:199], v174 offset:20480
	ds_read_b128 v[200:203], v174 offset:21504
	ds_read_b128 v[204:207], v174 offset:22528
	ds_read_b128 v[208:211], v174 offset:23552
	s_mov_b32 s33, m0
	s_mov_b32 m0, s67
	s_nop 2
	global_load_lds_dwordx4 v1, s[42:43]
	s_mov_b32 m0, s33
	s_add_u32 s56, s42, 0x20000
	s_mov_b32 s33, m0
	s_mov_b32 m0, s68
	s_nop 2
	global_load_lds_dwordx4 v163, s[42:43]
	s_mov_b32 m0, s33
	s_addc_u32 s57, s43, 0
	s_mov_b32 s33, m0
	s_mov_b32 m0, s69
	s_nop 2
	global_load_lds_dwordx4 v1, s[56:57]
	s_mov_b32 m0, s33
	s_nop 0
	s_mov_b32 s33, m0
	s_mov_b32 m0, s76
	s_nop 2
	global_load_lds_dwordx4 v163, s[56:57]
	s_mov_b32 m0, s33
	s_nop 0
	s_mov_b32 s33, m0
	s_mov_b32 m0, s15
	s_nop 2
	global_load_lds_dwordx4 v168, s[54:55]
	s_mov_b32 m0, s33
	s_nop 0
	s_mov_b32 s33, m0
	s_mov_b32 m0, s79
	s_nop 2
	global_load_lds_dwordx4 v172, s[54:55]
	s_mov_b32 m0, s33
	s_waitcnt vmcnt(8)
	s_waitcnt lgkmcnt(0)
	s_barrier
	s_setprio 1
	v_mfma_f32_16x16x128_f8f6f4 v[94:97], v[18:25], v[180:187], 0
	v_mfma_f32_16x16x128_f8f6f4 v[90:93], v[26:33], v[180:187], 0
	v_mfma_f32_16x16x128_f8f6f4 v[86:89], v[18:25], v[188:195], 0
	v_mfma_f32_16x16x128_f8f6f4 v[82:85], v[26:33], v[188:195], 0
	v_mfma_f32_16x16x128_f8f6f4 v[78:81], v[18:25], v[196:203], 0
	v_mfma_f32_16x16x128_f8f6f4 v[74:77], v[26:33], v[196:203], 0
	v_mfma_f32_16x16x128_f8f6f4 v[70:73], v[18:25], v[204:211], 0
	v_mfma_f32_16x16x128_f8f6f4 v[66:69], v[26:33], v[204:211], 0
	v_mfma_f32_16x16x128_f8f6f4 v[62:65], v[2:9], v[180:187], 0
	v_mfma_f32_16x16x128_f8f6f4 v[58:61], v[10:17], v[180:187], 0
	v_mfma_f32_16x16x128_f8f6f4 v[54:57], v[2:9], v[188:195], 0
	v_mfma_f32_16x16x128_f8f6f4 v[50:53], v[10:17], v[188:195], 0
	v_mfma_f32_16x16x128_f8f6f4 v[46:49], v[2:9], v[196:203], 0
	v_mfma_f32_16x16x128_f8f6f4 v[42:45], v[10:17], v[196:203], 0
	v_mfma_f32_16x16x128_f8f6f4 v[38:41], v[2:9], v[204:211], 0
	v_mfma_f32_16x16x128_f8f6f4 v[34:37], v[10:17], v[204:211], 0
	s_setprio 0
	s_barrier
	s_branch .Lmid6

.LBB0_1943:
	s_add_u32 s54, s38, 0x80
	s_addc_u32 s55, s39, 0
	v_add_u32_e32 v2, 0x10000, v174
	v_add_u32_e32 v14, 0x14000, v174
	s_add_u32 s38, s38, 0x100
	ds_read_b128 v[18:21], v2
	ds_read_b128 v[22:25], v2 offset:1024
	ds_read_b128 v[26:29], v2 offset:2048
	ds_read_b128 v[30:33], v2 offset:3072
	ds_read_b128 v[2:5], v14
	ds_read_b128 v[6:9], v14 offset:1024
	ds_read_b128 v[10:13], v14 offset:2048
	ds_read_b128 v[14:17], v14 offset:3072
	s_addc_u32 s39, s39, 0
	s_and_b64 s[40:41], s[40:41], exec
	s_cselect_b32 s52, s10, s38
	s_cselect_b32 s53, s11, s39
	s_cselect_b32 s41, s1, s87
	s_cselect_b32 s40, s0, s86
	s_add_u32 s42, s52, 0x80
	s_addc_u32 s43, s53, 0
	s_add_u32 s44, s40, 0x80
	s_addc_u32 s45, s41, 0
	ds_read_b128 v[180:183], v175
	ds_read_b128 v[184:187], v175 offset:1024
	ds_read_b128 v[188:191], v175 offset:2048
	ds_read_b128 v[192:195], v175 offset:3072
	ds_read_b128 v[196:199], v175 offset:4096
	ds_read_b128 v[200:203], v175 offset:5120
	ds_read_b128 v[204:207], v175 offset:6144
	ds_read_b128 v[208:211], v175 offset:7168
	s_mov_b32 s33, m0
	s_mov_b32 m0, s78
	s_nop 2
	global_load_lds_dwordx4 v164, s[54:55]
	s_mov_b32 m0, s33
	s_nop 0
	s_mov_b32 s33, m0
	s_mov_b32 m0, s79
	s_nop 2
	global_load_lds_dwordx4 v166, s[54:55]
	s_mov_b32 m0, s33
	s_waitcnt vmcnt(8)
	s_waitcnt lgkmcnt(0)
	s_barrier
	s_setprio 1
	v_mfma_f32_16x16x128_f8f6f4 v[158:161], v[18:25], v[180:187], v[158:161]
	v_mfma_f32_16x16x128_f8f6f4 v[150:153], v[26:33], v[180:187], v[150:153]
	v_mfma_f32_16x16x128_f8f6f4 v[142:145], v[18:25], v[188:195], v[142:145]
	v_mfma_f32_16x16x128_f8f6f4 v[134:137], v[26:33], v[188:195], v[134:137]
	v_mfma_f32_16x16x128_f8f6f4 v[126:129], v[18:25], v[196:203], v[126:129]
	v_mfma_f32_16x16x128_f8f6f4 v[118:121], v[26:33], v[196:203], v[118:121]
	v_mfma_f32_16x16x128_f8f6f4 v[110:113], v[18:25], v[204:211], v[110:113]
	v_mfma_f32_16x16x128_f8f6f4 v[102:105], v[26:33], v[204:211], v[102:105]
	v_mfma_f32_16x16x128_f8f6f4 v[154:157], v[2:9], v[180:187], v[154:157]
	v_mfma_f32_16x16x128_f8f6f4 v[146:149], v[10:17], v[180:187], v[146:149]
	v_mfma_f32_16x16x128_f8f6f4 v[138:141], v[2:9], v[188:195], v[138:141]
	v_mfma_f32_16x16x128_f8f6f4 v[130:133], v[10:17], v[188:195], v[130:133]
	v_mfma_f32_16x16x128_f8f6f4 v[122:125], v[2:9], v[196:203], v[122:125]
	v_mfma_f32_16x16x128_f8f6f4 v[114:117], v[10:17], v[196:203], v[114:117]
	v_mfma_f32_16x16x128_f8f6f4 v[106:109], v[2:9], v[204:211], v[106:109]
	v_mfma_f32_16x16x128_f8f6f4 v[98:101], v[10:17], v[204:211], v[98:101]
	s_setprio 0
	s_barrier
	ds_read_b128 v[180:183], v175 offset:16384
	ds_read_b128 v[184:187], v175 offset:17408
	ds_read_b128 v[188:191], v175 offset:18432
	ds_read_b128 v[192:195], v175 offset:19456
	ds_read_b128 v[196:199], v175 offset:20480
	ds_read_b128 v[200:203], v175 offset:21504
	ds_read_b128 v[204:207], v175 offset:22528
	ds_read_b128 v[208:211], v175 offset:23552
	s_mov_b32 s33, m0
	s_mov_b32 m0, s34
	s_nop 2
	global_load_lds_dwordx4 v165, s[40:41]
	s_mov_b32 m0, s33
	s_add_u32 s54, s40, 0x20000
	s_mov_b32 s33, m0
	s_mov_b32 m0, s35
	s_nop 2
	global_load_lds_dwordx4 v167, s[40:41]
	s_mov_b32 m0, s33
	s_addc_u32 s55, s41, 0
	s_mov_b32 s33, m0
	s_mov_b32 m0, s36
	s_nop 2
	global_load_lds_dwordx4 v165, s[54:55]
	s_mov_b32 m0, s33
	s_nop 0
	s_mov_b32 s33, m0
	s_mov_b32 m0, s37
	s_nop 2
	global_load_lds_dwordx4 v167, s[54:55]
	s_mov_b32 m0, s33
	s_nop 0
	s_mov_b32 s33, m0
	s_mov_b32 m0, s31
	s_nop 2
	global_load_lds_dwordx4 v171, s[52:53]
	s_mov_b32 m0, s33
	s_nop 0
	s_mov_b32 s33, m0
	s_mov_b32 m0, s56
	s_nop 2
	global_load_lds_dwordx4 v173, s[52:53]
	s_mov_b32 m0, s33
	s_waitcnt vmcnt(8)
	s_waitcnt lgkmcnt(0)
	s_barrier
	s_setprio 1
	v_mfma_f32_16x16x128_f8f6f4 v[94:97], v[18:25], v[180:187], v[94:97]
	v_mfma_f32_16x16x128_f8f6f4 v[86:89], v[26:33], v[180:187], v[86:89]
	v_mfma_f32_16x16x128_f8f6f4 v[78:81], v[18:25], v[188:195], v[78:81]
	v_mfma_f32_16x16x128_f8f6f4 v[70:73], v[26:33], v[188:195], v[70:73]
	v_mfma_f32_16x16x128_f8f6f4 v[62:65], v[18:25], v[196:203], v[62:65]
	v_mfma_f32_16x16x128_f8f6f4 v[54:57], v[26:33], v[196:203], v[54:57]
	v_mfma_f32_16x16x128_f8f6f4 v[46:49], v[18:25], v[204:211], v[46:49]
	v_mfma_f32_16x16x128_f8f6f4 v[38:41], v[26:33], v[204:211], v[38:41]
	v_mfma_f32_16x16x128_f8f6f4 v[90:93], v[2:9], v[180:187], v[90:93]
	v_mfma_f32_16x16x128_f8f6f4 v[82:85], v[10:17], v[180:187], v[82:85]
	v_mfma_f32_16x16x128_f8f6f4 v[74:77], v[2:9], v[188:195], v[74:77]
	v_mfma_f32_16x16x128_f8f6f4 v[66:69], v[10:17], v[188:195], v[66:69]
	v_mfma_f32_16x16x128_f8f6f4 v[58:61], v[2:9], v[196:203], v[58:61]
	v_mfma_f32_16x16x128_f8f6f4 v[50:53], v[10:17], v[196:203], v[50:53]
	v_mfma_f32_16x16x128_f8f6f4 v[42:45], v[2:9], v[204:211], v[42:45]
	v_mfma_f32_16x16x128_f8f6f4 v[34:37], v[10:17], v[204:211], v[34:37]
	s_setprio 0
	s_barrier
	v_add_u32_e32 v14, 0x18000, v174
	v_add_u32_e32 v30, 0x1c000, v174
	ds_read_b128 v[2:5], v14
	ds_read_b128 v[6:9], v14 offset:1024
	ds_read_b128 v[10:13], v14 offset:2048
	ds_read_b128 v[14:17], v14 offset:3072
	ds_read_b128 v[18:21], v30
	ds_read_b128 v[22:25], v30 offset:1024
	ds_read_b128 v[26:29], v30 offset:2048
	ds_read_b128 v[30:33], v30 offset:3072
	ds_read_b128 v[180:183], v175 offset:32768
	ds_read_b128 v[184:187], v175 offset:33792
	ds_read_b128 v[188:191], v175 offset:34816
	ds_read_b128 v[192:195], v175 offset:35840
	ds_read_b128 v[196:199], v175 offset:36864
	ds_read_b128 v[200:203], v175 offset:37888
	ds_read_b128 v[204:207], v175 offset:38912
	ds_read_b128 v[208:211], v175 offset:39936
	s_mov_b32 s33, m0
	s_mov_b32 m0, s57
	s_nop 2
	global_load_lds_dwordx4 v177, s[52:53]
	s_mov_b32 m0, s33
	s_nop 0
	s_mov_b32 s33, m0
	s_mov_b32 m0, s63
	s_nop 2
	global_load_lds_dwordx4 v178, s[52:53]
	s_mov_b32 m0, s33
	s_waitcnt vmcnt(8)
	s_waitcnt lgkmcnt(0)
	s_barrier
	s_setprio 1
	v_mfma_f32_16x16x128_f8f6f4 v[158:161], v[2:9], v[180:187], v[158:161]
	v_mfma_f32_16x16x128_f8f6f4 v[150:153], v[10:17], v[180:187], v[150:153]
	v_mfma_f32_16x16x128_f8f6f4 v[142:145], v[2:9], v[188:195], v[142:145]
	v_mfma_f32_16x16x128_f8f6f4 v[134:137], v[10:17], v[188:195], v[134:137]
	v_mfma_f32_16x16x128_f8f6f4 v[126:129], v[2:9], v[196:203], v[126:129]
	v_mfma_f32_16x16x128_f8f6f4 v[118:121], v[10:17], v[196:203], v[118:121]
	v_mfma_f32_16x16x128_f8f6f4 v[110:113], v[2:9], v[204:211], v[110:113]
	v_mfma_f32_16x16x128_f8f6f4 v[102:105], v[10:17], v[204:211], v[102:105]
	v_mfma_f32_16x16x128_f8f6f4 v[154:157], v[18:25], v[180:187], v[154:157]
	v_mfma_f32_16x16x128_f8f6f4 v[146:149], v[26:33], v[180:187], v[146:149]
	v_mfma_f32_16x16x128_f8f6f4 v[138:141], v[18:25], v[188:195], v[138:141]
	v_mfma_f32_16x16x128_f8f6f4 v[130:133], v[26:33], v[188:195], v[130:133]
	v_mfma_f32_16x16x128_f8f6f4 v[122:125], v[18:25], v[196:203], v[122:125]
	v_mfma_f32_16x16x128_f8f6f4 v[114:117], v[26:33], v[196:203], v[114:117]
	v_mfma_f32_16x16x128_f8f6f4 v[106:109], v[18:25], v[204:211], v[106:109]
	v_mfma_f32_16x16x128_f8f6f4 v[98:101], v[26:33], v[204:211], v[98:101]
	s_setprio 0
	s_barrier
	ds_read_b128 v[180:183], v175 offset:49152
	ds_read_b128 v[184:187], v175 offset:50176
	ds_read_b128 v[188:191], v175 offset:51200
	ds_read_b128 v[192:195], v175 offset:52224
	ds_read_b128 v[196:199], v175 offset:53248
	ds_read_b128 v[200:203], v175 offset:54272
	ds_read_b128 v[204:207], v175 offset:55296
	ds_read_b128 v[208:211], v175 offset:56320
	s_mov_b32 s33, m0
	s_mov_b32 m0, s66
	s_nop 2
	global_load_lds_dwordx4 v165, s[44:45]
	s_mov_b32 m0, s33
	s_add_u32 s40, s40, 0x20080
	s_mov_b32 s33, m0
	s_mov_b32 m0, s67
	s_nop 2
	global_load_lds_dwordx4 v167, s[44:45]
	s_mov_b32 m0, s33
	s_addc_u32 s41, s41, 0
	s_mov_b32 s33, m0
	s_mov_b32 m0, s76
	s_nop 2
	global_load_lds_dwordx4 v165, s[40:41]
	s_mov_b32 m0, s33
	s_nop 0
	s_mov_b32 s33, m0
	s_mov_b32 m0, s77
	s_nop 2
	global_load_lds_dwordx4 v167, s[40:41]
	s_mov_b32 m0, s33
	s_nop 0
	s_mov_b32 s33, m0
	s_mov_b32 m0, s68
	s_nop 2
	global_load_lds_dwordx4 v171, s[42:43]
	s_mov_b32 m0, s33
	s_nop 0
	s_mov_b32 s33, m0
	s_mov_b32 m0, s69
	s_nop 2
	global_load_lds_dwordx4 v173, s[42:43]
	s_mov_b32 m0, s33
	s_waitcnt vmcnt(8)
	s_waitcnt lgkmcnt(0)
	s_barrier
	s_setprio 1
	v_mfma_f32_16x16x128_f8f6f4 v[94:97], v[2:9], v[180:187], v[94:97]
	v_mfma_f32_16x16x128_f8f6f4 v[86:89], v[10:17], v[180:187], v[86:89]
	v_mfma_f32_16x16x128_f8f6f4 v[78:81], v[2:9], v[188:195], v[78:81]
	v_mfma_f32_16x16x128_f8f6f4 v[70:73], v[10:17], v[188:195], v[70:73]
	v_mfma_f32_16x16x128_f8f6f4 v[62:65], v[2:9], v[196:203], v[62:65]
	v_mfma_f32_16x16x128_f8f6f4 v[54:57], v[10:17], v[196:203], v[54:57]
	v_mfma_f32_16x16x128_f8f6f4 v[46:49], v[2:9], v[204:211], v[46:49]
	v_mfma_f32_16x16x128_f8f6f4 v[38:41], v[10:17], v[204:211], v[38:41]
	v_mfma_f32_16x16x128_f8f6f4 v[90:93], v[18:25], v[180:187], v[90:93]
	v_mfma_f32_16x16x128_f8f6f4 v[82:85], v[26:33], v[180:187], v[82:85]
	v_mfma_f32_16x16x128_f8f6f4 v[74:77], v[18:25], v[188:195], v[74:77]
	v_mfma_f32_16x16x128_f8f6f4 v[66:69], v[26:33], v[188:195], v[66:69]
	v_mfma_f32_16x16x128_f8f6f4 v[58:61], v[18:25], v[196:203], v[58:61]
	v_mfma_f32_16x16x128_f8f6f4 v[50:53], v[26:33], v[196:203], v[50:53]
	v_mfma_f32_16x16x128_f8f6f4 v[42:45], v[18:25], v[204:211], v[42:45]
	v_mfma_f32_16x16x128_f8f6f4 v[34:37], v[26:33], v[204:211], v[34:37]
	s_setprio 0
	s_barrier
	s_add_i32 s88, s88, 2
	s_add_u32 s86, s86, 0x100
	s_addc_u32 s87, s87, 0
	s_cmp_gt_u32 s88, 5
	s_cbranch_scc1 .LBB0_1957

.LBB0_2092:
	s_cmp_eq_u32 s91, 0
	s_cbranch_scc1 .Lpeel7
	s_lshl_b32 s33, s91, 7
	s_add_u32 s52, s36, s33
	s_addc_u32 s53, s37, 0
	s_add_u32 s46, s52, 0x100
	s_addc_u32 s47, s53, 0
	s_and_b64 s[44:45], s[42:43], exec
	s_cselect_b32 s49, s15, s47
	s_cselect_b32 s48, s17, s46
	s_add_u32 s33, s26, s33
	v_add_u32_e32 v2, 0x10000, v171
	v_add_u32_e32 v14, 0x14000, v171
	s_addc_u32 s44, s27, 0
	ds_read_b128 v[18:21], v2
	ds_read_b128 v[22:25], v2 offset:1024
	ds_read_b128 v[26:29], v2 offset:2048
	ds_read_b128 v[30:33], v2 offset:3072
	ds_read_b128 v[2:5], v14
	ds_read_b128 v[6:9], v14 offset:1024
	ds_read_b128 v[10:13], v14 offset:2048
	ds_read_b128 v[14:17], v14 offset:3072
	s_add_u32 s33, s33, 0x100
	s_addc_u32 s44, s44, 0
	s_and_b64 s[42:43], s[42:43], exec
	s_cselect_b32 s43, s19, s44
	s_cselect_b32 s42, s18, s33
	s_add_u32 s44, s48, 0x80
	s_addc_u32 s45, s49, 0
	s_add_u32 s46, s42, 0x80
	s_addc_u32 s47, s43, 0
	ds_read_b128 v[176:179], v172
	ds_read_b128 v[180:183], v172 offset:1024
	ds_read_b128 v[184:187], v172 offset:2048
	ds_read_b128 v[188:191], v172 offset:3072
	ds_read_b128 v[192:195], v172 offset:4096
	ds_read_b128 v[196:199], v172 offset:5120
	ds_read_b128 v[200:203], v172 offset:6144
	ds_read_b128 v[204:207], v172 offset:7168
	s_add_u32 s52, s52, 0x20080
	s_addc_u32 s53, s53, 0
	s_mov_b32 s33, m0
	s_mov_b32 m0, s79
	s_nop 2
	global_load_lds_dwordx4 v163, s[52:53]
	s_mov_b32 m0, s33
	s_nop 0
	s_mov_b32 s33, m0
	s_mov_b32 m0, s80
	s_nop 2
	global_load_lds_dwordx4 v164, s[52:53]
	s_mov_b32 m0, s33
	s_waitcnt vmcnt(8)
	s_waitcnt lgkmcnt(0)
	s_barrier
	s_setprio 1
	v_mfma_f32_16x16x128_f8f6f4 v[158:161], v[18:25], v[176:183], v[158:161]
	v_mfma_f32_16x16x128_f8f6f4 v[154:157], v[26:33], v[176:183], v[154:157]
	v_mfma_f32_16x16x128_f8f6f4 v[142:145], v[18:25], v[184:191], v[142:145]
	v_mfma_f32_16x16x128_f8f6f4 v[138:141], v[26:33], v[184:191], v[138:141]
	v_mfma_f32_16x16x128_f8f6f4 v[126:129], v[18:25], v[192:199], v[126:129]
	v_mfma_f32_16x16x128_f8f6f4 v[122:125], v[26:33], v[192:199], v[122:125]
	v_mfma_f32_16x16x128_f8f6f4 v[110:113], v[18:25], v[200:207], v[110:113]
	v_mfma_f32_16x16x128_f8f6f4 v[106:109], v[26:33], v[200:207], v[106:109]
	v_mfma_f32_16x16x128_f8f6f4 v[150:153], v[2:9], v[176:183], v[150:153]
	v_mfma_f32_16x16x128_f8f6f4 v[146:149], v[10:17], v[176:183], v[146:149]
	v_mfma_f32_16x16x128_f8f6f4 v[134:137], v[2:9], v[184:191], v[134:137]
	v_mfma_f32_16x16x128_f8f6f4 v[130:133], v[10:17], v[184:191], v[130:133]
	v_mfma_f32_16x16x128_f8f6f4 v[118:121], v[2:9], v[192:199], v[118:121]
	v_mfma_f32_16x16x128_f8f6f4 v[114:117], v[10:17], v[192:199], v[114:117]
	v_mfma_f32_16x16x128_f8f6f4 v[102:105], v[2:9], v[200:207], v[102:105]
	v_mfma_f32_16x16x128_f8f6f4 v[98:101], v[10:17], v[200:207], v[98:101]
	s_setprio 0
	s_barrier
	ds_read_b128 v[176:179], v172 offset:16384
	ds_read_b128 v[180:183], v172 offset:17408
	ds_read_b128 v[184:187], v172 offset:18432
	ds_read_b128 v[188:191], v172 offset:19456
	ds_read_b128 v[192:195], v172 offset:20480
	ds_read_b128 v[196:199], v172 offset:21504
	ds_read_b128 v[200:203], v172 offset:22528
	ds_read_b128 v[204:207], v172 offset:23552
	s_mov_b32 s33, m0
	s_mov_b32 m0, s64
	s_nop 2
	global_load_lds_dwordx4 v1, s[42:43]
	s_mov_b32 m0, s33
	s_add_u32 s52, s42, 0x20000
	s_mov_b32 s33, m0
	s_mov_b32 m0, s65
	s_nop 2
	global_load_lds_dwordx4 v162, s[42:43]
	s_mov_b32 m0, s33
	s_addc_u32 s53, s43, 0
	s_mov_b32 s33, m0
	s_mov_b32 m0, s24
	s_nop 2
	global_load_lds_dwordx4 v1, s[52:53]
	s_mov_b32 m0, s33
	s_nop 0
	s_mov_b32 s33, m0
	s_mov_b32 m0, s25
	s_nop 2
	global_load_lds_dwordx4 v162, s[52:53]
	s_mov_b32 m0, s33
	s_nop 0
	s_mov_b32 s33, m0
	s_mov_b32 m0, s63
	s_nop 2
	global_load_lds_dwordx4 v163, s[48:49]
	s_mov_b32 m0, s33
	s_nop 0
	s_mov_b32 s33, m0
	s_mov_b32 m0, s2
	s_nop 2
	global_load_lds_dwordx4 v164, s[48:49]
	s_mov_b32 m0, s33
	s_waitcnt vmcnt(8)
	s_waitcnt lgkmcnt(0)
	s_barrier
	s_setprio 1
	v_mfma_f32_16x16x128_f8f6f4 v[94:97], v[18:25], v[176:183], v[94:97]
	v_mfma_f32_16x16x128_f8f6f4 v[90:93], v[26:33], v[176:183], v[90:93]
	v_mfma_f32_16x16x128_f8f6f4 v[78:81], v[18:25], v[184:191], v[78:81]
	v_mfma_f32_16x16x128_f8f6f4 v[74:77], v[26:33], v[184:191], v[74:77]
	v_mfma_f32_16x16x128_f8f6f4 v[62:65], v[18:25], v[192:199], v[62:65]
	v_mfma_f32_16x16x128_f8f6f4 v[58:61], v[26:33], v[192:199], v[58:61]
	v_mfma_f32_16x16x128_f8f6f4 v[46:49], v[18:25], v[200:207], v[46:49]
	v_mfma_f32_16x16x128_f8f6f4 v[42:45], v[26:33], v[200:207], v[42:45]
	v_mfma_f32_16x16x128_f8f6f4 v[86:89], v[2:9], v[176:183], v[86:89]
	v_mfma_f32_16x16x128_f8f6f4 v[82:85], v[10:17], v[176:183], v[82:85]
	v_mfma_f32_16x16x128_f8f6f4 v[70:73], v[2:9], v[184:191], v[70:73]
	v_mfma_f32_16x16x128_f8f6f4 v[66:69], v[10:17], v[184:191], v[66:69]
	v_mfma_f32_16x16x128_f8f6f4 v[54:57], v[2:9], v[192:199], v[54:57]
	v_mfma_f32_16x16x128_f8f6f4 v[50:53], v[10:17], v[192:199], v[50:53]
	v_mfma_f32_16x16x128_f8f6f4 v[38:41], v[2:9], v[200:207], v[38:41]
	v_mfma_f32_16x16x128_f8f6f4 v[34:37], v[10:17], v[200:207], v[34:37]
	s_setprio 0
	s_barrier
.Lmid7:
	v_add_u32_e32 v14, 0x18000, v171
	v_add_u32_e32 v30, 0x1c000, v171
	ds_read_b128 v[2:5], v14
	ds_read_b128 v[6:9], v14 offset:1024
	ds_read_b128 v[10:13], v14 offset:2048
	ds_read_b128 v[14:17], v14 offset:3072
	ds_read_b128 v[18:21], v30
	ds_read_b128 v[22:25], v30 offset:1024
	ds_read_b128 v[26:29], v30 offset:2048
	ds_read_b128 v[30:33], v30 offset:3072
	ds_read_b128 v[176:179], v172 offset:32768
	ds_read_b128 v[180:183], v172 offset:33792
	ds_read_b128 v[184:187], v172 offset:34816
	ds_read_b128 v[188:191], v172 offset:35840
	ds_read_b128 v[192:195], v172 offset:36864
	ds_read_b128 v[196:199], v172 offset:37888
	ds_read_b128 v[200:203], v172 offset:38912
	ds_read_b128 v[204:207], v172 offset:39936
	s_add_u32 s48, s48, 0x20000
	s_addc_u32 s49, s49, 0
	s_mov_b32 s33, m0
	s_mov_b32 m0, s23
	s_nop 2
	global_load_lds_dwordx4 v163, s[48:49]
	s_mov_b32 m0, s33
	s_nop 0
	s_mov_b32 s33, m0
	s_mov_b32 m0, s28
	s_nop 2
	global_load_lds_dwordx4 v164, s[48:49]
	s_mov_b32 m0, s33
	s_waitcnt vmcnt(8)
	s_waitcnt lgkmcnt(0)
	s_barrier
	s_setprio 1
	v_mfma_f32_16x16x128_f8f6f4 v[158:161], v[2:9], v[176:183], v[158:161]
	v_mfma_f32_16x16x128_f8f6f4 v[154:157], v[10:17], v[176:183], v[154:157]
	v_mfma_f32_16x16x128_f8f6f4 v[142:145], v[2:9], v[184:191], v[142:145]
	v_mfma_f32_16x16x128_f8f6f4 v[138:141], v[10:17], v[184:191], v[138:141]
	v_mfma_f32_16x16x128_f8f6f4 v[126:129], v[2:9], v[192:199], v[126:129]
	v_mfma_f32_16x16x128_f8f6f4 v[122:125], v[10:17], v[192:199], v[122:125]
	v_mfma_f32_16x16x128_f8f6f4 v[110:113], v[2:9], v[200:207], v[110:113]
	v_mfma_f32_16x16x128_f8f6f4 v[106:109], v[10:17], v[200:207], v[106:109]
	v_mfma_f32_16x16x128_f8f6f4 v[150:153], v[18:25], v[176:183], v[150:153]
	v_mfma_f32_16x16x128_f8f6f4 v[146:149], v[26:33], v[176:183], v[146:149]
	v_mfma_f32_16x16x128_f8f6f4 v[134:137], v[18:25], v[184:191], v[134:137]
	v_mfma_f32_16x16x128_f8f6f4 v[130:133], v[26:33], v[184:191], v[130:133]
	v_mfma_f32_16x16x128_f8f6f4 v[118:121], v[18:25], v[192:199], v[118:121]
	v_mfma_f32_16x16x128_f8f6f4 v[114:117], v[26:33], v[192:199], v[114:117]
	v_mfma_f32_16x16x128_f8f6f4 v[102:105], v[18:25], v[200:207], v[102:105]
	v_mfma_f32_16x16x128_f8f6f4 v[98:101], v[26:33], v[200:207], v[98:101]
	s_setprio 0
	s_barrier
	ds_read_b128 v[176:179], v172 offset:49152
	ds_read_b128 v[180:183], v172 offset:50176
	ds_read_b128 v[184:187], v172 offset:51200
	ds_read_b128 v[188:191], v172 offset:52224
	ds_read_b128 v[192:195], v172 offset:53248
	ds_read_b128 v[196:199], v172 offset:54272
	ds_read_b128 v[200:203], v172 offset:55296
	ds_read_b128 v[204:207], v172 offset:56320
	s_mov_b32 s33, m0
	s_mov_b32 m0, s67
	s_nop 2
	global_load_lds_dwordx4 v1, s[46:47]
	s_mov_b32 m0, s33
	s_add_u32 s42, s42, 0x20080
	s_mov_b32 s33, m0
	s_mov_b32 m0, s68
	s_nop 2
	global_load_lds_dwordx4 v162, s[46:47]
	s_mov_b32 m0, s33
	s_addc_u32 s43, s43, 0
	s_mov_b32 s33, m0
	s_mov_b32 m0, s77
	s_nop 2
	global_load_lds_dwordx4 v1, s[42:43]
	s_mov_b32 m0, s33
	s_nop 0
	s_mov_b32 s33, m0
	s_mov_b32 m0, s78
	s_nop 2
	global_load_lds_dwordx4 v162, s[42:43]
	s_mov_b32 m0, s33
	s_nop 0
	s_mov_b32 s33, m0
	s_mov_b32 m0, s69
	s_nop 2
	global_load_lds_dwordx4 v163, s[44:45]
	s_mov_b32 m0, s33
	s_nop 0
	s_mov_b32 s33, m0
	s_mov_b32 m0, s76
	s_nop 2
	global_load_lds_dwordx4 v164, s[44:45]
	s_mov_b32 m0, s33
	s_waitcnt vmcnt(8)
	s_waitcnt lgkmcnt(0)
	s_barrier
	s_setprio 1
	v_mfma_f32_16x16x128_f8f6f4 v[94:97], v[2:9], v[176:183], v[94:97]
	v_mfma_f32_16x16x128_f8f6f4 v[90:93], v[10:17], v[176:183], v[90:93]
	v_mfma_f32_16x16x128_f8f6f4 v[78:81], v[2:9], v[184:191], v[78:81]
	v_mfma_f32_16x16x128_f8f6f4 v[74:77], v[10:17], v[184:191], v[74:77]
	v_mfma_f32_16x16x128_f8f6f4 v[62:65], v[2:9], v[192:199], v[62:65]
	v_mfma_f32_16x16x128_f8f6f4 v[58:61], v[10:17], v[192:199], v[58:61]
	v_mfma_f32_16x16x128_f8f6f4 v[46:49], v[2:9], v[200:207], v[46:49]
	v_mfma_f32_16x16x128_f8f6f4 v[42:45], v[10:17], v[200:207], v[42:45]
	v_mfma_f32_16x16x128_f8f6f4 v[86:89], v[18:25], v[176:183], v[86:89]
	v_mfma_f32_16x16x128_f8f6f4 v[82:85], v[26:33], v[176:183], v[82:85]
	v_mfma_f32_16x16x128_f8f6f4 v[70:73], v[18:25], v[184:191], v[70:73]
	v_mfma_f32_16x16x128_f8f6f4 v[66:69], v[26:33], v[184:191], v[66:69]
	v_mfma_f32_16x16x128_f8f6f4 v[54:57], v[18:25], v[192:199], v[54:57]
	v_mfma_f32_16x16x128_f8f6f4 v[50:53], v[26:33], v[192:199], v[50:53]
	v_mfma_f32_16x16x128_f8f6f4 v[38:41], v[18:25], v[200:207], v[38:41]
	v_mfma_f32_16x16x128_f8f6f4 v[34:37], v[26:33], v[200:207], v[34:37]
	s_setprio 0
	s_cmp_lt_u32 s91, 6
	s_cbranch_scc1 .Lkb7_do
	s_cmp_lg_u64 s[12:13], 0
	s_cbranch_scc0 .Lkb7_skip

.Lpeel7:
	s_lshl_b32 s33, s91, 7
	s_add_u32 s52, s36, s33
	s_addc_u32 s53, s37, 0
	s_add_u32 s46, s52, 0x100
	s_addc_u32 s47, s53, 0
	s_and_b64 s[44:45], s[42:43], exec
	s_cselect_b32 s49, s15, s47
	s_cselect_b32 s48, s17, s46
	s_add_u32 s33, s26, s33
	v_add_u32_e32 v2, 0x10000, v171
	v_add_u32_e32 v14, 0x14000, v171
	s_addc_u32 s44, s27, 0
	ds_read_b128 v[18:21], v2
	ds_read_b128 v[22:25], v2 offset:1024
	ds_read_b128 v[26:29], v2 offset:2048
	ds_read_b128 v[30:33], v2 offset:3072
	ds_read_b128 v[2:5], v14
	ds_read_b128 v[6:9], v14 offset:1024
	ds_read_b128 v[10:13], v14 offset:2048
	ds_read_b128 v[14:17], v14 offset:3072
	s_add_u32 s33, s33, 0x100
	s_addc_u32 s44, s44, 0
	s_and_b64 s[42:43], s[42:43], exec
	s_cselect_b32 s43, s19, s44
	s_cselect_b32 s42, s18, s33
	s_add_u32 s44, s48, 0x80
	s_addc_u32 s45, s49, 0
	s_add_u32 s46, s42, 0x80
	s_addc_u32 s47, s43, 0
	ds_read_b128 v[176:179], v172
	ds_read_b128 v[180:183], v172 offset:1024
	ds_read_b128 v[184:187], v172 offset:2048
	ds_read_b128 v[188:191], v172 offset:3072
	ds_read_b128 v[192:195], v172 offset:4096
	ds_read_b128 v[196:199], v172 offset:5120
	ds_read_b128 v[200:203], v172 offset:6144
	ds_read_b128 v[204:207], v172 offset:7168
	s_add_u32 s52, s52, 0x20080
	s_addc_u32 s53, s53, 0
	s_mov_b32 s33, m0
	s_mov_b32 m0, s79
	s_nop 2
	global_load_lds_dwordx4 v163, s[52:53]
	s_mov_b32 m0, s33
	s_nop 0
	s_mov_b32 s33, m0
	s_mov_b32 m0, s80
	s_nop 2
	global_load_lds_dwordx4 v164, s[52:53]
	s_mov_b32 m0, s33
	s_waitcnt vmcnt(8)
	s_waitcnt lgkmcnt(0)
	s_barrier
	s_setprio 1
	v_mfma_f32_16x16x128_f8f6f4 v[158:161], v[18:25], v[176:183], 0
	v_mfma_f32_16x16x128_f8f6f4 v[154:157], v[26:33], v[176:183], 0
	v_mfma_f32_16x16x128_f8f6f4 v[142:145], v[18:25], v[184:191], 0
	v_mfma_f32_16x16x128_f8f6f4 v[138:141], v[26:33], v[184:191], 0
	v_mfma_f32_16x16x128_f8f6f4 v[126:129], v[18:25], v[192:199], 0
	v_mfma_f32_16x16x128_f8f6f4 v[122:125], v[26:33], v[192:199], 0
	v_mfma_f32_16x16x128_f8f6f4 v[110:113], v[18:25], v[200:207], 0
	v_mfma_f32_16x16x128_f8f6f4 v[106:109], v[26:33], v[200:207], 0
	v_mfma_f32_16x16x128_f8f6f4 v[150:153], v[2:9], v[176:183], 0
	v_mfma_f32_16x16x128_f8f6f4 v[146:149], v[10:17], v[176:183], 0
	v_mfma_f32_16x16x128_f8f6f4 v[134:137], v[2:9], v[184:191], 0
	v_mfma_f32_16x16x128_f8f6f4 v[130:133], v[10:17], v[184:191], 0
	v_mfma_f32_16x16x128_f8f6f4 v[118:121], v[2:9], v[192:199], 0
	v_mfma_f32_16x16x128_f8f6f4 v[114:117], v[10:17], v[192:199], 0
	v_mfma_f32_16x16x128_f8f6f4 v[102:105], v[2:9], v[200:207], 0
	v_mfma_f32_16x16x128_f8f6f4 v[98:101], v[10:17], v[200:207], 0
	s_setprio 0
	s_barrier
	ds_read_b128 v[176:179], v172 offset:16384
	ds_read_b128 v[180:183], v172 offset:17408
	ds_read_b128 v[184:187], v172 offset:18432
	ds_read_b128 v[188:191], v172 offset:19456
	ds_read_b128 v[192:195], v172 offset:20480
	ds_read_b128 v[196:199], v172 offset:21504
	ds_read_b128 v[200:203], v172 offset:22528
	ds_read_b128 v[204:207], v172 offset:23552
	s_mov_b32 s33, m0
	s_mov_b32 m0, s64
	s_nop 2
	global_load_lds_dwordx4 v1, s[42:43]
	s_mov_b32 m0, s33
	s_add_u32 s52, s42, 0x20000
	s_mov_b32 s33, m0
	s_mov_b32 m0, s65
	s_nop 2
	global_load_lds_dwordx4 v162, s[42:43]
	s_mov_b32 m0, s33
	s_addc_u32 s53, s43, 0
	s_mov_b32 s33, m0
	s_mov_b32 m0, s24
	s_nop 2
	global_load_lds_dwordx4 v1, s[52:53]
	s_mov_b32 m0, s33
	s_nop 0
	s_mov_b32 s33, m0
	s_mov_b32 m0, s25
	s_nop 2
	global_load_lds_dwordx4 v162, s[52:53]
	s_mov_b32 m0, s33
	s_nop 0
	s_mov_b32 s33, m0
	s_mov_b32 m0, s63
	s_nop 2
	global_load_lds_dwordx4 v163, s[48:49]
	s_mov_b32 m0, s33
	s_nop 0
	s_mov_b32 s33, m0
	s_mov_b32 m0, s2
	s_nop 2
	global_load_lds_dwordx4 v164, s[48:49]
	s_mov_b32 m0, s33
	s_waitcnt vmcnt(8)
	s_waitcnt lgkmcnt(0)
	s_barrier
	s_setprio 1
	v_mfma_f32_16x16x128_f8f6f4 v[94:97], v[18:25], v[176:183], 0
	v_mfma_f32_16x16x128_f8f6f4 v[90:93], v[26:33], v[176:183], 0
	v_mfma_f32_16x16x128_f8f6f4 v[78:81], v[18:25], v[184:191], 0
	v_mfma_f32_16x16x128_f8f6f4 v[74:77], v[26:33], v[184:191], 0
	v_mfma_f32_16x16x128_f8f6f4 v[62:65], v[18:25], v[192:199], 0
	v_mfma_f32_16x16x128_f8f6f4 v[58:61], v[26:33], v[192:199], 0
	v_mfma_f32_16x16x128_f8f6f4 v[46:49], v[18:25], v[200:207], 0
	v_mfma_f32_16x16x128_f8f6f4 v[42:45], v[26:33], v[200:207], 0
	v_mfma_f32_16x16x128_f8f6f4 v[86:89], v[2:9], v[176:183], 0
	v_mfma_f32_16x16x128_f8f6f4 v[82:85], v[10:17], v[176:183], 0
	v_mfma_f32_16x16x128_f8f6f4 v[70:73], v[2:9], v[184:191], 0
	v_mfma_f32_16x16x128_f8f6f4 v[66:69], v[10:17], v[184:191], 0
	v_mfma_f32_16x16x128_f8f6f4 v[54:57], v[2:9], v[192:199], 0
	v_mfma_f32_16x16x128_f8f6f4 v[50:53], v[10:17], v[192:199], 0
	v_mfma_f32_16x16x128_f8f6f4 v[38:41], v[2:9], v[200:207], 0
	v_mfma_f32_16x16x128_f8f6f4 v[34:37], v[10:17], v[200:207], 0
	s_setprio 0
	s_barrier
	s_branch .Lmid7

.LBB0_2128:
	v_add_u32_e32 v0, 0x10000, v169
	v_add_u32_e32 v12, 0x14000, v169
	s_add_u32 s26, s22, 0x100
	ds_read_b128 v[16:19], v0
	ds_read_b128 v[20:23], v0 offset:1024
	ds_read_b128 v[24:27], v0 offset:2048
	ds_read_b128 v[28:31], v0 offset:3072
	ds_read_b128 v[0:3], v12
	ds_read_b128 v[4:7], v12 offset:1024
	ds_read_b128 v[8:11], v12 offset:2048
	ds_read_b128 v[12:15], v12 offset:3072
	s_addc_u32 s27, s23, 0
	s_cmp_eq_u32 s83, 4
	s_cselect_b32 s42, s15, s26
	s_cselect_b32 s43, s13, s27
	s_cselect_b32 s37, s17, s82
	s_cselect_b32 s36, s16, s81
	s_add_u32 s38, s42, 0x80
	s_addc_u32 s39, s43, 0
	s_add_u32 s40, s36, 0x80
	s_addc_u32 s41, s37, 0
	ds_read_b128 v[172:175], v170
	ds_read_b128 v[176:179], v170 offset:1024
	ds_read_b128 v[180:183], v170 offset:2048
	ds_read_b128 v[184:187], v170 offset:3072
	ds_read_b128 v[188:191], v170 offset:4096
	ds_read_b128 v[192:195], v170 offset:5120
	ds_read_b128 v[196:199], v170 offset:6144
	ds_read_b128 v[200:203], v170 offset:7168
	s_add_u32 s22, s22, 0x20080
	s_addc_u32 s23, s23, 0
	s_mov_b32 s33, m0
	s_mov_b32 m0, s64
	s_nop 2
	global_load_lds_dwordx4 v162, s[22:23]
	s_mov_b32 m0, s33
	s_nop 0
	s_mov_b32 s33, m0
	s_mov_b32 m0, s65
	s_nop 2
	global_load_lds_dwordx4 v164, s[22:23]
	s_mov_b32 m0, s33
	s_waitcnt vmcnt(8)
	s_waitcnt lgkmcnt(0)
	s_barrier
	s_setprio 1
	v_mfma_f32_16x16x128_f8f6f4 v[156:159], v[16:23], v[172:179], v[156:159]
	v_mfma_f32_16x16x128_f8f6f4 v[152:155], v[24:31], v[172:179], v[152:155]
	v_mfma_f32_16x16x128_f8f6f4 v[140:143], v[16:23], v[180:187], v[140:143]
	v_mfma_f32_16x16x128_f8f6f4 v[136:139], v[24:31], v[180:187], v[136:139]
	v_mfma_f32_16x16x128_f8f6f4 v[124:127], v[16:23], v[188:195], v[124:127]
	v_mfma_f32_16x16x128_f8f6f4 v[120:123], v[24:31], v[188:195], v[120:123]
	v_mfma_f32_16x16x128_f8f6f4 v[108:111], v[16:23], v[196:203], v[108:111]
	v_mfma_f32_16x16x128_f8f6f4 v[104:107], v[24:31], v[196:203], v[104:107]
	v_mfma_f32_16x16x128_f8f6f4 v[148:151], v[0:7], v[172:179], v[148:151]
	v_mfma_f32_16x16x128_f8f6f4 v[144:147], v[8:15], v[172:179], v[144:147]
	v_mfma_f32_16x16x128_f8f6f4 v[132:135], v[0:7], v[180:187], v[132:135]
	v_mfma_f32_16x16x128_f8f6f4 v[128:131], v[8:15], v[180:187], v[128:131]
	v_mfma_f32_16x16x128_f8f6f4 v[116:119], v[0:7], v[188:195], v[116:119]
	v_mfma_f32_16x16x128_f8f6f4 v[112:115], v[8:15], v[188:195], v[112:115]
	v_mfma_f32_16x16x128_f8f6f4 v[100:103], v[0:7], v[196:203], v[100:103]
	v_mfma_f32_16x16x128_f8f6f4 v[96:99], v[8:15], v[196:203], v[96:99]
	s_setprio 0
	s_barrier
	ds_read_b128 v[172:175], v170 offset:16384
	ds_read_b128 v[176:179], v170 offset:17408
	ds_read_b128 v[180:183], v170 offset:18432
	ds_read_b128 v[184:187], v170 offset:19456
	ds_read_b128 v[188:191], v170 offset:20480
	ds_read_b128 v[192:195], v170 offset:21504
	ds_read_b128 v[196:199], v170 offset:22528
	ds_read_b128 v[200:203], v170 offset:23552
	s_mov_b32 s22, m0
	s_mov_b32 m0, s31
	s_nop 2
	global_load_lds_dwordx4 v163, s[36:37]
	s_mov_b32 m0, s22
	s_nop 0
	s_mov_b32 s22, m0
	s_mov_b32 m0, s44
	s_nop 2
	global_load_lds_dwordx4 v165, s[36:37]
	s_mov_b32 m0, s22
	s_add_u32 s22, s36, 0x20000
	s_addc_u32 s23, s37, 0
	s_mov_b32 s33, m0
	s_mov_b32 m0, s45
	s_nop 2
	global_load_lds_dwordx4 v163, s[22:23]
	s_mov_b32 m0, s33
	s_nop 0
	s_mov_b32 s33, m0
	s_mov_b32 m0, s46
	s_nop 2
	global_load_lds_dwordx4 v165, s[22:23]
	s_mov_b32 m0, s33
	s_mov_b32 s22, m0
	s_mov_b32 m0, s21
	s_nop 2
	global_load_lds_dwordx4 v162, s[42:43]
	s_mov_b32 m0, s22
	s_nop 0
	s_mov_b32 s22, m0
	s_mov_b32 m0, s47
	s_nop 2
	global_load_lds_dwordx4 v164, s[42:43]
	s_mov_b32 m0, s22
	s_waitcnt vmcnt(8)
	s_waitcnt lgkmcnt(0)
	s_barrier
	s_setprio 1
	v_mfma_f32_16x16x128_f8f6f4 v[92:95], v[16:23], v[172:179], v[92:95]
	v_mfma_f32_16x16x128_f8f6f4 v[88:91], v[24:31], v[172:179], v[88:91]
	v_mfma_f32_16x16x128_f8f6f4 v[76:79], v[16:23], v[180:187], v[76:79]
	v_mfma_f32_16x16x128_f8f6f4 v[72:75], v[24:31], v[180:187], v[72:75]
	v_mfma_f32_16x16x128_f8f6f4 v[60:63], v[16:23], v[188:195], v[60:63]
	v_mfma_f32_16x16x128_f8f6f4 v[56:59], v[24:31], v[188:195], v[56:59]
	v_mfma_f32_16x16x128_f8f6f4 v[44:47], v[16:23], v[196:203], v[44:47]
	v_mfma_f32_16x16x128_f8f6f4 v[40:43], v[24:31], v[196:203], v[40:43]
	v_mfma_f32_16x16x128_f8f6f4 v[84:87], v[0:7], v[172:179], v[84:87]
	v_mfma_f32_16x16x128_f8f6f4 v[80:83], v[8:15], v[172:179], v[80:83]
	v_mfma_f32_16x16x128_f8f6f4 v[68:71], v[0:7], v[180:187], v[68:71]
	v_mfma_f32_16x16x128_f8f6f4 v[64:67], v[8:15], v[180:187], v[64:67]
	v_mfma_f32_16x16x128_f8f6f4 v[52:55], v[0:7], v[188:195], v[52:55]
	v_mfma_f32_16x16x128_f8f6f4 v[48:51], v[8:15], v[188:195], v[48:51]
	v_mfma_f32_16x16x128_f8f6f4 v[36:39], v[0:7], v[196:203], v[36:39]
	v_mfma_f32_16x16x128_f8f6f4 v[32:35], v[8:15], v[196:203], v[32:35]
	s_setprio 0
	s_barrier
	v_add_u32_e32 v12, 0x18000, v169
	v_add_u32_e32 v28, 0x1c000, v169
	ds_read_b128 v[0:3], v12
	ds_read_b128 v[4:7], v12 offset:1024
	ds_read_b128 v[8:11], v12 offset:2048
	ds_read_b128 v[12:15], v12 offset:3072
	ds_read_b128 v[16:19], v28
	ds_read_b128 v[20:23], v28 offset:1024
	ds_read_b128 v[24:27], v28 offset:2048
	ds_read_b128 v[28:31], v28 offset:3072
	ds_read_b128 v[172:175], v170 offset:32768
	ds_read_b128 v[176:179], v170 offset:33792
	ds_read_b128 v[180:183], v170 offset:34816
	ds_read_b128 v[184:187], v170 offset:35840
	ds_read_b128 v[188:191], v170 offset:36864
	ds_read_b128 v[192:195], v170 offset:37888
	ds_read_b128 v[196:199], v170 offset:38912
	ds_read_b128 v[200:203], v170 offset:39936
	s_add_u32 s22, s42, 0x20000
	s_addc_u32 s23, s43, 0
	s_mov_b32 s33, m0
	s_mov_b32 m0, s48
	s_nop 2
	global_load_lds_dwordx4 v162, s[22:23]
	s_mov_b32 m0, s33
	s_nop 0
	s_mov_b32 s33, m0
	s_mov_b32 m0, s49
	s_nop 2
	global_load_lds_dwordx4 v164, s[22:23]
	s_mov_b32 m0, s33
	s_waitcnt vmcnt(8)
	s_waitcnt lgkmcnt(0)
	s_barrier
	s_setprio 1
	v_mfma_f32_16x16x128_f8f6f4 v[156:159], v[0:7], v[172:179], v[156:159]
	v_mfma_f32_16x16x128_f8f6f4 v[152:155], v[8:15], v[172:179], v[152:155]
	v_mfma_f32_16x16x128_f8f6f4 v[140:143], v[0:7], v[180:187], v[140:143]
	v_mfma_f32_16x16x128_f8f6f4 v[136:139], v[8:15], v[180:187], v[136:139]
	v_mfma_f32_16x16x128_f8f6f4 v[124:127], v[0:7], v[188:195], v[124:127]
	v_mfma_f32_16x16x128_f8f6f4 v[120:123], v[8:15], v[188:195], v[120:123]
	v_mfma_f32_16x16x128_f8f6f4 v[108:111], v[0:7], v[196:203], v[108:111]
	v_mfma_f32_16x16x128_f8f6f4 v[104:107], v[8:15], v[196:203], v[104:107]
	v_mfma_f32_16x16x128_f8f6f4 v[148:151], v[16:23], v[172:179], v[148:151]
	v_mfma_f32_16x16x128_f8f6f4 v[144:147], v[24:31], v[172:179], v[144:147]
	v_mfma_f32_16x16x128_f8f6f4 v[132:135], v[16:23], v[180:187], v[132:135]
	v_mfma_f32_16x16x128_f8f6f4 v[128:131], v[24:31], v[180:187], v[128:131]
	v_mfma_f32_16x16x128_f8f6f4 v[116:119], v[16:23], v[188:195], v[116:119]
	v_mfma_f32_16x16x128_f8f6f4 v[112:115], v[24:31], v[188:195], v[112:115]
	v_mfma_f32_16x16x128_f8f6f4 v[100:103], v[16:23], v[196:203], v[100:103]
	v_mfma_f32_16x16x128_f8f6f4 v[96:99], v[24:31], v[196:203], v[96:99]
	s_setprio 0
	s_barrier
	ds_read_b128 v[172:175], v170 offset:49152
	ds_read_b128 v[176:179], v170 offset:50176
	ds_read_b128 v[180:183], v170 offset:51200
	ds_read_b128 v[184:187], v170 offset:52224
	ds_read_b128 v[188:191], v170 offset:53248
	ds_read_b128 v[192:195], v170 offset:54272
	ds_read_b128 v[196:199], v170 offset:55296
	ds_read_b128 v[200:203], v170 offset:56320
	s_mov_b32 s22, m0
	s_mov_b32 m0, s58
	s_nop 2
	global_load_lds_dwordx4 v163, s[40:41]
	s_mov_b32 m0, s22
	s_nop 0
	s_mov_b32 s22, m0
	s_mov_b32 m0, s59
	s_nop 2
	global_load_lds_dwordx4 v165, s[40:41]
	s_mov_b32 m0, s22
	s_add_u32 s22, s36, 0x20080
	s_addc_u32 s23, s37, 0
	s_mov_b32 s33, m0
	s_mov_b32 m0, s62
	s_nop 2
	global_load_lds_dwordx4 v163, s[22:23]
	s_mov_b32 m0, s33
	s_nop 0
	s_mov_b32 s33, m0
	s_mov_b32 m0, s63
	s_nop 2
	global_load_lds_dwordx4 v165, s[22:23]
	s_mov_b32 m0, s33
	s_mov_b32 s22, m0
	s_mov_b32 m0, s60
	s_nop 2
	global_load_lds_dwordx4 v162, s[38:39]
	s_mov_b32 m0, s22
	s_nop 0
	s_mov_b32 s22, m0
	s_mov_b32 m0, s61
	s_nop 2
	global_load_lds_dwordx4 v164, s[38:39]
	s_mov_b32 m0, s22
	s_waitcnt vmcnt(8)
	s_waitcnt lgkmcnt(0)
	s_barrier
	s_setprio 1
	v_mfma_f32_16x16x128_f8f6f4 v[92:95], v[0:7], v[172:179], v[92:95]
	v_mfma_f32_16x16x128_f8f6f4 v[88:91], v[8:15], v[172:179], v[88:91]
	v_mfma_f32_16x16x128_f8f6f4 v[76:79], v[0:7], v[180:187], v[76:79]
	v_mfma_f32_16x16x128_f8f6f4 v[72:75], v[8:15], v[180:187], v[72:75]
	v_mfma_f32_16x16x128_f8f6f4 v[60:63], v[0:7], v[188:195], v[60:63]
	v_mfma_f32_16x16x128_f8f6f4 v[56:59], v[8:15], v[188:195], v[56:59]
	v_mfma_f32_16x16x128_f8f6f4 v[44:47], v[0:7], v[196:203], v[44:47]
	v_mfma_f32_16x16x128_f8f6f4 v[40:43], v[8:15], v[196:203], v[40:43]
	v_mfma_f32_16x16x128_f8f6f4 v[84:87], v[16:23], v[172:179], v[84:87]
	v_mfma_f32_16x16x128_f8f6f4 v[80:83], v[24:31], v[172:179], v[80:83]
	v_mfma_f32_16x16x128_f8f6f4 v[68:71], v[16:23], v[180:187], v[68:71]
	v_mfma_f32_16x16x128_f8f6f4 v[64:67], v[24:31], v[180:187], v[64:67]
	v_mfma_f32_16x16x128_f8f6f4 v[52:55], v[16:23], v[188:195], v[52:55]
	v_mfma_f32_16x16x128_f8f6f4 v[48:51], v[24:31], v[188:195], v[48:51]
	v_mfma_f32_16x16x128_f8f6f4 v[36:39], v[16:23], v[196:203], v[36:39]
	v_mfma_f32_16x16x128_f8f6f4 v[32:35], v[24:31], v[196:203], v[32:35]
	s_setprio 0
	s_barrier
	s_add_i32 s83, s83, 2
	s_add_u32 s81, s81, 0x100
	s_addc_u32 s82, s82, 0
	s_cmp_gt_u32 s83, 5
	s_cbranch_scc1 .LBB0_2130
	s_mov_b64 s[22:23], s[26:27]
	s_cmp_lg_u32 s83, -2
	s_cbranch_scc0 .LBB0_2121
	s_branch .LBB0_2128
